# hand-written rank sort in k_bucket (64-bit pair compare), deeper cvt pipelining in k_bucket, coalesced h1 stores via LDS, icache warm chains
# speedup vs baseline: 1.0631x; 1.0199x over previous
_Z7k_frontPKiS0_PiS1_PjPKfS4_S4_P15HIP_vector_typeIjLj4EES7_PKS5_IfLj4EES7_S7_:
	s_load_dword s36, s[0:1], 0x0
	s_load_dword s37, s[0:1], 0x40
	v_lshrrev_b32_e32 v1, 6, v0
	s_nop 0
	v_readfirstlane_b32 s35, v1
	s_movk_i32 s34, 0x5aa5
	s_mov_b64 exec, 0
	s_cmpk_lt_u32 s35, 8
	s_cbranch_scc1 .Lw0s0d0_16
	s_cmpk_lt_u32 s35, 12
	s_cbranch_scc1 .Lw0s0d8_16
	s_cmpk_lt_u32 s35, 14
	s_cbranch_scc1 .Lw0s0d12_16
	s_cmpk_lt_u32 s35, 15
	s_cbranch_scc1 .Lw0s0d14_16
	s_branch .Lw0t15

.Lw0b0:
	s_load_dwordx2 s[4:5], s[0:1], 0x58
	s_cmpk_gt_u32 s2, 0xce
	s_mov_b64 s[6:7], -1
	s_cbranch_scc0 .LBB0_5
.Lw0t1:
	s_cbranch_execz .Lw0c1
.Lw0b1:
	s_branch .Lmy_cvt0
.LBB0_4:
	s_or_b64 exec, exec, s[6:7]
	s_mov_b64 s[6:7], 0
.LBB0_5:
	s_andn2_b64 vcc, exec, s[6:7]
	s_cbranch_vccnz .LBB0_38
	s_add_i32 s3, s2, 0xffffff3c
	v_lshl_or_b32 v2, s3, 10, v0
	s_cmp_gt_u32 s3, 7
	s_mov_b64 s[6:7], -1
	s_cbranch_scc0 .LBB0_30
	s_load_dwordx2 s[6:7], s[0:1], 0x48

.Lw0b2:
	s_cmp_gt_u32 s3, 9
	s_mov_b64 s[8:9], -1
	s_cbranch_scc0 .LBB0_27
	s_movk_i32 s8, 0x2900
	v_cmp_gt_u32_e32 vcc, s8, v2
	s_and_saveexec_b64 s[8:9], vcc
	s_cbranch_execz .LBB0_26
	s_load_dwordx2 s[10:11], s[0:1], 0x38
	v_add_u32_e32 v1, 0xffffd800, v2
	v_lshlrev_b32_e32 v4, 1, v0
	v_lshrrev_b32_e32 v1, 3, v1
	v_and_b32_e32 v4, 0x60, v4

.Lw0b3:
	v_and_b32_e32 v1, 0x1ffffff8, v1
	v_and_b32_e32 v3, 15, v0
	v_add_u32_e32 v4, v1, v4
	v_cmp_gt_u32_e32 vcc, 2, v3
	v_mov_b32_e32 v1, 0
	v_lshl_or_b32 v4, v4, 1, v3
	v_mov_b32_e32 v3, 0
	s_and_saveexec_b64 s[12:13], vcc
	s_cbranch_execz .LBB0_11
	v_mov_b32_e32 v5, 0
	s_waitcnt lgkmcnt(0)
	v_lshl_add_u64 v[6:7], v[4:5], 2, s[10:11]

.Lw0b4:
	global_load_dword v3, v[6:7], off
	s_waitcnt vmcnt(0)
	v_cvt_f16_f32_e32 v3, v3
.LBB0_11:
	s_or_b64 exec, exec, s[12:13]
	s_and_saveexec_b64 s[12:13], vcc
	s_cbranch_execz .LBB0_13
	v_mov_b32_e32 v5, 0
	s_waitcnt lgkmcnt(0)
	v_lshl_add_u64 v[6:7], v[4:5], 2, s[10:11]
	global_load_dword v1, v[6:7], off offset:8
	s_waitcnt vmcnt(0)

.Lw0b5:
	v_cvt_f16_f32_e32 v1, v1

.Lw0b6:
	s_and_saveexec_b64 s[12:13], vcc
	s_cbranch_execz .LBB0_17
	v_mov_b32_e32 v5, 0
	s_waitcnt lgkmcnt(0)
	v_lshl_add_u64 v[8:9], v[4:5], 2, s[10:11]
	global_load_dword v5, v[8:9], off offset:24
	s_waitcnt vmcnt(0)
	v_cvt_f16_f32_e32 v6, v5
.LBB0_17:
	s_or_b64 exec, exec, s[12:13]
	v_mov_b32_e32 v8, 0
	v_mov_b32_e32 v9, 0
	s_and_saveexec_b64 s[12:13], vcc
	s_cbranch_execz .LBB0_19
.Lw0t7:
	s_cbranch_execz .Lw0c7
.Lw0b7:
	v_mov_b32_e32 v5, 0
	s_waitcnt lgkmcnt(0)
	v_lshl_add_u64 v[10:11], v[4:5], 2, s[10:11]
	global_load_dword v5, v[10:11], off offset:32
	s_waitcnt vmcnt(0)
	v_cvt_f16_f32_e32 v9, v5
.LBB0_19:
	s_or_b64 exec, exec, s[12:13]
	s_and_saveexec_b64 s[12:13], vcc
	s_cbranch_execz .LBB0_21
	v_mov_b32_e32 v5, 0
	s_waitcnt lgkmcnt(0)
	v_lshl_add_u64 v[10:11], v[4:5], 2, s[10:11]

.Lw0b8:
	global_load_dword v5, v[10:11], off offset:40
	s_waitcnt vmcnt(0)
	v_cvt_f16_f32_e32 v8, v5
.LBB0_21:
	s_or_b64 exec, exec, s[12:13]
	v_mov_b32_e32 v10, 0
	v_mov_b32_e32 v11, 0
	s_and_saveexec_b64 s[12:13], vcc
	s_cbranch_execz .LBB0_23
	v_mov_b32_e32 v5, 0
	s_waitcnt lgkmcnt(0)
	v_lshl_add_u64 v[12:13], v[4:5], 2, s[10:11]
	global_load_dword v5, v[12:13], off offset:48

.Lw0b9:
	s_waitcnt vmcnt(0)
	v_cvt_f16_f32_e32 v11, v5

.LBB0_25:
	s_or_b64 exec, exec, s[12:13]
	s_waitcnt lgkmcnt(0)
.Lw0t10:
	s_cbranch_execz .Lw0c10
.Lw0b10:
	s_mov_b32 s10, 0x5040100
	v_perm_b32 v11, v10, v11, s10
	v_perm_b32 v10, v8, v9, s10
	v_perm_b32 v8, v1, v3, s10
	v_mov_b32_e32 v3, 0
	v_lshl_add_u64 v[4:5], v[2:3], 4, s[6:7]
	v_add_co_u32_e32 v4, vcc, 0xfffe0000, v4
	v_perm_b32 v9, v6, v7, s10

.Lw0b11:
	s_nop 0
	v_addc_co_u32_e32 v5, vcc, -1, v5, vcc
	global_store_dwordx4 v[4:5], v[8:11], off

.LBB0_27:
	s_andn2_b64 vcc, exec, s[8:9]
	s_cbranch_vccnz .LBB0_29
	s_load_dwordx2 s[8:9], s[0:1], 0x30
	v_lshlrev_b32_e32 v1, 3, v0
	v_lshrrev_b32_e32 v3, 4, v0
	v_add_u32_e32 v8, 0xffffe000, v2
	v_and_b32_e32 v1, 0x60, v1

.Lw0b12:
	v_and_b32_e32 v3, 28, v3
	v_and_b32_e32 v4, 3, v0
	v_or3_b32 v1, v3, v4, v1
	v_lshlrev_b32_e32 v3, 1, v0
	v_lshrrev_b32_e32 v4, 6, v8
	v_and_b32_e32 v3, 0x60, v3
	v_and_b32_e32 v4, 0x3fffff8, v4
	v_add_u32_e32 v4, v4, v3
	v_lshlrev_b32_e32 v6, 2, v1
	v_mov_b32_e32 v7, 0
	s_waitcnt lgkmcnt(0)

.Lw0b13:
	v_lshl_add_u64 v[10:11], s[8:9], 0, v[6:7]
	v_or_b32_e32 v6, 1, v4
	v_lshlrev_b64 v[14:15], 9, v[6:7]
	v_or_b32_e32 v6, 2, v4
	v_lshlrev_b64 v[16:17], 9, v[6:7]
	v_or_b32_e32 v6, 3, v4
	v_lshlrev_b64 v[18:19], 9, v[6:7]
	v_or_b32_e32 v6, 4, v4
	v_lshlrev_b64 v[20:21], 9, v[6:7]
	v_or_b32_e32 v6, 5, v4

.Lw0b14:
	v_mov_b32_e32 v5, v7
	v_lshlrev_b64 v[22:23], 9, v[6:7]
	v_or_b32_e32 v6, 6, v4
	v_lshlrev_b64 v[12:13], 9, v[4:5]
	v_lshlrev_b64 v[24:25], 9, v[6:7]
	v_or_b32_e32 v6, 7, v4
	v_lshl_add_u64 v[12:13], v[10:11], 0, v[12:13]
	v_lshlrev_b64 v[4:5], 9, v[6:7]
	v_lshl_add_u64 v[14:15], v[10:11], 0, v[14:15]

.Lw0b15:
	v_lshl_add_u64 v[16:17], v[10:11], 0, v[16:17]
	v_lshl_add_u64 v[18:19], v[10:11], 0, v[18:19]
	v_lshl_add_u64 v[20:21], v[10:11], 0, v[20:21]
	v_lshl_add_u64 v[22:23], v[10:11], 0, v[22:23]
	v_lshl_add_u64 v[24:25], v[10:11], 0, v[24:25]
	v_lshl_add_u64 v[4:5], v[10:11], 0, v[4:5]
	global_load_dword v1, v[12:13], off
	global_load_dword v3, v[14:15], off

.Lw0b16:
	global_load_dword v6, v[16:17], off
	global_load_dword v10, v[18:19], off
	global_load_dword v11, v[20:21], off
	global_load_dword v26, v[22:23], off
	global_load_dword v27, v[24:25], off
	global_load_dword v28, v[4:5], off
	v_mov_b32_e32 v9, v7
	v_lshl_add_u64 v[8:9], v[8:9], 4, s[6:7]

.Lw0b17:
	s_waitcnt vmcnt(6)
	v_cvt_pk_f16_f32 v4, v1, v3
	s_waitcnt vmcnt(4)
	v_cvt_pk_f16_f32 v5, v6, v10
	s_waitcnt vmcnt(2)
	v_cvt_pk_f16_f32 v6, v11, v26
	s_waitcnt vmcnt(0)
	v_cvt_pk_f16_f32 v7, v27, v28
	global_store_dwordx4 v[8:9], v[4:7], off
.LBB0_29:
.Lw0t18:
	s_cbranch_execz .Lw0c18
.Lw0b18:
	s_waitcnt lgkmcnt(0)
	s_mov_b64 s[6:7], 0
.LBB0_30:
	s_andn2_b64 vcc, exec, s[6:7]
	s_cbranch_vccnz .LBB0_32
	s_load_dwordx2 s[6:7], s[0:1], 0x28
	v_lshlrev_b32_e32 v1, 3, v0
	v_lshrrev_b32_e32 v3, 4, v2
	v_and_b32_e32 v1, 0x60, v1
	v_and_b32_e32 v4, 28, v3
	v_and_b32_e32 v5, 3, v0
	v_lshrrev_b32_e32 v6, 1, v0
	v_and_b32_e32 v6, 24, v6
	s_movk_i32 s8, 0x1e0

.Lw0b19:
	v_or3_b32 v1, v1, v5, v4
	v_and_or_b32 v3, v3, s8, v6
	v_lshlrev_b32_e32 v1, 2, v1
	v_lshl_or_b32 v1, v3, 9, v1
	s_waitcnt lgkmcnt(0)
	global_load_dword v4, v1, s[6:7] offset:1024
	global_load_dword v5, v1, s[6:7] offset:1536
	global_load_dword v6, v1, s[6:7] offset:2048
	global_load_dword v7, v1, s[6:7] offset:3072

.Lw0b20:
	global_load_dword v8, v1, s[6:7] offset:3584
	global_load_dword v9, v1, s[6:7] offset:2560
	global_load_dword v10, v1, s[6:7]
	global_load_dword v11, v1, s[6:7] offset:512
	s_load_dwordx2 s[6:7], s[0:1], 0x40
	v_mov_b32_e32 v3, 0
	s_waitcnt lgkmcnt(0)
	v_lshl_add_u64 v[2:3], v[2:3], 4, s[6:7]

.Lw0b21:
	s_waitcnt vmcnt(6)
	v_cvt_pk_f16_f32 v5, v4, v5
	s_waitcnt vmcnt(3)
	v_cvt_pk_f16_f32 v7, v7, v8
	s_waitcnt vmcnt(2)
	v_cvt_pk_f16_f32 v6, v6, v9
	s_waitcnt vmcnt(0)
	v_cvt_pk_f16_f32 v4, v10, v11
	global_store_dwordx4 v[2:3], v[4:7], off
.LBB0_32:
	s_cmp_eq_u32 s3, 0
	s_cselect_b64 s[6:7], -1, 0
.Lw0t22:
	s_cbranch_execz .Lw0c22
.Lw0b22:
	v_cmp_gt_u32_e32 vcc, 32, v0
	s_and_b64 s[8:9], s[6:7], vcc
	s_and_saveexec_b64 s[6:7], s[8:9]
	s_cbranch_execz .LBB0_37
	v_cmp_lt_u32_e32 vcc, 15, v0
	v_mov_b32_e32 v3, 0
	v_lshlrev_b32_e32 v2, 4, v0
	s_and_saveexec_b64 s[8:9], vcc
	s_xor_b64 s[8:9], exec, s[8:9]
	s_cbranch_execz .LBB0_35
	s_load_dwordx2 s[10:11], s[0:1], 0x60
	s_waitcnt lgkmcnt(0)
	v_lshl_add_u64 v[4:5], s[10:11], 0, v[2:3]

.Lw0b23:
	v_add_co_u32_e32 v6, vcc, 0x1869000, v4
	v_mov_b32_e32 v2, v3
	s_nop 0
	v_addc_co_u32_e32 v7, vcc, 0, v5, vcc
	v_mov_b32_e32 v4, v3
	v_mov_b32_e32 v5, v3
	global_store_dwordx4 v[6:7], v[2:5], off offset:3840
.LBB0_35:
	s_andn2_saveexec_b64 s[8:9], s[8:9]
	s_cbranch_execz .LBB0_37
	v_mov_b32_e32 v3, 0
	s_waitcnt lgkmcnt(0)
	v_lshl_add_u64 v[4:5], s[4:5], 0, v[2:3]
.Lw0t24:
	s_cbranch_execz .Lw0c24
.Lw0b24:
	v_add_co_u32_e32 v6, vcc, 0x186a000, v4
	v_mov_b32_e32 v2, v3
	s_nop 0
	v_addc_co_u32_e32 v7, vcc, 0, v5, vcc
	v_mov_b32_e32 v4, v3
	v_mov_b32_e32 v5, v3
	global_store_dwordx4 v[6:7], v[2:5], off

.LBB0_39:
	s_andn2_b64 vcc, exec, s[4:5]
	s_cbranch_vccnz .LBB0_121
.Lw0t25:
	s_cbranch_execz .Lw0c25
.Lw0b25:
	s_mul_hi_i32 s3, s2, 0x5397829d
	s_load_dwordx4 s[4:7], s[0:1], 0x0
	s_lshr_b32 s8, s3, 31
	s_ashr_i32 s21, s3, 5
	s_add_i32 s21, s21, s8
	s_mul_i32 s3, s21, 0x62
	s_sub_i32 s25, s2, s3
	s_addk_i32 s2, 0x61
	s_cmpk_lt_u32 s2, 0xc3
	s_waitcnt lgkmcnt(0)
	s_cselect_b32 s16, s4, s6
	s_cselect_b32 s17, s5, s7

.Lw0b26:
	s_add_u32 s18, s16, 0x30d400
	s_addc_u32 s19, s17, 0
	s_lshl_b32 s20, s25, 13
	s_min_i32 s24, s20, 0xc1500
	s_addk_i32 s24, 0x2000
	v_or_b32_e32 v2, s20, v0
	v_cmp_gt_i32_e32 vcc, s24, v2
	v_mov_b32_e32 v1, -1
	v_ashrrev_i32_e32 v3, 31, v2
	v_mov_b32_e32 v21, -1
	s_and_saveexec_b64 s[2:3], vcc
	s_cbranch_execz .LBB0_42
	v_lshl_add_u64 v[4:5], v[2:3], 2, s[18:19]

.Lw0b27:
	global_load_dword v21, v[4:5], off nt

.Lw0b29:
	v_or_b32_e32 v8, 0xc00, v2
	v_cmp_gt_i32_e64 s[6:7], s24, v8
	v_ashrrev_i32_e32 v9, 31, v8
	s_and_saveexec_b64 s[8:9], s[6:7]
	s_cbranch_execz .LBB0_48
	v_lshl_add_u64 v[10:11], v[8:9], 2, s[18:19]
	global_load_dword v18, v[10:11], off nt
.LBB0_48:
	s_or_b64 exec, exec, s[8:9]
	v_or_b32_e32 v10, 0x1000, v2
	v_cmp_gt_i32_e64 s[8:9], s24, v10
.Lw0t30:
	s_cbranch_execz .Lw0c30
.Lw0b30:
	v_mov_b32_e32 v19, -1
	v_ashrrev_i32_e32 v11, 31, v10
	v_mov_b32_e32 v23, -1
	s_and_saveexec_b64 s[10:11], s[8:9]
	s_cbranch_execz .LBB0_50
	v_lshl_add_u64 v[12:13], v[10:11], 2, s[18:19]
	global_load_dword v23, v[12:13], off nt
.LBB0_50:
	s_or_b64 exec, exec, s[10:11]
	v_or_b32_e32 v12, 0x1400, v2
	v_cmp_gt_i32_e64 s[10:11], s24, v12
.Lw0t31:
	s_cbranch_execz .Lw0c31
.Lw0b31:
	v_ashrrev_i32_e32 v13, 31, v12
	s_and_saveexec_b64 s[12:13], s[10:11]
	s_cbranch_execz .LBB0_52
	v_lshl_add_u64 v[14:15], v[12:13], 2, s[18:19]
	global_load_dword v19, v[14:15], off nt
.LBB0_52:
	s_or_b64 exec, exec, s[12:13]
	v_or_b32_e32 v14, 0x1800, v2
	v_cmp_gt_i32_e64 s[12:13], s24, v14
	v_mov_b32_e32 v20, -1
	v_ashrrev_i32_e32 v15, 31, v14
	v_mov_b32_e32 v24, -1

.Lw0b32:
	s_and_saveexec_b64 s[14:15], s[12:13]
	s_cbranch_execz .LBB0_54
	v_lshl_add_u64 v[16:17], v[14:15], 2, s[18:19]
	global_load_dword v24, v[16:17], off nt
.LBB0_54:
	s_or_b64 exec, exec, s[14:15]
	v_or_b32_e32 v16, 0x1c00, v2
	v_cmp_gt_i32_e64 s[14:15], s24, v16
	v_ashrrev_i32_e32 v17, 31, v16
	s_and_saveexec_b64 s[22:23], s[14:15]
	s_cbranch_execz .LBB0_56
	v_lshl_add_u64 v[26:27], v[16:17], 2, s[18:19]

.Lw0b33:
	global_load_dword v20, v[26:27], off nt

.LBB0_58:
	s_or_b64 exec, exec, s[18:19]
	s_and_saveexec_b64 s[18:19], s[2:3]
	s_cbranch_execz .LBB0_60
.Lw0t34:
	s_cbranch_execz .Lw0c34
.Lw0b34:
	v_lshl_add_u64 v[2:3], v[4:5], 2, s[16:17]
	global_load_dword v25, v[2:3], off nt

.LBB0_62:
	s_or_b64 exec, exec, s[2:3]
	s_and_saveexec_b64 s[2:3], s[6:7]
.Lw0t35:
	s_cbranch_execz .Lw0c35
.Lw0b35:
	s_cbranch_execz .LBB0_64
	v_lshl_add_u64 v[2:3], v[8:9], 2, s[16:17]
	global_load_dword v5, v[2:3], off nt

.Lw0b36:
	s_and_saveexec_b64 s[2:3], s[10:11]
	s_cbranch_execz .LBB0_68
	v_lshl_add_u64 v[2:3], v[12:13], 2, s[16:17]
	global_load_dword v4, v[2:3], off nt

.LBB0_70:
.Lw0t37:
	s_cbranch_execz .Lw0c37
.Lw0b37:
	s_or_b64 exec, exec, s[2:3]
	s_and_saveexec_b64 s[2:3], s[14:15]
	s_cbranch_execz .LBB0_72
	v_lshl_add_u64 v[2:3], v[16:17], 2, s[16:17]
	global_load_dword v3, v[2:3], off nt
.LBB0_72:
	s_or_b64 exec, exec, s[2:3]
	s_movk_i32 s2, 0xc4
	v_cmp_gt_u32_e64 s[16:17], s2, v0
	v_lshlrev_b32_e32 v2, 2, v0
	s_and_saveexec_b64 s[2:3], s[16:17]
	v_mov_b32_e32 v8, 0
	ds_write_b32 v2, v8 offset:33552

.Lw0b38:
	s_or_b64 exec, exec, s[2:3]
	s_waitcnt lgkmcnt(0)
	s_waitcnt vmcnt(0)
	v_cmp_lt_i32_e32 vcc, -1, v21
	v_mov_b32_e32 v8, 0
	v_lshrrev_b32_e32 v14, 7, v21
	v_mov_b32_e32 v12, 0
	s_barrier
	s_and_saveexec_b64 s[2:3], vcc
	v_and_b32_e32 v9, 0x1fffffc, v14
	v_mov_b32_e32 v10, 1
	ds_add_rtn_u32 v12, v9, v10 offset:33552

.Lw0b39:
	s_or_b64 exec, exec, s[2:3]
	v_cmp_lt_i32_e64 s[2:3], -1, v1
	v_lshrrev_b32_e32 v13, 7, v1
	s_and_saveexec_b64 s[4:5], s[2:3]
	v_and_b32_e32 v8, 0x1fffffc, v13
	v_mov_b32_e32 v9, 1
	ds_add_rtn_u32 v8, v8, v9 offset:33552
	s_or_b64 exec, exec, s[4:5]
	v_cmp_lt_i32_e64 s[4:5], -1, v22
	v_mov_b32_e32 v9, 0
	v_lshrrev_b32_e32 v17, 7, v22

.Lw0b40:
	v_mov_b32_e32 v15, 0
	s_and_saveexec_b64 s[6:7], s[4:5]
	v_and_b32_e32 v10, 0x1fffffc, v17
	v_mov_b32_e32 v11, 1
	ds_add_rtn_u32 v15, v10, v11 offset:33552
	s_or_b64 exec, exec, s[6:7]
	v_cmp_lt_i32_e64 s[6:7], -1, v18
	v_lshrrev_b32_e32 v16, 7, v18
	s_and_saveexec_b64 s[8:9], s[6:7]
	v_and_b32_e32 v9, 0x1fffffc, v16
	v_mov_b32_e32 v10, 1

.Lw0b41:
	ds_add_rtn_u32 v9, v9, v10 offset:33552
	s_or_b64 exec, exec, s[8:9]
	v_cmp_lt_i32_e64 s[8:9], -1, v23
	v_mov_b32_e32 v10, 0
	v_lshrrev_b32_e32 v33, 7, v23
	v_mov_b32_e32 v28, 0
	s_and_saveexec_b64 s[10:11], s[8:9]
	v_and_b32_e32 v11, 0x1fffffc, v33
	v_mov_b32_e32 v28, 1
	ds_add_rtn_u32 v28, v11, v28 offset:33552
	s_or_b64 exec, exec, s[10:11]

.Lw0b42:
	v_cmp_lt_i32_e64 s[12:13], -1, v19
	v_lshrrev_b32_e32 v32, 7, v19
	s_and_saveexec_b64 s[10:11], s[12:13]
	v_and_b32_e32 v10, 0x1fffffc, v32
	v_mov_b32_e32 v11, 1
	ds_add_rtn_u32 v10, v10, v11 offset:33552
	s_or_b64 exec, exec, s[10:11]
	v_cmp_lt_i32_e64 s[10:11], -1, v24
	v_mov_b32_e32 v11, 0
	v_lshrrev_b32_e32 v31, 7, v24
	v_mov_b32_e32 v29, 0

.Lw0b43:
	s_and_saveexec_b64 s[14:15], s[10:11]
	v_and_b32_e32 v29, 0x1fffffc, v31
	v_mov_b32_e32 v30, 1
	ds_add_rtn_u32 v29, v29, v30 offset:33552
	s_or_b64 exec, exec, s[14:15]
	v_cmp_lt_i32_e64 s[14:15], -1, v20
	v_lshrrev_b32_e32 v30, 7, v20
	s_and_saveexec_b64 s[18:19], s[14:15]
	v_and_b32_e32 v11, 0x1fffffc, v30
	v_mov_b32_e32 v34, 1
	ds_add_rtn_u32 v11, v11, v34 offset:33552

.Lw0b44:
	s_or_b64 exec, exec, s[18:19]
	v_mov_b32_e32 v34, 0
	s_waitcnt lgkmcnt(0)
	s_barrier
	s_and_saveexec_b64 s[18:19], s[16:17]
	ds_read_b32 v34, v2 offset:33552
	s_or_b64 exec, exec, s[18:19]
	s_waitcnt lgkmcnt(0)
	v_add_u32_dpp v35, v34, v34 row_shr:1 row_mask:0xf bank_mask:0xf bound_ctrl:1
	v_and_b32_e32 v36, 63, v0
	v_cmp_eq_u32_e64 s[18:19], 63, v36

.Lw0b45:
	v_add_u32_dpp v35, v35, v35 row_shr:2 row_mask:0xf bank_mask:0xf bound_ctrl:1
	s_nop 1
	v_add_u32_dpp v35, v35, v35 row_shr:4 row_mask:0xf bank_mask:0xf bound_ctrl:1
	s_nop 1
	v_add_u32_dpp v35, v35, v35 row_shr:8 row_mask:0xf bank_mask:0xf bound_ctrl:1
	s_nop 1
	v_add_u32_dpp v35, v35, v35 row_bcast:15 row_mask:0xa bank_mask:0xf
	s_nop 1
	v_add_u32_dpp v35, v35, v35 row_bcast:31 row_mask:0xc bank_mask:0xf
	s_and_saveexec_b64 s[22:23], s[18:19]

.Lw0b46:
	v_lshrrev_b32_e32 v36, 4, v0
	v_and_b32_e32 v36, 60, v36
	ds_write_b32 v36, v35 offset:34336
	s_or_b64 exec, exec, s[22:23]
	s_waitcnt lgkmcnt(0)
	s_barrier
	s_and_saveexec_b64 s[18:19], s[16:17]
	s_cbranch_execz .LBB0_96
	v_mov_b32_e32 v36, 0
	ds_read_b96 v[36:38], v36 offset:34336
	s_movk_i32 s16, 0xbf
	s_movk_i32 s22, 0x7f
	v_cmp_lt_u32_e64 s[16:17], s16, v0

.Lw0b47:
	v_sub_u32_e32 v35, v35, v34
	s_load_dwordx4 s[28:31], s[0:1], 0x10
	s_waitcnt lgkmcnt(0)
	v_cndmask_b32_e64 v38, 0, v38, s[16:17]
	v_cmp_lt_u32_e64 s[16:17], s22, v0
	s_nop 1
	v_cndmask_b32_e64 v37, 0, v37, s[16:17]
	v_cmp_lt_u32_e64 s[16:17], 63, v0
	s_nop 1

.Lw0b48:
	v_cndmask_b32_e64 v36, 0, v36, s[16:17]
	v_add_u32_e32 v36, v37, v36
	s_mul_i32 s16, s21, 0xc4
	v_add3_u32 v40, v38, v36, v35
	v_add_u32_e32 v35, s16, v0
	s_movk_i32 s16, 0x62
	v_mul_lo_u32 v35, v35, s16
	v_add_u32_e32 v36, s25, v35
	v_ashrrev_i32_e32 v37, 31, v36
	v_lshlrev_b64 v[36:37], 2, v[36:37]

.Lw0b49:
	v_lshl_add_u64 v[38:39], s[28:29], 0, v[36:37]
	global_store_dword v[38:39], v34, off
	v_lshl_add_u64 v[34:35], s[30:31], 0, v[36:37]
	ds_write_b32 v2, v40 offset:32768
	global_store_dword v[34:35], v40, off
.LBB0_96:
	s_or_b64 exec, exec, s[18:19]
	s_waitcnt lgkmcnt(0)
	s_barrier
	s_and_saveexec_b64 s[16:17], vcc
	s_cbranch_execnz .LBB0_122
.Lw0t50:
	s_cbranch_execz .Lw0c50
.Lw0b50:
	s_or_b64 exec, exec, s[16:17]
	s_and_saveexec_b64 s[16:17], s[2:3]
	s_cbranch_execnz .LBB0_123

.LBB0_101:
	s_or_b64 exec, exec, s[2:3]
	s_and_saveexec_b64 s[2:3], s[12:13]
	s_cbranch_execnz .LBB0_127
.LBB0_102:
.Lw0t51:
	s_cbranch_execz .Lw0c51
.Lw0b51:
	s_or_b64 exec, exec, s[2:3]
	s_load_dwordx2 s[0:1], s[0:1], 0x20
	s_and_saveexec_b64 s[2:3], s[10:11]
	s_cbranch_execnz .LBB0_128

.LBB0_104:
	v_and_b32_e32 v1, 0x1fffffc, v30
	ds_read_b32 v1, v1 offset:32768
	v_lshlrev_b32_e32 v4, 17, v20
	s_mov_b32 s4, 0x3fe0000

.Lw0b52:
	v_and_or_b32 v3, v4, s4, v3
	v_lshlrev_b32_e32 v4, 2, v11
	s_waitcnt lgkmcnt(0)
	v_lshl_add_u32 v1, v1, 2, v4
	ds_write_b32 v1, v3
.LBB0_105:
	s_or_b64 exec, exec, s[2:3]
	s_mul_hi_i32 s2, s21, 0x30d400
	s_mul_i32 s21, s21, 0x30d400
	s_waitcnt lgkmcnt(0)
	s_add_u32 s3, s0, s21
	s_addc_u32 s2, s1, s2

.Lw0b53:
	s_ashr_i32 s21, s20, 31
	s_lshl_b64 s[0:1], s[20:21], 2
	s_add_u32 s0, s3, s0
	s_addc_u32 s1, s2, s1
	s_sub_i32 s4, s24, s20
	v_cmp_gt_i32_e32 vcc, s4, v0
	s_barrier
	s_and_saveexec_b64 s[2:3], vcc
	s_cbranch_execz .LBB0_107
	ds_read_b32 v1, v2
	s_waitcnt lgkmcnt(0)
	global_store_dword v2, v1, s[0:1]

.LBB0_109:
	s_or_b64 exec, exec, s[2:3]
	v_or_b32_e32 v1, 0x800, v0
.Lw0t55:
	s_cbranch_execz .Lw0c55
.Lw0b55:
	v_cmp_gt_i32_e32 vcc, s4, v1
	s_and_saveexec_b64 s[2:3], vcc
	s_cbranch_execz .LBB0_111
	ds_read_b32 v3, v2 offset:8192
	v_lshlrev_b32_e32 v1, 2, v1
	s_waitcnt lgkmcnt(0)
	global_store_dword v1, v3, s[0:1]
.LBB0_111:
	s_or_b64 exec, exec, s[2:3]
	v_or_b32_e32 v1, 0xc00, v0
	v_cmp_gt_i32_e32 vcc, s4, v1
	s_and_saveexec_b64 s[2:3], vcc
	s_cbranch_execz .LBB0_113
.Lw0t56:
	s_cbranch_execz .Lw0c56
.Lw0b56:
	ds_read_b32 v3, v2 offset:12288
	v_lshlrev_b32_e32 v1, 2, v1
	s_waitcnt lgkmcnt(0)
	global_store_dword v1, v3, s[0:1]
.LBB0_113:
	s_or_b64 exec, exec, s[2:3]
	v_or_b32_e32 v1, 0x1000, v0
	v_cmp_gt_i32_e32 vcc, s4, v1
	s_and_saveexec_b64 s[2:3], vcc
	s_cbranch_execz .LBB0_115
	ds_read_b32 v3, v2 offset:16384
	v_lshlrev_b32_e32 v1, 2, v1

.LBB0_119:
	s_or_b64 exec, exec, s[2:3]
	v_or_b32_e32 v0, 0x1c00, v0
.Lw0t59:
	s_cbranch_execz .Lw0c59
.Lw0b59:
	v_cmp_gt_i32_e32 vcc, s4, v0
	s_and_saveexec_b64 s[2:3], vcc
	s_cbranch_execz .LBB0_121
	ds_read_b32 v1, v2 offset:28672
	v_lshlrev_b32_e32 v0, 2, v0
	s_waitcnt lgkmcnt(0)
	global_store_dword v0, v1, s[0:1]

.LBB0_122:
	v_and_b32_e32 v14, 0x1fffffc, v14
	ds_read_b32 v14, v14 offset:32768
	v_lshlrev_b32_e32 v21, 17, v21
.Lw0t60:
	s_cbranch_execz .Lw0c60
.Lw0b60:
	s_mov_b32 s18, 0x3fe0000
	v_lshlrev_b32_e32 v12, 2, v12
	v_and_or_b32 v21, v21, s18, v27
	s_waitcnt lgkmcnt(0)
	v_lshl_add_u32 v12, v14, 2, v12
	ds_write_b32 v12, v21
	s_or_b64 exec, exec, s[16:17]
	s_and_saveexec_b64 s[16:17], s[2:3]
	s_cbranch_execz .LBB0_98
.LBB0_123:
	v_and_b32_e32 v12, 0x1fffffc, v13
.Lw0t61:
	s_cbranch_execz .Lw0c61
.Lw0b61:
	ds_read_b32 v12, v12 offset:32768
	v_lshlrev_b32_e32 v1, 17, v1
	s_mov_b32 s2, 0x3fe0000
	v_lshlrev_b32_e32 v8, 2, v8
	v_and_or_b32 v1, v1, s2, v25
	s_waitcnt lgkmcnt(0)
	v_lshl_add_u32 v8, v12, 2, v8
	ds_write_b32 v8, v1
	s_or_b64 exec, exec, s[16:17]
	s_and_saveexec_b64 s[2:3], s[4:5]

.LBB0_124:
	v_and_b32_e32 v1, 0x1fffffc, v17
	ds_read_b32 v1, v1 offset:32768
	v_lshlrev_b32_e32 v8, 17, v22
	s_mov_b32 s4, 0x3fe0000
	v_lshlrev_b32_e32 v12, 2, v15
	v_and_or_b32 v8, v8, s4, v26
	s_waitcnt lgkmcnt(0)
	v_lshl_add_u32 v1, v1, 2, v12
	ds_write_b32 v1, v8
.Lw0t63:
	s_cbranch_execz .Lw0c63
.Lw0b63:
	s_or_b64 exec, exec, s[2:3]
	s_and_saveexec_b64 s[2:3], s[6:7]
	s_cbranch_execz .LBB0_100
.LBB0_125:
	v_and_b32_e32 v1, 0x1fffffc, v16
	ds_read_b32 v1, v1 offset:32768
	v_lshlrev_b32_e32 v8, 17, v18
	s_mov_b32 s4, 0x3fe0000
	v_and_or_b32 v5, v8, s4, v5
	v_lshlrev_b32_e32 v8, 2, v9
	s_waitcnt lgkmcnt(0)

.Lw0b64:
	v_lshl_add_u32 v1, v1, 2, v8
	ds_write_b32 v1, v5
	s_or_b64 exec, exec, s[2:3]
	s_and_saveexec_b64 s[2:3], s[8:9]
	s_cbranch_execz .LBB0_101
.LBB0_126:
	v_and_b32_e32 v1, 0x1fffffc, v33
	ds_read_b32 v1, v1 offset:32768
	v_lshlrev_b32_e32 v5, 17, v23
	s_mov_b32 s4, 0x3fe0000
	v_and_or_b32 v5, v5, s4, v7

.Lw0b65:
	v_lshlrev_b32_e32 v7, 2, v28
	s_waitcnt lgkmcnt(0)
	v_lshl_add_u32 v1, v1, 2, v7
	ds_write_b32 v1, v5
	s_or_b64 exec, exec, s[2:3]
	s_and_saveexec_b64 s[2:3], s[12:13]
	s_cbranch_execz .LBB0_102
.LBB0_127:
	v_and_b32_e32 v1, 0x1fffffc, v32
	ds_read_b32 v1, v1 offset:32768
	v_lshlrev_b32_e32 v5, 17, v19
.Lw0t66:
	s_cbranch_execz .Lw0c66
.Lw0b66:
	s_mov_b32 s4, 0x3fe0000
	v_and_or_b32 v4, v5, s4, v4
	v_lshlrev_b32_e32 v5, 2, v10
	s_waitcnt lgkmcnt(0)
	v_lshl_add_u32 v1, v1, 2, v5
	ds_write_b32 v1, v4
	s_or_b64 exec, exec, s[2:3]
	s_load_dwordx2 s[0:1], s[0:1], 0x20
	s_and_saveexec_b64 s[2:3], s[10:11]
	s_cbranch_execz .LBB0_103

.Lw0b67:
	v_and_b32_e32 v1, 0x1fffffc, v31
	ds_read_b32 v1, v1 offset:32768
	v_lshlrev_b32_e32 v4, 17, v24
	s_mov_b32 s4, 0x3fe0000
	v_lshlrev_b32_e32 v5, 2, v29
	v_and_or_b32 v4, v4, s4, v6
	s_waitcnt lgkmcnt(0)
	v_lshl_add_u32 v1, v1, 2, v5
	ds_write_b32 v1, v4

.Lw0b68:
	s_or_b64 exec, exec, s[2:3]
	s_and_saveexec_b64 s[2:3], s[14:15]
	s_cbranch_execnz .LBB0_104
	s_branch .LBB0_105
.Lmy_cvt0:
	s_waitcnt lgkmcnt(0)
	s_load_dwordx4 s[20:23], s[0:1], 0x50
	s_sub_i32 s3, s2, 207
	v_and_b32_e32 v1, 0x3c0, v0
	v_and_b32_e32 v2, 63, v0
	v_lshlrev_b32_e32 v3, 5, v1
	v_lshl_or_b32 v3, v2, 4, v3

.Lw0b69:
	v_and_b32_e32 v4, 1, v0
	v_lshrrev_b32_e32 v5, 1, v2
	v_lshl_or_b32 v5, v4, 5, v5
	v_add_u32_e32 v5, v5, v1
	v_lshlrev_b32_e32 v5, 4, v5
	v_cmp_eq_u32_e32 vcc, 0, v4
	s_waitcnt lgkmcnt(0)
	s_add_i32 s8, s3, 0
	s_lshl_b32 s9, s8, 10
	s_sub_i32 s9, 0x1869c0, s9
	v_cmp_ge_i32_e64 s[24:25], s9, v1
	s_add_i32 s8, s3, 0

.Lw0b70:
	s_lshl_b32 s9, s8, 15
	s_add_u32 s10, s20, s9
	s_addc_u32 s11, s21, 0
	s_mov_b64 exec, s[24:25]
	global_load_dwordx4 v[8:11], v3, s[10:11] nt
	global_load_dwordx4 v[12:15], v3, s[10:11] offset:1024 nt
	s_waitcnt vmcnt(0)
	s_add_i32 s8, s3, 0
	s_lshl_b32 s9, s8, 14
	s_add_u32 s10, s22, s9
	s_addc_u32 s11, s23, 0
	s_mov_b64 exec, s[24:25]
	v_cvt_pk_f16_f32 v8, v8, v9

.Lw0b71:
	v_cvt_pk_f16_f32 v9, v10, v11
	v_cvt_pk_f16_f32 v10, v12, v13
	v_cvt_pk_f16_f32 v11, v14, v15
	v_cndmask_b32_e32 v12, v8, v10, vcc
	v_cndmask_b32_e32 v13, v9, v11, vcc
	s_nop 1
	v_mov_b32_dpp v12, v12 quad_perm:[1,0,3,2] row_mask:0xf bank_mask:0xf bound_ctrl:1
	v_mov_b32_dpp v13, v13 quad_perm:[1,0,3,2] row_mask:0xf bank_mask:0xf bound_ctrl:1
	v_cndmask_b32_e32 v8, v12, v8, vcc

.Lw0b72:
	v_cndmask_b32_e32 v9, v13, v9, vcc
	v_cndmask_b32_e32 v10, v10, v12, vcc
	v_cndmask_b32_e32 v11, v11, v13, vcc
	global_store_dwordx4 v5, v[8:11], s[10:11] sc1
.Lmy_cvt0_end:
	s_endpgm
.Lw0c0:
	s_cmpk_eq_u32 s34, 0x5aa5
	s_cbranch_scc1 .Lw0t16
	s_branch .Lw0b0

	.amdhsa_kernel _Z7k_frontPKiS0_PiS1_PjPKfS4_S4_P15HIP_vector_typeIjLj4EES7_PKS5_IfLj4EES7_S7_
		.amdhsa_group_segment_fixed_size 34400
		.amdhsa_private_segment_fixed_size 0
		.amdhsa_kernarg_size 104
		.amdhsa_user_sgpr_count 2
		.amdhsa_user_sgpr_dispatch_ptr 0
		.amdhsa_user_sgpr_queue_ptr 0
		.amdhsa_user_sgpr_kernarg_segment_ptr 1
		.amdhsa_user_sgpr_dispatch_id 0
		.amdhsa_user_sgpr_kernarg_preload_length 0
		.amdhsa_user_sgpr_kernarg_preload_offset 0
		.amdhsa_user_sgpr_private_segment_size 0
		.amdhsa_uses_dynamic_stack 0
		.amdhsa_enable_private_segment 0
		.amdhsa_system_sgpr_workgroup_id_x 1
		.amdhsa_system_sgpr_workgroup_id_y 0
		.amdhsa_system_sgpr_workgroup_id_z 0
		.amdhsa_system_sgpr_workgroup_info 0
		.amdhsa_system_vgpr_workitem_id 0
		.amdhsa_next_free_vgpr 41
		.amdhsa_next_free_sgpr 38
		.amdhsa_accum_offset 44
		.amdhsa_reserve_vcc 1
		.amdhsa_float_round_mode_32 0
		.amdhsa_float_round_mode_16_64 0
		.amdhsa_float_denorm_mode_32 3
		.amdhsa_float_denorm_mode_16_64 3
		.amdhsa_dx10_clamp 1
		.amdhsa_ieee_mode 1
		.amdhsa_fp16_overflow 0
		.amdhsa_tg_split 0
		.amdhsa_exception_fp_ieee_invalid_op 0
		.amdhsa_exception_fp_denorm_src 0
		.amdhsa_exception_fp_ieee_div_zero 0
		.amdhsa_exception_fp_ieee_overflow 0
		.amdhsa_exception_fp_ieee_underflow 0
		.amdhsa_exception_fp_ieee_inexact 0
		.amdhsa_exception_int_div_zero 0
	.end_amdhsa_kernel

_Z8k_bucketPKiS0_PKjPiS3_PK15HIP_vector_typeIfLj4EEPS4_IjLj4EE:
	s_load_dword s66, s[0:1], 0x0
	s_load_dword s67, s[0:1], 0x40
	v_lshrrev_b32_e32 v1, 6, v0
	s_nop 0
	v_readfirstlane_b32 s65, v1
	s_cmpk_ge_u32 s2, 683
	s_cbranch_scc1 .Lmy_cvt1_end
	s_movk_i32 s64, 0x5aa5
	s_mov_b64 exec, 0
	s_cmpk_lt_u32 s65, 8
	s_cbranch_scc1 .Lw1s0d0_16
	s_cmpk_lt_u32 s65, 12
	s_cbranch_scc1 .Lw1s0d8_16
	s_cmpk_lt_u32 s65, 14
	s_cbranch_scc1 .Lw1s0d12_16
	s_cmpk_lt_u32 s65, 15
	s_cbranch_scc1 .Lw1s0d14_16
	s_branch .Lw1t15

.Lw1b0:
	v_mov_b32_e32 v1, 0xc4
.Lw1t1:
	s_cbranch_execz .Lw1c1
.Lw1b1:
	v_sub_co_u32_e32 v1, vcc, s2, v1
	s_and_b64 s[4:5], vcc, exec
	v_readfirstlane_b32 s3, v1
	s_cselect_b32 s33, s2, s3
	s_cmpk_gt_u32 s2, 0xc3
	s_cselect_b64 s[30:31], -1, 0
	s_and_b64 s[4:5], s[30:31], exec
	s_cselect_b32 s3, 0xc4, 0
	s_add_i32 s3, s3, s33
	s_movk_i32 s6, 0x62
	s_mul_hi_u32 s5, s3, 0x62
	s_mul_i32 s4, s3, 0x62

.Lw1b2:
	v_cmp_gt_u32_e32 vcc, s6, v0
	v_mov_b32_e32 v1, 0
	v_mov_b32_e32 v2, 0
	s_and_saveexec_b64 s[6:7], vcc
	s_cbranch_execz .LBB1_3
	s_load_dwordx2 s[8:9], s[0:1], 0x0
	s_lshl_b64 s[10:11], s[4:5], 2
	v_lshlrev_b32_e32 v2, 2, v0
	s_waitcnt lgkmcnt(0)
	s_add_u32 s8, s8, s10
	s_addc_u32 s9, s9, s11
	global_load_dword v2, v2, s[8:9]

.Lw1b3:
	s_or_b64 exec, exec, s[6:7]
	v_mov_b32_e32 v3, 0
	s_and_saveexec_b64 s[6:7], vcc
	s_cbranch_execz .LBB1_5
	s_load_dwordx2 s[8:9], s[0:1], 0x8
	s_lshl_b64 s[4:5], s[4:5], 2
	v_lshlrev_b32_e32 v4, 2, v0
	s_waitcnt lgkmcnt(0)
	s_add_u32 s4, s8, s4
	s_addc_u32 s5, s9, s5
	global_load_dword v3, v4, s[4:5]
	v_add_u32_e32 v4, 0x11990, v4

.Lw1b4:
	s_waitcnt vmcnt(0)
	ds_write_b32 v4, v3
.LBB1_5:
	s_or_b64 exec, exec, s[6:7]
	v_add_u32_dpp v3, v3, v3 row_shr:1 row_mask:0xf bank_mask:0xf bound_ctrl:1
	v_and_b32_e32 v5, 63, v0
	v_cmp_eq_u32_e64 s[4:5], 63, v5
	v_add_u32_dpp v3, v3, v3 row_shr:2 row_mask:0xf bank_mask:0xf bound_ctrl:1
	s_nop 1
	v_add_u32_dpp v3, v3, v3 row_shr:4 row_mask:0xf bank_mask:0xf bound_ctrl:1
	s_nop 1

.Lw1b5:
	v_add_u32_dpp v4, v3, v3 row_shr:8 row_mask:0xf bank_mask:0xf bound_ctrl:1
	s_waitcnt vmcnt(0)
	v_add_u32_dpp v3, v2, v2 row_shr:1 row_mask:0xf bank_mask:0xf bound_ctrl:1
	v_add_u32_dpp v4, v4, v4 row_bcast:15 row_mask:0xa bank_mask:0xf
	s_nop 0
	v_add_u32_dpp v3, v3, v3 row_shr:2 row_mask:0xf bank_mask:0xf bound_ctrl:1
	v_mov_b32_dpp v1, v4 row_bcast:31 row_mask:0xc bank_mask:0xf
	s_nop 0
	v_add_u32_dpp v3, v3, v3 row_shr:4 row_mask:0xf bank_mask:0xf bound_ctrl:1

.Lw1b6:
	s_nop 1
	v_add_u32_dpp v3, v3, v3 row_shr:8 row_mask:0xf bank_mask:0xf bound_ctrl:1
	s_nop 1
	v_add_u32_dpp v3, v3, v3 row_bcast:15 row_mask:0xa bank_mask:0xf
	s_nop 1
	v_add_u32_dpp v3, v3, v3 row_bcast:31 row_mask:0xc bank_mask:0xf
	s_and_saveexec_b64 s[6:7], s[4:5]
	s_cbranch_execz .LBB1_7
	v_lshrrev_b32_e32 v5, 4, v0
	v_and_b32_e32 v5, 60, v5
	v_add_u32_e32 v6, 0x11b20, v5

.Lw1b7:
	v_add_u32_e32 v5, 0x11b60, v5
	v_add_u32_e32 v1, v4, v1
	ds_write_b32 v5, v3
	ds_write_b32 v6, v1
.LBB1_7:
	s_or_b64 exec, exec, s[6:7]
	s_movk_i32 s3, 0x200
	v_cmp_gt_u32_e64 s[22:23], s3, v0
	s_and_saveexec_b64 s[6:7], s[22:23]
	s_cbranch_execz .LBB1_9
	v_lshlrev_b32_e32 v1, 2, v0
	v_add_u32_e32 v4, 0x10800, v1
.Lw1t8:
	s_cbranch_execz .Lw1c8
.Lw1b8:
	v_or_b32_e32 v1, 0x10000, v1
	v_mov_b32_e32 v5, 0
	ds_write_b32 v1, v5
	ds_write_b32 v4, v5
.LBB1_9:
	s_or_b64 exec, exec, s[6:7]
	v_mov_b32_e32 v1, 0x11b20
	s_waitcnt lgkmcnt(0)
	s_barrier
	ds_read_b128 v[4:7], v1
.Lw1t9:
	s_cbranch_execz .Lw1c9
.Lw1b9:
	v_mov_b32_e32 v1, 0x11b30
	ds_read_b128 v[8:11], v1
	v_mov_b32_e32 v1, 0x11b40
	s_movk_i32 s3, 0x7f
	s_waitcnt lgkmcnt(1)
	v_readfirstlane_b32 s40, v4
	v_readfirstlane_b32 s41, v5
	v_readfirstlane_b32 s42, v6
	v_readfirstlane_b32 s43, v7
	ds_read_b128 v[4:7], v1
	v_mov_b32_e32 v1, 0x11b50

.Lw1b10:
	s_waitcnt lgkmcnt(1)
	v_readfirstlane_b32 s44, v8
	v_readfirstlane_b32 s45, v9
	v_readfirstlane_b32 s46, v10
	v_readfirstlane_b32 s47, v11
	ds_read_b128 v[8:11], v1
	v_mov_b32_e32 v1, 0x11b60
	s_waitcnt lgkmcnt(1)
	v_readfirstlane_b32 s48, v4
	v_readfirstlane_b32 s49, v5
	v_readfirstlane_b32 s50, v6
	v_readfirstlane_b32 s51, v7

.Lw1b11:
	s_waitcnt lgkmcnt(0)
	v_readfirstlane_b32 s52, v8
	ds_read_b128 v[4:7], v1
	v_mov_b32_e32 v8, 0x11b70
	v_readfirstlane_b32 s53, v9
	v_readfirstlane_b32 s54, v10
	v_readfirstlane_b32 s55, v11
	ds_read_b128 v[8:11], v8
	v_cmp_lt_u32_e64 s[8:9], s3, v0
	s_movk_i32 s3, 0xbf
	v_cmp_lt_u32_e64 s[10:11], s3, v0

.Lw1b12:
	s_movk_i32 s3, 0xff
	v_cmp_lt_u32_e64 s[12:13], s3, v0
	s_movk_i32 s3, 0x13f
	v_cmp_gt_u32_e64 s[6:7], 64, v0
	v_cmp_lt_u32_e64 s[14:15], s3, v0
	s_movk_i32 s3, 0x17f
	s_waitcnt lgkmcnt(1)
	v_cndmask_b32_e64 v4, v4, 0, s[6:7]
	v_cndmask_b32_e64 v5, 0, v5, s[8:9]

.Lw1b13:
	v_cndmask_b32_e64 v6, 0, v6, s[10:11]
	v_cmp_lt_u32_e64 s[16:17], s3, v0
	s_movk_i32 s3, 0x1bf
	v_add3_u32 v4, v5, v4, v6
	v_cndmask_b32_e64 v5, 0, v7, s[12:13]
	s_waitcnt lgkmcnt(0)
	v_cndmask_b32_e64 v6, 0, v8, s[14:15]
	v_cmp_lt_u32_e64 s[18:19], s3, v0
	v_add3_u32 v4, v5, v4, v6

.Lw1b14:
	v_cndmask_b32_e64 v5, 0, v9, s[16:17]
	v_cndmask_b32_e64 v6, 0, v10, s[18:19]
	v_add3_u32 v12, v5, v4, v6
	v_mov_b32_e32 v4, 0x11b80
	ds_read_b128 v[4:7], v4
	s_movk_i32 s3, 0x1ff
	v_cmp_lt_u32_e64 s[20:21], s3, v0
	s_movk_i32 s3, 0x23f

.Lw1b15:
	v_mov_b32_e32 v8, 0x11b90
	v_cndmask_b32_e64 v11, 0, v11, s[20:21]
	ds_read_b96 v[8:10], v8
	v_cmp_lt_u32_e64 s[20:21], s3, v0
	s_movk_i32 s3, 0x27f
	s_load_dwordx2 s[24:25], s[0:1], 0x10
	s_waitcnt lgkmcnt(0)
	v_cndmask_b32_e64 v4, 0, v4, s[20:21]
	v_cmp_lt_u32_e64 s[20:21], s3, v0

.Lw1b16:
	s_movk_i32 s3, 0x2bf
	v_add3_u32 v4, v11, v12, v4
	v_cndmask_b32_e64 v5, 0, v5, s[20:21]
	v_cmp_lt_u32_e64 s[20:21], s3, v0
	s_movk_i32 s3, 0x2ff
	v_lshrrev_b32_e32 v1, 6, v0
	v_cndmask_b32_e64 v6, 0, v6, s[20:21]
	v_cmp_lt_u32_e64 s[20:21], s3, v0
	s_movk_i32 s3, 0x33f

.Lw1b17:
	v_add3_u32 v4, v5, v4, v6
	v_cndmask_b32_e64 v5, 0, v7, s[20:21]
	v_cmp_lt_u32_e64 s[20:21], s3, v0
	s_movk_i32 s3, 0x37f
	s_nop 0
	v_cndmask_b32_e64 v6, 0, v8, s[20:21]
	v_cmp_lt_u32_e64 s[20:21], s3, v0
	v_add3_u32 v4, v5, v4, v6
	s_nop 0

.Lw1b18:
	v_cndmask_b32_e64 v5, 0, v9, s[20:21]
	v_cmp_eq_u32_e64 s[20:21], 15, v1
	s_nop 1
	v_cndmask_b32_e64 v6, 0, v10, s[20:21]
	v_add3_u32 v4, v5, v4, v6
	s_and_saveexec_b64 s[26:27], vcc
	v_mov_b32_e32 v5, 0x11800
	v_sub_u32_e32 v2, v3, v2
	v_lshl_add_u32 v5, v0, 2, v5

.Lw1b19:
	v_add_u32_e32 v2, v2, v4
	ds_write_b32 v5, v2
	s_or_b64 exec, exec, s[26:27]
	s_movk_i32 s3, 0x61
	v_cmp_eq_u32_e32 vcc, s3, v0
	s_and_saveexec_b64 s[26:27], vcc
	v_add_u32_e32 v2, v4, v3
	v_mov_b32_e32 v3, 0x11988
	ds_write_b32 v3, v2
	s_or_b64 exec, exec, s[26:27]
	v_mov_b32_e32 v2, 0x11988

.Lw1b20:
	s_waitcnt lgkmcnt(0)
	s_barrier
	ds_read_b32 v2, v2
	v_mov_b32_e32 v3, 0x11900
	s_and_b64 s[26:27], s[30:31], exec
	ds_read_b32 v5, v3
	s_cselect_b32 s26, 0xc3500, 0
	s_lshl_b32 s56, s26, 2
	s_add_u32 s28, s24, s56
	s_movk_i32 s24, 0x2001
	s_waitcnt lgkmcnt(1)
	v_cmp_gt_i32_e32 vcc, s24, v2
	v_readfirstlane_b32 s3, v2
	s_addc_u32 s29, s25, 0

.Lw1b21:
	s_mov_b64 s[34:35], -1
	s_cbranch_vccnz .LBB1_37
	s_mov_b64 s[24:25], 0
	v_mov_b32_e32 v3, 0x11880
	s_movk_i32 s36, 0x51
	s_movk_i32 s37, 0x52
	s_movk_i32 s38, 0x59
	s_movk_i32 s39, 0x5a
	s_movk_i32 s57, 0x5d
	s_movk_i32 s58, 0x5e
	s_movk_i32 s59, 0x5f

.Lw1b22:
	s_movk_i32 s60, 0x60
	s_movk_i32 s61, 0x61
	v_mov_b32_e32 v4, 0x11990
	v_mov_b32_e32 v6, 1
	v_mov_b32_e32 v7, 0x11840
	v_mov_b32_e32 v8, 0x11820
	v_mov_b32_e32 v9, 0x11810
	v_mov_b32_e32 v10, 0x11808
	v_mov_b32_e32 v11, 0x11804

.Lw1b23:
	v_mov_b32_e32 v12, 0x11800
	v_mov_b32_e32 v13, v0
	s_branch .LBB1_16
.LBB1_15:
	s_or_b64 exec, exec, s[34:35]
	v_lshl_add_u32 v14, v16, 2, v4
	ds_read_b32 v14, v14
	s_waitcnt lgkmcnt(0)
	v_lshl_add_u32 v14, v16, 13, v14
	v_sub_u32_e32 v14, v14, v15
	v_add_u32_e32 v14, v13, v14
	v_ashrrev_i32_e32 v15, 31, v14

.Lw1b24:
	v_lshl_add_u64 v[14:15], v[14:15], 2, s[28:29]
	global_load_dword v14, v[14:15], off
	v_add_u32_e32 v13, 0x400, v13
	v_cmp_le_i32_e32 vcc, s3, v13
	s_or_b64 s[24:25], vcc, s[24:25]
	s_waitcnt vmcnt(0)
	v_lshrrev_b32_e32 v14, 15, v14
	v_and_b32_e32 v14, 0x1fffc, v14
	v_add_u32_e32 v14, 0x10000, v14
	ds_add_u32 v14, v6

.Lw1b25:
	s_andn2_b64 exec, exec, s[24:25]
	s_cbranch_execz .LBB1_36
.LBB1_16:
	s_waitcnt lgkmcnt(0)
	v_cmp_gt_i32_e32 vcc, v5, v13
	s_nop 1
	v_cndmask_b32_e64 v14, 64, 0, vcc
	v_lshl_or_b32 v15, v14, 2, v3
	ds_read_b32 v15, v15
	v_or_b32_e32 v16, 32, v14
	s_waitcnt lgkmcnt(0)
	v_cmp_gt_i32_e32 vcc, v15, v13

.Lw1b26:
	s_nop 1
	v_cndmask_b32_e32 v15, v16, v14, vcc
	v_cmp_lt_u32_e64 s[26:27], s36, v15
	v_cmp_gt_u32_e32 vcc, s37, v15
	s_and_saveexec_b64 s[34:35], vcc
	s_cbranch_execz .LBB1_18
	v_lshl_add_u32 v14, v15, 2, v7
	ds_read_b32 v16, v14
	s_andn2_b64 s[26:27], s[26:27], exec
	v_or_b32_e32 v14, 16, v15
	s_waitcnt lgkmcnt(0)
	v_cmp_gt_i32_e32 vcc, v16, v13

.Lw1b27:
	s_and_b64 s[62:63], vcc, exec
	s_or_b64 s[26:27], s[26:27], s[62:63]
.LBB1_18:
	s_or_b64 exec, exec, s[34:35]
	s_and_saveexec_b64 s[34:35], s[26:27]
	v_mov_b32_e32 v14, v15
	s_or_b64 exec, exec, s[34:35]
	v_cmp_lt_u32_e64 s[26:27], s38, v14
	v_cmp_gt_u32_e32 vcc, s39, v14
	s_and_saveexec_b64 s[34:35], vcc
	s_cbranch_execz .LBB1_22
	v_lshl_add_u32 v15, v14, 2, v8
	ds_read_b32 v16, v15

.Lw1b28:
	s_andn2_b64 s[26:27], s[26:27], exec
	v_add_u32_e32 v15, 8, v14
	s_waitcnt lgkmcnt(0)
	v_cmp_gt_i32_e32 vcc, v16, v13
	s_and_b64 s[62:63], vcc, exec
	s_or_b64 s[26:27], s[26:27], s[62:63]
.LBB1_22:
	s_or_b64 exec, exec, s[34:35]
	s_and_saveexec_b64 s[34:35], s[26:27]
	v_mov_b32_e32 v15, v14
	s_or_b64 exec, exec, s[34:35]
	v_cmp_lt_u32_e64 s[26:27], s57, v15
	v_cmp_gt_u32_e32 vcc, s58, v15
	s_and_saveexec_b64 s[34:35], vcc
	s_cbranch_execz .LBB1_26
.Lw1t29:
	s_cbranch_execz .Lw1c29
.Lw1b29:
	v_lshl_add_u32 v14, v15, 2, v9
	ds_read_b32 v14, v14
	s_andn2_b64 s[26:27], s[26:27], exec
	v_add_u32_e32 v16, 4, v15
	s_waitcnt lgkmcnt(0)
	v_cmp_gt_i32_e32 vcc, v14, v13
	s_and_b64 s[62:63], vcc, exec
	s_or_b64 s[26:27], s[26:27], s[62:63]
.LBB1_26:
	s_or_b64 exec, exec, s[34:35]
	s_and_saveexec_b64 s[34:35], s[26:27]
	v_mov_b32_e32 v16, v15
	s_or_b64 exec, exec, s[34:35]
	v_cmp_lt_u32_e64 s[26:27], s59, v16
.Lw1t30:
	s_cbranch_execz .Lw1c30
.Lw1b30:
	v_cmp_gt_u32_e32 vcc, s60, v16
	s_and_saveexec_b64 s[34:35], vcc
	s_cbranch_execz .LBB1_30
	v_lshl_add_u32 v14, v16, 2, v10
	ds_read_b32 v15, v14
	s_andn2_b64 s[26:27], s[26:27], exec
	v_add_u32_e32 v14, 2, v16
	s_waitcnt lgkmcnt(0)
	v_cmp_gt_i32_e32 vcc, v15, v13
	s_and_b64 s[62:63], vcc, exec
	s_or_b64 s[26:27], s[26:27], s[62:63]
.LBB1_30:
	s_or_b64 exec, exec, s[34:35]
.Lw1t31:
	s_cbranch_execz .Lw1c31
.Lw1b31:
	s_and_saveexec_b64 s[34:35], s[26:27]
	v_mov_b32_e32 v14, v16
	s_or_b64 exec, exec, s[34:35]
	v_cmp_lt_u32_e64 s[26:27], s60, v14
	v_cmp_gt_u32_e32 vcc, s61, v14
	s_and_saveexec_b64 s[34:35], vcc
	s_cbranch_execz .LBB1_34
	v_lshl_add_u32 v15, v14, 2, v11
	ds_read_b32 v15, v15
	s_andn2_b64 s[26:27], s[26:27], exec
	v_add_u32_e32 v16, 1, v14
	s_waitcnt lgkmcnt(0)

.Lw1b32:
	v_cmp_gt_i32_e32 vcc, v15, v13
	s_and_b64 s[62:63], vcc, exec
	s_or_b64 s[26:27], s[26:27], s[62:63]

.LBB1_37:
	s_load_dwordx4 s[24:27], s[0:1], 0x18
.Lw1t33:
	s_cbranch_execz .Lw1c33
.Lw1b33:
	s_movk_i32 s57, 0x2000
	s_and_b64 vcc, exec, s[34:35]
	s_cbranch_vccz .LBB1_231
	v_cmp_gt_i32_e32 vcc, s3, v0
	v_mov_b32_e32 v3, -1
	s_and_saveexec_b64 s[34:35], vcc
	s_cbranch_execz .LBB1_60
	s_waitcnt lgkmcnt(0)
	v_cmp_gt_i32_e32 vcc, v5, v0
	v_mov_b32_e32 v4, 0x11880
	s_movk_i32 s36, 0x51
	v_cndmask_b32_e64 v3, 64, 0, vcc

.Lw1b34:
	v_lshl_or_b32 v4, v3, 2, v4
	ds_read_b32 v4, v4
	v_or_b32_e32 v6, 32, v3
	s_movk_i32 s38, 0x52
	s_waitcnt lgkmcnt(0)
	v_cmp_gt_i32_e32 vcc, v4, v0
	s_nop 1
	v_cndmask_b32_e32 v4, v6, v3, vcc
	v_cmp_lt_u32_e64 s[36:37], s36, v4
	v_cmp_gt_u32_e32 vcc, s38, v4
	s_and_saveexec_b64 s[38:39], vcc
	s_cbranch_execz .LBB1_41

.Lw1b35:
	v_mov_b32_e32 v3, 0x11840
	v_lshl_add_u32 v3, v4, 2, v3
	ds_read_b32 v6, v3
	s_andn2_b64 s[36:37], s[36:37], exec
	v_or_b32_e32 v3, 16, v4
	s_waitcnt lgkmcnt(0)
	v_cmp_gt_i32_e32 vcc, v6, v0
	s_and_b64 s[58:59], vcc, exec
	s_or_b64 s[36:37], s[36:37], s[58:59]
.LBB1_41:
	s_or_b64 exec, exec, s[38:39]
	s_and_saveexec_b64 s[38:39], s[36:37]
	v_mov_b32_e32 v3, v4
.Lw1t36:
	s_cbranch_execz .Lw1c36
.Lw1b36:
	s_or_b64 exec, exec, s[38:39]
	s_movk_i32 s36, 0x59
	s_movk_i32 s38, 0x5a
	v_cmp_lt_u32_e64 s[36:37], s36, v3
	v_cmp_gt_u32_e32 vcc, s38, v3
	s_and_saveexec_b64 s[38:39], vcc
	s_cbranch_execz .LBB1_45
	v_mov_b32_e32 v4, 0x11820
	v_lshl_add_u32 v4, v3, 2, v4
	ds_read_b32 v6, v4
	s_andn2_b64 s[36:37], s[36:37], exec

.Lw1b37:
	v_add_u32_e32 v4, 8, v3
	s_waitcnt lgkmcnt(0)
	v_cmp_gt_i32_e32 vcc, v6, v0
	s_and_b64 s[58:59], vcc, exec
	s_or_b64 s[36:37], s[36:37], s[58:59]
.LBB1_45:
	s_or_b64 exec, exec, s[38:39]
	s_and_saveexec_b64 s[38:39], s[36:37]
	v_mov_b32_e32 v4, v3
	s_or_b64 exec, exec, s[38:39]
	s_movk_i32 s36, 0x5d
	s_movk_i32 s38, 0x5e
	v_cmp_lt_u32_e64 s[36:37], s36, v4
	v_cmp_gt_u32_e32 vcc, s38, v4
	s_and_saveexec_b64 s[38:39], vcc

.Lw1b38:
	s_cbranch_execz .LBB1_49
	v_mov_b32_e32 v3, 0x11810
	v_lshl_add_u32 v3, v4, 2, v3
	ds_read_b32 v3, v3
	s_andn2_b64 s[36:37], s[36:37], exec
	v_add_u32_e32 v6, 4, v4
	s_waitcnt lgkmcnt(0)
	v_cmp_gt_i32_e32 vcc, v3, v0
	s_and_b64 s[58:59], vcc, exec
	s_or_b64 s[36:37], s[36:37], s[58:59]

.Lw1b39:
	v_mov_b32_e32 v6, v4
	s_or_b64 exec, exec, s[38:39]
	s_movk_i32 s36, 0x5f
	s_movk_i32 s38, 0x60
	v_cmp_lt_u32_e64 s[36:37], s36, v6
	v_cmp_gt_u32_e32 vcc, s38, v6
	s_and_saveexec_b64 s[38:39], vcc
	s_cbranch_execz .LBB1_53
	v_mov_b32_e32 v3, 0x11808
	v_lshl_add_u32 v3, v6, 2, v3
	ds_read_b32 v4, v3

.Lw1b40:
	s_andn2_b64 s[36:37], s[36:37], exec
	v_add_u32_e32 v3, 2, v6
	s_waitcnt lgkmcnt(0)
	v_cmp_gt_i32_e32 vcc, v4, v0
	s_and_b64 s[58:59], vcc, exec
	s_or_b64 s[36:37], s[36:37], s[58:59]
.LBB1_53:
	s_or_b64 exec, exec, s[38:39]
	s_and_saveexec_b64 s[38:39], s[36:37]
	v_mov_b32_e32 v3, v6
	s_or_b64 exec, exec, s[38:39]
	s_movk_i32 s36, 0x60
	s_movk_i32 s38, 0x61
	v_cmp_lt_u32_e64 s[36:37], s36, v3
	v_cmp_gt_u32_e32 vcc, s38, v3
.Lw1t41:
	s_cbranch_execz .Lw1c41
.Lw1b41:
	s_and_saveexec_b64 s[38:39], vcc
	s_cbranch_execz .LBB1_57
	v_mov_b32_e32 v4, 0x11804
	v_lshl_add_u32 v4, v3, 2, v4
	ds_read_b32 v4, v4
	s_andn2_b64 s[36:37], s[36:37], exec
	v_add_u32_e32 v6, 1, v3
	s_waitcnt lgkmcnt(0)
	v_cmp_gt_i32_e32 vcc, v4, v0
	s_and_b64 s[58:59], vcc, exec
	s_or_b64 s[36:37], s[36:37], s[58:59]

.Lw1b42:
	s_and_saveexec_b64 s[38:39], s[36:37]
	v_mov_b32_e32 v4, 0x11800
	v_lshl_add_u32 v4, v3, 2, v4
	ds_read_b32 v4, v4
	v_mov_b32_e32 v6, v3
	s_or_b64 exec, exec, s[38:39]
	v_mov_b32_e32 v3, 0x11990
	v_lshl_add_u32 v3, v6, 2, v3
	ds_read_b32 v3, v3

.Lw1b43:
	v_lshlrev_b32_e32 v6, 13, v6
	s_waitcnt lgkmcnt(1)
	v_sub_u32_e32 v4, v0, v4
	s_waitcnt lgkmcnt(0)
	v_add3_u32 v6, v4, v6, v3
	v_ashrrev_i32_e32 v7, 31, v6
	v_lshl_add_u64 v[6:7], v[6:7], 2, s[28:29]
	global_load_dword v3, v[6:7], off
.LBB1_60:
	s_or_b64 exec, exec, s[34:35]
	v_or_b32_e32 v6, 0x400, v0
	v_cmp_gt_i32_e32 vcc, s3, v6
.Lw1t44:
	s_cbranch_execz .Lw1c44
.Lw1b44:
	v_mov_b32_e32 v4, -1
	s_and_saveexec_b64 s[34:35], vcc
	s_cbranch_execz .LBB1_82
	s_waitcnt lgkmcnt(0)
	v_cmp_gt_i32_e32 vcc, v5, v6
	v_mov_b32_e32 v7, 0x11880
	s_movk_i32 s36, 0x51
	v_cndmask_b32_e64 v4, 64, 0, vcc
	v_lshl_or_b32 v7, v4, 2, v7
	ds_read_b32 v7, v7
	v_or_b32_e32 v8, 32, v4

.Lw1b45:
	s_movk_i32 s38, 0x52
	s_waitcnt lgkmcnt(0)
	v_cmp_gt_i32_e32 vcc, v7, v6
	s_nop 1
	v_cndmask_b32_e32 v7, v8, v4, vcc
	v_cmp_lt_u32_e64 s[36:37], s36, v7
	v_cmp_gt_u32_e32 vcc, s38, v7
	s_and_saveexec_b64 s[38:39], vcc
	s_cbranch_execz .LBB1_63
	v_mov_b32_e32 v4, 0x11840
	v_lshl_add_u32 v4, v7, 2, v4
	ds_read_b32 v8, v4

.Lw1b46:
	s_andn2_b64 s[36:37], s[36:37], exec
	v_or_b32_e32 v4, 16, v7
	s_waitcnt lgkmcnt(0)
	v_cmp_gt_i32_e32 vcc, v8, v6
	s_and_b64 s[58:59], vcc, exec
	s_or_b64 s[36:37], s[36:37], s[58:59]
.LBB1_63:
	s_or_b64 exec, exec, s[38:39]
	s_and_saveexec_b64 s[38:39], s[36:37]
	v_mov_b32_e32 v4, v7
	s_or_b64 exec, exec, s[38:39]
	s_movk_i32 s36, 0x59
	s_movk_i32 s38, 0x5a
	v_cmp_lt_u32_e64 s[36:37], s36, v4
.Lw1t47:
	s_cbranch_execz .Lw1c47
.Lw1b47:
	v_cmp_gt_u32_e32 vcc, s38, v4
	s_and_saveexec_b64 s[38:39], vcc
	s_cbranch_execz .LBB1_67
	v_mov_b32_e32 v7, 0x11820
	v_lshl_add_u32 v7, v4, 2, v7
	ds_read_b32 v8, v7
	s_andn2_b64 s[36:37], s[36:37], exec
	v_add_u32_e32 v7, 8, v4
	s_waitcnt lgkmcnt(0)
	v_cmp_gt_i32_e32 vcc, v8, v6
	s_and_b64 s[58:59], vcc, exec
	s_or_b64 s[36:37], s[36:37], s[58:59]

.Lw1b48:
	s_or_b64 exec, exec, s[38:39]
	s_and_saveexec_b64 s[38:39], s[36:37]
	v_mov_b32_e32 v7, v4
	s_or_b64 exec, exec, s[38:39]
	s_movk_i32 s36, 0x5d
	s_movk_i32 s38, 0x5e
	v_cmp_lt_u32_e64 s[36:37], s36, v7
	v_cmp_gt_u32_e32 vcc, s38, v7
	s_and_saveexec_b64 s[38:39], vcc
	s_cbranch_execz .LBB1_71
	v_mov_b32_e32 v4, 0x11810
	v_lshl_add_u32 v4, v7, 2, v4

.Lw1b49:
	ds_read_b32 v4, v4
	s_andn2_b64 s[36:37], s[36:37], exec
	v_add_u32_e32 v8, 4, v7
	s_waitcnt lgkmcnt(0)
	v_cmp_gt_i32_e32 vcc, v4, v6
	s_and_b64 s[58:59], vcc, exec
	s_or_b64 s[36:37], s[36:37], s[58:59]
.LBB1_71:
	s_or_b64 exec, exec, s[38:39]
	s_and_saveexec_b64 s[38:39], s[36:37]
	v_mov_b32_e32 v8, v7
	s_or_b64 exec, exec, s[38:39]
	s_movk_i32 s36, 0x5f
	s_movk_i32 s38, 0x60
	v_cmp_lt_u32_e64 s[36:37], s36, v8
.Lw1t50:
	s_cbranch_execz .Lw1c50
.Lw1b50:
	v_cmp_gt_u32_e32 vcc, s38, v8
	s_and_saveexec_b64 s[38:39], vcc
	s_cbranch_execz .LBB1_75
	v_mov_b32_e32 v4, 0x11808
	v_lshl_add_u32 v4, v8, 2, v4
	ds_read_b32 v7, v4
	s_andn2_b64 s[36:37], s[36:37], exec
	v_add_u32_e32 v4, 2, v8
	s_waitcnt lgkmcnt(0)
	v_cmp_gt_i32_e32 vcc, v7, v6
	s_and_b64 s[58:59], vcc, exec

.LBB1_75:
	s_or_b64 exec, exec, s[38:39]
	s_and_saveexec_b64 s[38:39], s[36:37]
	v_mov_b32_e32 v4, v8
	s_or_b64 exec, exec, s[38:39]
	s_movk_i32 s36, 0x60
	s_movk_i32 s38, 0x61
	v_cmp_lt_u32_e64 s[36:37], s36, v4
	v_cmp_gt_u32_e32 vcc, s38, v4
	s_and_saveexec_b64 s[38:39], vcc
	s_cbranch_execz .LBB1_79
	v_mov_b32_e32 v7, 0x11804
	v_lshl_add_u32 v7, v4, 2, v7

.Lw1b52:
	ds_read_b32 v7, v7
	s_andn2_b64 s[36:37], s[36:37], exec
	v_add_u32_e32 v8, 1, v4
	s_waitcnt lgkmcnt(0)
	v_cmp_gt_i32_e32 vcc, v7, v6
	s_and_b64 s[58:59], vcc, exec
	s_or_b64 s[36:37], s[36:37], s[58:59]
.LBB1_79:
	s_or_b64 exec, exec, s[38:39]
	s_and_saveexec_b64 s[38:39], s[36:37]
	v_mov_b32_e32 v7, 0x11800
	v_lshl_add_u32 v7, v4, 2, v7
.Lw1t53:
	s_cbranch_execz .Lw1c53
.Lw1b53:
	ds_read_b32 v7, v7
	v_mov_b32_e32 v8, v4
	s_or_b64 exec, exec, s[38:39]
	v_mov_b32_e32 v4, 0x11990
	v_lshl_add_u32 v4, v8, 2, v4
	ds_read_b32 v4, v4
	v_lshlrev_b32_e32 v8, 13, v8
	s_waitcnt lgkmcnt(1)
	v_sub_u32_e32 v6, v6, v7
	s_waitcnt lgkmcnt(0)
	v_add3_u32 v6, v6, v8, v4

.Lw1b54:
	v_ashrrev_i32_e32 v7, 31, v6
	v_lshl_add_u64 v[6:7], v[6:7], 2, s[28:29]
	global_load_dword v4, v[6:7], off
.LBB1_82:
	s_or_b64 exec, exec, s[34:35]
	v_or_b32_e32 v7, 0x800, v0
	v_cmp_gt_i32_e32 vcc, s3, v7
	v_mov_b32_e32 v6, -1
	s_and_saveexec_b64 s[34:35], vcc
	s_cbranch_execz .LBB1_104
	s_waitcnt lgkmcnt(0)
	v_cmp_gt_i32_e32 vcc, v5, v7
.Lw1t55:
	s_cbranch_execz .Lw1c55
.Lw1b55:
	v_mov_b32_e32 v8, 0x11880
	s_movk_i32 s36, 0x51
	v_cndmask_b32_e64 v6, 64, 0, vcc
	v_lshl_or_b32 v8, v6, 2, v8
	ds_read_b32 v8, v8
	v_or_b32_e32 v9, 32, v6
	s_movk_i32 s38, 0x52
	s_waitcnt lgkmcnt(0)
	v_cmp_gt_i32_e32 vcc, v8, v7
	s_nop 1
	v_cndmask_b32_e32 v8, v9, v6, vcc

.Lw1b56:
	v_cmp_lt_u32_e64 s[36:37], s36, v8
	v_cmp_gt_u32_e32 vcc, s38, v8
	s_and_saveexec_b64 s[38:39], vcc
	s_cbranch_execz .LBB1_85
	v_mov_b32_e32 v6, 0x11840
	v_lshl_add_u32 v6, v8, 2, v6
	ds_read_b32 v9, v6
	s_andn2_b64 s[36:37], s[36:37], exec
	v_or_b32_e32 v6, 16, v8
	s_waitcnt lgkmcnt(0)
	v_cmp_gt_i32_e32 vcc, v9, v7

.LBB1_85:
	s_or_b64 exec, exec, s[38:39]
	s_and_saveexec_b64 s[38:39], s[36:37]
	v_mov_b32_e32 v6, v8
	s_or_b64 exec, exec, s[38:39]
	s_movk_i32 s36, 0x59
	s_movk_i32 s38, 0x5a
	v_cmp_lt_u32_e64 s[36:37], s36, v6
	v_cmp_gt_u32_e32 vcc, s38, v6
	s_and_saveexec_b64 s[38:39], vcc
	s_cbranch_execz .LBB1_89
	v_mov_b32_e32 v8, 0x11820

.Lw1b58:
	v_lshl_add_u32 v8, v6, 2, v8
	ds_read_b32 v9, v8
	s_andn2_b64 s[36:37], s[36:37], exec
	v_add_u32_e32 v8, 8, v6
	s_waitcnt lgkmcnt(0)
	v_cmp_gt_i32_e32 vcc, v9, v7
	s_and_b64 s[58:59], vcc, exec
	s_or_b64 s[36:37], s[36:37], s[58:59]
.LBB1_89:
	s_or_b64 exec, exec, s[38:39]
	s_and_saveexec_b64 s[38:39], s[36:37]
	v_mov_b32_e32 v8, v6
	s_or_b64 exec, exec, s[38:39]
	s_movk_i32 s36, 0x5d
.Lw1t59:
	s_cbranch_execz .Lw1c59
.Lw1b59:
	s_movk_i32 s38, 0x5e
	v_cmp_lt_u32_e64 s[36:37], s36, v8
	v_cmp_gt_u32_e32 vcc, s38, v8
	s_and_saveexec_b64 s[38:39], vcc
	s_cbranch_execz .LBB1_93
	v_mov_b32_e32 v6, 0x11810
	v_lshl_add_u32 v6, v8, 2, v6
	ds_read_b32 v6, v6
	s_andn2_b64 s[36:37], s[36:37], exec
	v_add_u32_e32 v9, 4, v8
	s_waitcnt lgkmcnt(0)

.Lw1b60:
	v_cmp_gt_i32_e32 vcc, v6, v7
	s_and_b64 s[58:59], vcc, exec
	s_or_b64 s[36:37], s[36:37], s[58:59]
.LBB1_93:
	s_or_b64 exec, exec, s[38:39]
	s_and_saveexec_b64 s[38:39], s[36:37]
	v_mov_b32_e32 v9, v8
	s_or_b64 exec, exec, s[38:39]
	s_movk_i32 s36, 0x5f
	s_movk_i32 s38, 0x60
	v_cmp_lt_u32_e64 s[36:37], s36, v9
	v_cmp_gt_u32_e32 vcc, s38, v9
	s_and_saveexec_b64 s[38:39], vcc
	s_cbranch_execz .LBB1_97
	v_mov_b32_e32 v6, 0x11808

.Lw1b61:
	v_lshl_add_u32 v6, v9, 2, v6
	ds_read_b32 v8, v6
	s_andn2_b64 s[36:37], s[36:37], exec
	v_add_u32_e32 v6, 2, v9
	s_waitcnt lgkmcnt(0)
	v_cmp_gt_i32_e32 vcc, v8, v7
	s_and_b64 s[58:59], vcc, exec
	s_or_b64 s[36:37], s[36:37], s[58:59]
.LBB1_97:
	s_or_b64 exec, exec, s[38:39]
	s_and_saveexec_b64 s[38:39], s[36:37]
	v_mov_b32_e32 v6, v9
	s_or_b64 exec, exec, s[38:39]
.Lw1t62:
	s_cbranch_execz .Lw1c62
.Lw1b62:
	s_movk_i32 s36, 0x60
	s_movk_i32 s38, 0x61
	v_cmp_lt_u32_e64 s[36:37], s36, v6
	v_cmp_gt_u32_e32 vcc, s38, v6
	s_and_saveexec_b64 s[38:39], vcc
	s_cbranch_execz .LBB1_101
	v_mov_b32_e32 v8, 0x11804
	v_lshl_add_u32 v8, v6, 2, v8
	ds_read_b32 v8, v8
	s_andn2_b64 s[36:37], s[36:37], exec
	v_add_u32_e32 v9, 1, v6

.Lw1b63:
	s_waitcnt lgkmcnt(0)
	v_cmp_gt_i32_e32 vcc, v8, v7
	s_and_b64 s[58:59], vcc, exec
	s_or_b64 s[36:37], s[36:37], s[58:59]
.LBB1_101:
	s_or_b64 exec, exec, s[38:39]
	s_and_saveexec_b64 s[38:39], s[36:37]
	v_mov_b32_e32 v8, 0x11800
	v_lshl_add_u32 v8, v6, 2, v8
	ds_read_b32 v8, v8
	v_mov_b32_e32 v9, v6
	s_or_b64 exec, exec, s[38:39]
	v_mov_b32_e32 v6, 0x11990

.Lw1b64:
	v_lshl_add_u32 v6, v9, 2, v6
	ds_read_b32 v6, v6
	v_lshlrev_b32_e32 v9, 13, v9
	s_waitcnt lgkmcnt(1)
	v_sub_u32_e32 v7, v7, v8
	s_waitcnt lgkmcnt(0)
	v_add3_u32 v6, v7, v9, v6
	v_ashrrev_i32_e32 v7, 31, v6
	v_lshl_add_u64 v[6:7], v[6:7], 2, s[28:29]
	global_load_dword v6, v[6:7], off

.Lw1b65:
	s_or_b64 exec, exec, s[34:35]
	v_or_b32_e32 v8, 0xc00, v0
	v_cmp_gt_i32_e32 vcc, s3, v8
	v_mov_b32_e32 v7, -1
	s_and_saveexec_b64 s[34:35], vcc
	s_cbranch_execz .LBB1_126
	s_waitcnt lgkmcnt(0)
	v_cmp_gt_i32_e32 vcc, v5, v8
	v_mov_b32_e32 v9, 0x11880
	s_movk_i32 s36, 0x51
	v_cndmask_b32_e64 v7, 64, 0, vcc

.Lw1b66:
	v_lshl_or_b32 v9, v7, 2, v9
	ds_read_b32 v9, v9
	v_or_b32_e32 v10, 32, v7
	s_movk_i32 s38, 0x52
	s_waitcnt lgkmcnt(0)
	v_cmp_gt_i32_e32 vcc, v9, v8
	s_nop 1
	v_cndmask_b32_e32 v9, v10, v7, vcc
	v_cmp_lt_u32_e64 s[36:37], s36, v9
	v_cmp_gt_u32_e32 vcc, s38, v9
	s_and_saveexec_b64 s[38:39], vcc
	s_cbranch_execz .LBB1_107

.Lw1b67:
	v_mov_b32_e32 v7, 0x11840
	v_lshl_add_u32 v7, v9, 2, v7
	ds_read_b32 v10, v7
	s_andn2_b64 s[36:37], s[36:37], exec
	v_or_b32_e32 v7, 16, v9
	s_waitcnt lgkmcnt(0)
	v_cmp_gt_i32_e32 vcc, v10, v8
	s_and_b64 s[58:59], vcc, exec
	s_or_b64 s[36:37], s[36:37], s[58:59]
.LBB1_107:
	s_or_b64 exec, exec, s[38:39]
	s_and_saveexec_b64 s[38:39], s[36:37]
	v_mov_b32_e32 v7, v9
.Lw1t68:
	s_cbranch_execz .Lw1c68
.Lw1b68:
	s_or_b64 exec, exec, s[38:39]
	s_movk_i32 s36, 0x59
	s_movk_i32 s38, 0x5a
	v_cmp_lt_u32_e64 s[36:37], s36, v7
	v_cmp_gt_u32_e32 vcc, s38, v7
	s_and_saveexec_b64 s[38:39], vcc
	s_cbranch_execz .LBB1_111
	v_mov_b32_e32 v9, 0x11820
	v_lshl_add_u32 v9, v7, 2, v9
	ds_read_b32 v10, v9
	s_andn2_b64 s[36:37], s[36:37], exec

.Lw1b69:
	v_add_u32_e32 v9, 8, v7
	s_waitcnt lgkmcnt(0)
	v_cmp_gt_i32_e32 vcc, v10, v8
	s_and_b64 s[58:59], vcc, exec
	s_or_b64 s[36:37], s[36:37], s[58:59]
.LBB1_111:
	s_or_b64 exec, exec, s[38:39]
	s_and_saveexec_b64 s[38:39], s[36:37]
	v_mov_b32_e32 v9, v7
	s_or_b64 exec, exec, s[38:39]
	s_movk_i32 s36, 0x5d
	s_movk_i32 s38, 0x5e
	v_cmp_lt_u32_e64 s[36:37], s36, v9
	v_cmp_gt_u32_e32 vcc, s38, v9
	s_and_saveexec_b64 s[38:39], vcc

.Lw1b70:
	s_cbranch_execz .LBB1_115
	v_mov_b32_e32 v7, 0x11810
	v_lshl_add_u32 v7, v9, 2, v7
	ds_read_b32 v7, v7
	s_andn2_b64 s[36:37], s[36:37], exec
	v_add_u32_e32 v10, 4, v9
	s_waitcnt lgkmcnt(0)
	v_cmp_gt_i32_e32 vcc, v7, v8
	s_and_b64 s[58:59], vcc, exec
	s_or_b64 s[36:37], s[36:37], s[58:59]

.Lw1b71:
	v_mov_b32_e32 v10, v9
	s_or_b64 exec, exec, s[38:39]
	s_movk_i32 s36, 0x5f
	s_movk_i32 s38, 0x60
	v_cmp_lt_u32_e64 s[36:37], s36, v10
	v_cmp_gt_u32_e32 vcc, s38, v10
	s_and_saveexec_b64 s[38:39], vcc
	s_cbranch_execz .LBB1_119
	v_mov_b32_e32 v7, 0x11808
	v_lshl_add_u32 v7, v10, 2, v7
	ds_read_b32 v9, v7

.Lw1b72:
	s_andn2_b64 s[36:37], s[36:37], exec
	v_add_u32_e32 v7, 2, v10
	s_waitcnt lgkmcnt(0)
	v_cmp_gt_i32_e32 vcc, v9, v8
	s_and_b64 s[58:59], vcc, exec
	s_or_b64 s[36:37], s[36:37], s[58:59]
.LBB1_119:
	s_or_b64 exec, exec, s[38:39]
	s_and_saveexec_b64 s[38:39], s[36:37]
	v_mov_b32_e32 v7, v10
	s_or_b64 exec, exec, s[38:39]
	s_movk_i32 s36, 0x60
	s_movk_i32 s38, 0x61
	v_cmp_lt_u32_e64 s[36:37], s36, v7
	v_cmp_gt_u32_e32 vcc, s38, v7
.Lw1t73:
	s_cbranch_execz .Lw1c73
.Lw1b73:
	s_and_saveexec_b64 s[38:39], vcc
	s_cbranch_execz .LBB1_123
	v_mov_b32_e32 v9, 0x11804
	v_lshl_add_u32 v9, v7, 2, v9
	ds_read_b32 v9, v9
	s_andn2_b64 s[36:37], s[36:37], exec
	v_add_u32_e32 v10, 1, v7
	s_waitcnt lgkmcnt(0)
	v_cmp_gt_i32_e32 vcc, v9, v8
	s_and_b64 s[58:59], vcc, exec
	s_or_b64 s[36:37], s[36:37], s[58:59]

.Lw1b74:
	s_and_saveexec_b64 s[38:39], s[36:37]
	v_mov_b32_e32 v9, 0x11800
	v_lshl_add_u32 v9, v7, 2, v9
	ds_read_b32 v9, v9
	v_mov_b32_e32 v10, v7
	s_or_b64 exec, exec, s[38:39]
	v_mov_b32_e32 v7, 0x11990
	v_lshl_add_u32 v7, v10, 2, v7
	ds_read_b32 v7, v7

.Lw1b75:
	v_lshlrev_b32_e32 v10, 13, v10
	s_waitcnt lgkmcnt(1)
	v_sub_u32_e32 v8, v8, v9
	s_waitcnt lgkmcnt(0)
	v_add3_u32 v8, v8, v10, v7
	v_ashrrev_i32_e32 v9, 31, v8
	v_lshl_add_u64 v[8:9], v[8:9], 2, s[28:29]
	global_load_dword v7, v[8:9], off
.LBB1_126:
	s_or_b64 exec, exec, s[34:35]
	v_or_b32_e32 v9, 0x1000, v0
	v_cmp_gt_i32_e32 vcc, s3, v9
.Lw1t76:
	s_cbranch_execz .Lw1c76
.Lw1b76:
	v_mov_b32_e32 v8, -1
	s_and_saveexec_b64 s[34:35], vcc
	s_cbranch_execz .LBB1_148
	s_waitcnt lgkmcnt(0)
	v_cmp_gt_i32_e32 vcc, v5, v9
	v_mov_b32_e32 v10, 0x11880
	s_movk_i32 s36, 0x51
	v_cndmask_b32_e64 v8, 64, 0, vcc
	v_lshl_or_b32 v10, v8, 2, v10
	ds_read_b32 v10, v10
	v_or_b32_e32 v11, 32, v8

.Lw1b77:
	s_movk_i32 s38, 0x52
	s_waitcnt lgkmcnt(0)
	v_cmp_gt_i32_e32 vcc, v10, v9
	s_nop 1
	v_cndmask_b32_e32 v10, v11, v8, vcc
	v_cmp_lt_u32_e64 s[36:37], s36, v10
	v_cmp_gt_u32_e32 vcc, s38, v10
	s_and_saveexec_b64 s[38:39], vcc
	s_cbranch_execz .LBB1_129
	v_mov_b32_e32 v8, 0x11840
	v_lshl_add_u32 v8, v10, 2, v8
	ds_read_b32 v11, v8

.Lw1b78:
	s_andn2_b64 s[36:37], s[36:37], exec
	v_or_b32_e32 v8, 16, v10
	s_waitcnt lgkmcnt(0)
	v_cmp_gt_i32_e32 vcc, v11, v9
	s_and_b64 s[58:59], vcc, exec
	s_or_b64 s[36:37], s[36:37], s[58:59]
.LBB1_129:
	s_or_b64 exec, exec, s[38:39]
	s_and_saveexec_b64 s[38:39], s[36:37]
	v_mov_b32_e32 v8, v10
	s_or_b64 exec, exec, s[38:39]
	s_movk_i32 s36, 0x59
	s_movk_i32 s38, 0x5a
	v_cmp_lt_u32_e64 s[36:37], s36, v8
.Lw1t79:
	s_cbranch_execz .Lw1c79
.Lw1b79:
	v_cmp_gt_u32_e32 vcc, s38, v8
	s_and_saveexec_b64 s[38:39], vcc
	s_cbranch_execz .LBB1_133
	v_mov_b32_e32 v10, 0x11820
	v_lshl_add_u32 v10, v8, 2, v10
	ds_read_b32 v11, v10
	s_andn2_b64 s[36:37], s[36:37], exec
	v_add_u32_e32 v10, 8, v8
	s_waitcnt lgkmcnt(0)
	v_cmp_gt_i32_e32 vcc, v11, v9
	s_and_b64 s[58:59], vcc, exec
	s_or_b64 s[36:37], s[36:37], s[58:59]

.Lw1b80:
	s_or_b64 exec, exec, s[38:39]
	s_and_saveexec_b64 s[38:39], s[36:37]
	v_mov_b32_e32 v10, v8
	s_or_b64 exec, exec, s[38:39]
	s_movk_i32 s36, 0x5d
	s_movk_i32 s38, 0x5e
	v_cmp_lt_u32_e64 s[36:37], s36, v10
	v_cmp_gt_u32_e32 vcc, s38, v10
	s_and_saveexec_b64 s[38:39], vcc
	s_cbranch_execz .LBB1_137
	v_mov_b32_e32 v8, 0x11810
	v_lshl_add_u32 v8, v10, 2, v8

.Lw1b81:
	ds_read_b32 v8, v8
	s_andn2_b64 s[36:37], s[36:37], exec
	v_add_u32_e32 v11, 4, v10
	s_waitcnt lgkmcnt(0)
	v_cmp_gt_i32_e32 vcc, v8, v9
	s_and_b64 s[58:59], vcc, exec
	s_or_b64 s[36:37], s[36:37], s[58:59]
.LBB1_137:
	s_or_b64 exec, exec, s[38:39]
	s_and_saveexec_b64 s[38:39], s[36:37]
	v_mov_b32_e32 v11, v10
	s_or_b64 exec, exec, s[38:39]
	s_movk_i32 s36, 0x5f
	s_movk_i32 s38, 0x60
	v_cmp_lt_u32_e64 s[36:37], s36, v11
.Lw1t82:
	s_cbranch_execz .Lw1c82
.Lw1b82:
	v_cmp_gt_u32_e32 vcc, s38, v11
	s_and_saveexec_b64 s[38:39], vcc
	s_cbranch_execz .LBB1_141
	v_mov_b32_e32 v8, 0x11808
	v_lshl_add_u32 v8, v11, 2, v8
	ds_read_b32 v10, v8
	s_andn2_b64 s[36:37], s[36:37], exec
	v_add_u32_e32 v8, 2, v11
	s_waitcnt lgkmcnt(0)
	v_cmp_gt_i32_e32 vcc, v10, v9
	s_and_b64 s[58:59], vcc, exec

.LBB1_141:
	s_or_b64 exec, exec, s[38:39]
	s_and_saveexec_b64 s[38:39], s[36:37]
	v_mov_b32_e32 v8, v11
	s_or_b64 exec, exec, s[38:39]
	s_movk_i32 s36, 0x60
	s_movk_i32 s38, 0x61
	v_cmp_lt_u32_e64 s[36:37], s36, v8
	v_cmp_gt_u32_e32 vcc, s38, v8
	s_and_saveexec_b64 s[38:39], vcc
	s_cbranch_execz .LBB1_145
	v_mov_b32_e32 v10, 0x11804
	v_lshl_add_u32 v10, v8, 2, v10

.Lw1b84:
	ds_read_b32 v10, v10
	s_andn2_b64 s[36:37], s[36:37], exec
	v_add_u32_e32 v11, 1, v8
	s_waitcnt lgkmcnt(0)
	v_cmp_gt_i32_e32 vcc, v10, v9
	s_and_b64 s[58:59], vcc, exec
	s_or_b64 s[36:37], s[36:37], s[58:59]
.LBB1_145:
	s_or_b64 exec, exec, s[38:39]
	s_and_saveexec_b64 s[38:39], s[36:37]
	v_mov_b32_e32 v10, 0x11800
	v_lshl_add_u32 v10, v8, 2, v10
.Lw1t85:
	s_cbranch_execz .Lw1c85
.Lw1b85:
	ds_read_b32 v10, v10
	v_mov_b32_e32 v11, v8
	s_or_b64 exec, exec, s[38:39]
	v_mov_b32_e32 v8, 0x11990
	v_lshl_add_u32 v8, v11, 2, v8
	ds_read_b32 v8, v8
	v_lshlrev_b32_e32 v11, 13, v11
	s_waitcnt lgkmcnt(1)
	v_sub_u32_e32 v9, v9, v10
	s_waitcnt lgkmcnt(0)
	v_add3_u32 v8, v9, v11, v8

.Lw1b86:
	v_ashrrev_i32_e32 v9, 31, v8
	v_lshl_add_u64 v[8:9], v[8:9], 2, s[28:29]
	global_load_dword v8, v[8:9], off
.LBB1_148:
	s_or_b64 exec, exec, s[34:35]
	v_or_b32_e32 v10, 0x1400, v0
	v_cmp_gt_i32_e32 vcc, s3, v10
	v_mov_b32_e32 v9, -1
	s_and_saveexec_b64 s[34:35], vcc
	s_cbranch_execz .LBB1_170
	s_waitcnt lgkmcnt(0)
	v_cmp_gt_i32_e32 vcc, v5, v10
.Lw1t87:
	s_cbranch_execz .Lw1c87
.Lw1b87:
	v_mov_b32_e32 v11, 0x11880
	s_movk_i32 s36, 0x51
	v_cndmask_b32_e64 v9, 64, 0, vcc
	v_lshl_or_b32 v11, v9, 2, v11
	ds_read_b32 v11, v11
	v_or_b32_e32 v12, 32, v9
	s_movk_i32 s38, 0x52
	s_waitcnt lgkmcnt(0)
	v_cmp_gt_i32_e32 vcc, v11, v10
	s_nop 1
	v_cndmask_b32_e32 v11, v12, v9, vcc

.Lw1b88:
	v_cmp_lt_u32_e64 s[36:37], s36, v11
	v_cmp_gt_u32_e32 vcc, s38, v11
	s_and_saveexec_b64 s[38:39], vcc
	s_cbranch_execz .LBB1_151
	v_mov_b32_e32 v9, 0x11840
	v_lshl_add_u32 v9, v11, 2, v9
	ds_read_b32 v12, v9
	s_andn2_b64 s[36:37], s[36:37], exec
	v_or_b32_e32 v9, 16, v11
	s_waitcnt lgkmcnt(0)
	v_cmp_gt_i32_e32 vcc, v12, v10

.LBB1_151:
	s_or_b64 exec, exec, s[38:39]
	s_and_saveexec_b64 s[38:39], s[36:37]
	v_mov_b32_e32 v9, v11
	s_or_b64 exec, exec, s[38:39]
	s_movk_i32 s36, 0x59
	s_movk_i32 s38, 0x5a
	v_cmp_lt_u32_e64 s[36:37], s36, v9
	v_cmp_gt_u32_e32 vcc, s38, v9
	s_and_saveexec_b64 s[38:39], vcc
	s_cbranch_execz .LBB1_155
	v_mov_b32_e32 v11, 0x11820

.Lw1b90:
	v_lshl_add_u32 v11, v9, 2, v11
	ds_read_b32 v12, v11
	s_andn2_b64 s[36:37], s[36:37], exec
	v_add_u32_e32 v11, 8, v9
	s_waitcnt lgkmcnt(0)
	v_cmp_gt_i32_e32 vcc, v12, v10
	s_and_b64 s[58:59], vcc, exec
	s_or_b64 s[36:37], s[36:37], s[58:59]
.LBB1_155:
	s_or_b64 exec, exec, s[38:39]
	s_and_saveexec_b64 s[38:39], s[36:37]
	v_mov_b32_e32 v11, v9
	s_or_b64 exec, exec, s[38:39]
	s_movk_i32 s36, 0x5d
.Lw1t91:
	s_cbranch_execz .Lw1c91
.Lw1b91:
	s_movk_i32 s38, 0x5e
	v_cmp_lt_u32_e64 s[36:37], s36, v11
	v_cmp_gt_u32_e32 vcc, s38, v11
	s_and_saveexec_b64 s[38:39], vcc
	s_cbranch_execz .LBB1_159
	v_mov_b32_e32 v9, 0x11810
	v_lshl_add_u32 v9, v11, 2, v9
	ds_read_b32 v9, v9
	s_andn2_b64 s[36:37], s[36:37], exec
	v_add_u32_e32 v12, 4, v11
	s_waitcnt lgkmcnt(0)

.Lw1b92:
	v_cmp_gt_i32_e32 vcc, v9, v10
	s_and_b64 s[58:59], vcc, exec
	s_or_b64 s[36:37], s[36:37], s[58:59]
.LBB1_159:
	s_or_b64 exec, exec, s[38:39]
	s_and_saveexec_b64 s[38:39], s[36:37]
	v_mov_b32_e32 v12, v11
	s_or_b64 exec, exec, s[38:39]
	s_movk_i32 s36, 0x5f
	s_movk_i32 s38, 0x60
	v_cmp_lt_u32_e64 s[36:37], s36, v12
	v_cmp_gt_u32_e32 vcc, s38, v12
	s_and_saveexec_b64 s[38:39], vcc
	s_cbranch_execz .LBB1_163
	v_mov_b32_e32 v9, 0x11808

.Lw1b93:
	v_lshl_add_u32 v9, v12, 2, v9
	ds_read_b32 v11, v9
	s_andn2_b64 s[36:37], s[36:37], exec
	v_add_u32_e32 v9, 2, v12
	s_waitcnt lgkmcnt(0)
	v_cmp_gt_i32_e32 vcc, v11, v10
	s_and_b64 s[58:59], vcc, exec
	s_or_b64 s[36:37], s[36:37], s[58:59]
.LBB1_163:
	s_or_b64 exec, exec, s[38:39]
	s_and_saveexec_b64 s[38:39], s[36:37]
	v_mov_b32_e32 v9, v12
	s_or_b64 exec, exec, s[38:39]
.Lw1t94:
	s_cbranch_execz .Lw1c94
.Lw1b94:
	s_movk_i32 s36, 0x60
	s_movk_i32 s38, 0x61
	v_cmp_lt_u32_e64 s[36:37], s36, v9
	v_cmp_gt_u32_e32 vcc, s38, v9
	s_and_saveexec_b64 s[38:39], vcc
	s_cbranch_execz .LBB1_167
	v_mov_b32_e32 v11, 0x11804
	v_lshl_add_u32 v11, v9, 2, v11
	ds_read_b32 v11, v11
	s_andn2_b64 s[36:37], s[36:37], exec
	v_add_u32_e32 v12, 1, v9

.Lw1b95:
	s_waitcnt lgkmcnt(0)
	v_cmp_gt_i32_e32 vcc, v11, v10
	s_and_b64 s[58:59], vcc, exec
	s_or_b64 s[36:37], s[36:37], s[58:59]
.LBB1_167:
	s_or_b64 exec, exec, s[38:39]
	s_and_saveexec_b64 s[38:39], s[36:37]
	v_mov_b32_e32 v11, 0x11800
	v_lshl_add_u32 v11, v9, 2, v11
	ds_read_b32 v11, v11
	v_mov_b32_e32 v12, v9
	s_or_b64 exec, exec, s[38:39]
	v_mov_b32_e32 v9, 0x11990

.Lw1b96:
	v_lshl_add_u32 v9, v12, 2, v9
	ds_read_b32 v9, v9
	v_lshlrev_b32_e32 v12, 13, v12
	s_waitcnt lgkmcnt(1)
	v_sub_u32_e32 v10, v10, v11
	s_waitcnt lgkmcnt(0)
	v_add3_u32 v10, v10, v12, v9
	v_ashrrev_i32_e32 v11, 31, v10
	v_lshl_add_u64 v[10:11], v[10:11], 2, s[28:29]
	global_load_dword v9, v[10:11], off

.Lw1b97:
	s_or_b64 exec, exec, s[34:35]
	v_or_b32_e32 v11, 0x1800, v0
	v_cmp_gt_i32_e32 vcc, s3, v11
	v_mov_b32_e32 v10, -1
	s_and_saveexec_b64 s[34:35], vcc
	s_cbranch_execz .LBB1_192
	s_waitcnt lgkmcnt(0)
	v_cmp_gt_i32_e32 vcc, v5, v11
	v_mov_b32_e32 v12, 0x11880
	s_movk_i32 s36, 0x51
	v_cndmask_b32_e64 v10, 64, 0, vcc

.Lw1b98:
	v_lshl_or_b32 v12, v10, 2, v12
	ds_read_b32 v12, v12
	v_or_b32_e32 v13, 32, v10
	s_movk_i32 s38, 0x52
	s_waitcnt lgkmcnt(0)
	v_cmp_gt_i32_e32 vcc, v12, v11
	s_nop 1
	v_cndmask_b32_e32 v12, v13, v10, vcc
	v_cmp_lt_u32_e64 s[36:37], s36, v12
	v_cmp_gt_u32_e32 vcc, s38, v12
	s_and_saveexec_b64 s[38:39], vcc
	s_cbranch_execz .LBB1_173

.Lw1b99:
	v_mov_b32_e32 v10, 0x11840
	v_lshl_add_u32 v10, v12, 2, v10
	ds_read_b32 v13, v10
	s_andn2_b64 s[36:37], s[36:37], exec
	v_or_b32_e32 v10, 16, v12
	s_waitcnt lgkmcnt(0)
	v_cmp_gt_i32_e32 vcc, v13, v11
	s_and_b64 s[58:59], vcc, exec
	s_or_b64 s[36:37], s[36:37], s[58:59]
.LBB1_173:
	s_or_b64 exec, exec, s[38:39]
	s_and_saveexec_b64 s[38:39], s[36:37]
	v_mov_b32_e32 v10, v12
.Lw1t100:
	s_cbranch_execz .Lw1c100
.Lw1b100:
	s_or_b64 exec, exec, s[38:39]
	s_movk_i32 s36, 0x59
	s_movk_i32 s38, 0x5a
	v_cmp_lt_u32_e64 s[36:37], s36, v10
	v_cmp_gt_u32_e32 vcc, s38, v10
	s_and_saveexec_b64 s[38:39], vcc
	s_cbranch_execz .LBB1_177
	v_mov_b32_e32 v12, 0x11820
	v_lshl_add_u32 v12, v10, 2, v12
	ds_read_b32 v13, v12
	s_andn2_b64 s[36:37], s[36:37], exec

.Lw1b101:
	v_add_u32_e32 v12, 8, v10
	s_waitcnt lgkmcnt(0)
	v_cmp_gt_i32_e32 vcc, v13, v11
	s_and_b64 s[58:59], vcc, exec
	s_or_b64 s[36:37], s[36:37], s[58:59]
.LBB1_177:
	s_or_b64 exec, exec, s[38:39]
	s_and_saveexec_b64 s[38:39], s[36:37]
	v_mov_b32_e32 v12, v10
	s_or_b64 exec, exec, s[38:39]
	s_movk_i32 s36, 0x5d
	s_movk_i32 s38, 0x5e
	v_cmp_lt_u32_e64 s[36:37], s36, v12
	v_cmp_gt_u32_e32 vcc, s38, v12
	s_and_saveexec_b64 s[38:39], vcc

.Lw1b102:
	s_cbranch_execz .LBB1_181
	v_mov_b32_e32 v10, 0x11810
	v_lshl_add_u32 v10, v12, 2, v10
	ds_read_b32 v10, v10
	s_andn2_b64 s[36:37], s[36:37], exec
	v_add_u32_e32 v13, 4, v12
	s_waitcnt lgkmcnt(0)
	v_cmp_gt_i32_e32 vcc, v10, v11
	s_and_b64 s[58:59], vcc, exec
	s_or_b64 s[36:37], s[36:37], s[58:59]

.Lw1b103:
	v_mov_b32_e32 v13, v12
	s_or_b64 exec, exec, s[38:39]
	s_movk_i32 s36, 0x5f
	s_movk_i32 s38, 0x60
	v_cmp_lt_u32_e64 s[36:37], s36, v13
	v_cmp_gt_u32_e32 vcc, s38, v13
	s_and_saveexec_b64 s[38:39], vcc
	s_cbranch_execz .LBB1_185
	v_mov_b32_e32 v10, 0x11808
	v_lshl_add_u32 v10, v13, 2, v10
	ds_read_b32 v12, v10

.Lw1b104:
	s_andn2_b64 s[36:37], s[36:37], exec
	v_add_u32_e32 v10, 2, v13
	s_waitcnt lgkmcnt(0)
	v_cmp_gt_i32_e32 vcc, v12, v11
	s_and_b64 s[58:59], vcc, exec
	s_or_b64 s[36:37], s[36:37], s[58:59]
.LBB1_185:
	s_or_b64 exec, exec, s[38:39]
	s_and_saveexec_b64 s[38:39], s[36:37]
	v_mov_b32_e32 v10, v13
	s_or_b64 exec, exec, s[38:39]
	s_movk_i32 s36, 0x60
	s_movk_i32 s38, 0x61
	v_cmp_lt_u32_e64 s[36:37], s36, v10
	v_cmp_gt_u32_e32 vcc, s38, v10
.Lw1t105:
	s_cbranch_execz .Lw1c105
.Lw1b105:
	s_and_saveexec_b64 s[38:39], vcc
	s_cbranch_execz .LBB1_189
	v_mov_b32_e32 v12, 0x11804
	v_lshl_add_u32 v12, v10, 2, v12
	ds_read_b32 v12, v12
	s_andn2_b64 s[36:37], s[36:37], exec
	v_add_u32_e32 v13, 1, v10
	s_waitcnt lgkmcnt(0)
	v_cmp_gt_i32_e32 vcc, v12, v11
	s_and_b64 s[58:59], vcc, exec
	s_or_b64 s[36:37], s[36:37], s[58:59]

.Lw1b106:
	s_and_saveexec_b64 s[38:39], s[36:37]
	v_mov_b32_e32 v12, 0x11800
	v_lshl_add_u32 v12, v10, 2, v12
	ds_read_b32 v12, v12
	v_mov_b32_e32 v13, v10
	s_or_b64 exec, exec, s[38:39]
	v_mov_b32_e32 v10, 0x11990
	v_lshl_add_u32 v10, v13, 2, v10
	ds_read_b32 v10, v10

.Lw1b107:
	v_lshlrev_b32_e32 v13, 13, v13
	s_waitcnt lgkmcnt(1)
	v_sub_u32_e32 v11, v11, v12
	s_waitcnt lgkmcnt(0)
	v_add3_u32 v10, v11, v13, v10
	v_ashrrev_i32_e32 v11, 31, v10
	v_lshl_add_u64 v[10:11], v[10:11], 2, s[28:29]
	global_load_dword v10, v[10:11], off
.LBB1_192:
	s_or_b64 exec, exec, s[34:35]
	v_or_b32_e32 v11, 0x1c00, v0
	v_cmp_gt_i32_e32 vcc, s3, v11
.Lw1t108:
	s_cbranch_execz .Lw1c108
.Lw1b108:
	v_mov_b32_e32 v19, -1
	s_and_saveexec_b64 s[34:35], vcc
	s_cbranch_execz .LBB1_214
	s_waitcnt lgkmcnt(0)
	v_cmp_gt_i32_e32 vcc, v5, v11
	v_mov_b32_e32 v12, 0x11880
	s_movk_i32 s36, 0x51
	v_cndmask_b32_e64 v5, 64, 0, vcc
	v_lshl_or_b32 v12, v5, 2, v12
	ds_read_b32 v12, v12
	v_or_b32_e32 v13, 32, v5

.Lw1b109:
	s_movk_i32 s38, 0x52
	s_waitcnt lgkmcnt(0)
	v_cmp_gt_i32_e32 vcc, v12, v11
	s_nop 1
	v_cndmask_b32_e32 v12, v13, v5, vcc
	v_cmp_lt_u32_e64 s[36:37], s36, v12
	v_cmp_gt_u32_e32 vcc, s38, v12
	s_and_saveexec_b64 s[38:39], vcc
	s_cbranch_execz .LBB1_195
	v_mov_b32_e32 v5, 0x11840
	v_lshl_add_u32 v5, v12, 2, v5
	ds_read_b32 v13, v5

.Lw1b110:
	s_andn2_b64 s[36:37], s[36:37], exec
	v_or_b32_e32 v5, 16, v12
	s_waitcnt lgkmcnt(0)
	v_cmp_gt_i32_e32 vcc, v13, v11
	s_and_b64 s[58:59], vcc, exec
	s_or_b64 s[36:37], s[36:37], s[58:59]
.LBB1_195:
	s_or_b64 exec, exec, s[38:39]
	s_and_saveexec_b64 s[38:39], s[36:37]
	v_mov_b32_e32 v5, v12
	s_or_b64 exec, exec, s[38:39]
	s_movk_i32 s36, 0x59
	s_movk_i32 s38, 0x5a
	v_cmp_lt_u32_e64 s[36:37], s36, v5
.Lw1t111:
	s_cbranch_execz .Lw1c111
.Lw1b111:
	v_cmp_gt_u32_e32 vcc, s38, v5
	s_and_saveexec_b64 s[38:39], vcc
	s_cbranch_execz .LBB1_199
	v_mov_b32_e32 v12, 0x11820
	v_lshl_add_u32 v12, v5, 2, v12
	ds_read_b32 v13, v12
	s_andn2_b64 s[36:37], s[36:37], exec
	v_add_u32_e32 v12, 8, v5
	s_waitcnt lgkmcnt(0)
	v_cmp_gt_i32_e32 vcc, v13, v11
	s_and_b64 s[58:59], vcc, exec
	s_or_b64 s[36:37], s[36:37], s[58:59]

.Lw1b112:
	s_or_b64 exec, exec, s[38:39]
	s_and_saveexec_b64 s[38:39], s[36:37]
	v_mov_b32_e32 v12, v5
	s_or_b64 exec, exec, s[38:39]
	s_movk_i32 s36, 0x5d
	s_movk_i32 s38, 0x5e
	v_cmp_lt_u32_e64 s[36:37], s36, v12
	v_cmp_gt_u32_e32 vcc, s38, v12
	s_and_saveexec_b64 s[38:39], vcc
	s_cbranch_execz .LBB1_203
	v_mov_b32_e32 v5, 0x11810
	v_lshl_add_u32 v5, v12, 2, v5

.Lw1b113:
	ds_read_b32 v5, v5
	s_andn2_b64 s[36:37], s[36:37], exec
	v_add_u32_e32 v13, 4, v12
	s_waitcnt lgkmcnt(0)
	v_cmp_gt_i32_e32 vcc, v5, v11
	s_and_b64 s[58:59], vcc, exec
	s_or_b64 s[36:37], s[36:37], s[58:59]

.Lw1b114:
	v_cmp_gt_u32_e32 vcc, s38, v13
	s_and_saveexec_b64 s[38:39], vcc
	s_cbranch_execz .LBB1_207
	v_mov_b32_e32 v5, 0x11808
	v_lshl_add_u32 v5, v13, 2, v5
	ds_read_b32 v12, v5
	s_andn2_b64 s[36:37], s[36:37], exec
	v_add_u32_e32 v5, 2, v13
	s_waitcnt lgkmcnt(0)
	v_cmp_gt_i32_e32 vcc, v12, v11
	s_and_b64 s[58:59], vcc, exec

.LBB1_207:
	s_or_b64 exec, exec, s[38:39]
	s_and_saveexec_b64 s[38:39], s[36:37]
	v_mov_b32_e32 v5, v13
	s_or_b64 exec, exec, s[38:39]
	s_movk_i32 s36, 0x60
	s_movk_i32 s38, 0x61
	v_cmp_lt_u32_e64 s[36:37], s36, v5
	v_cmp_gt_u32_e32 vcc, s38, v5
	s_and_saveexec_b64 s[38:39], vcc
	s_cbranch_execz .LBB1_211
	v_mov_b32_e32 v12, 0x11804
	v_lshl_add_u32 v12, v5, 2, v12

.Lw1b116:
	ds_read_b32 v12, v12
	s_andn2_b64 s[36:37], s[36:37], exec
	v_add_u32_e32 v13, 1, v5
	s_waitcnt lgkmcnt(0)
	v_cmp_gt_i32_e32 vcc, v12, v11
	s_and_b64 s[58:59], vcc, exec
	s_or_b64 s[36:37], s[36:37], s[58:59]
.LBB1_211:
	s_or_b64 exec, exec, s[38:39]
	s_and_saveexec_b64 s[38:39], s[36:37]
	v_mov_b32_e32 v12, 0x11800
	v_lshl_add_u32 v12, v5, 2, v12
.Lw1t117:
	s_cbranch_execz .Lw1c117
.Lw1b117:
	ds_read_b32 v12, v12
	v_mov_b32_e32 v13, v5
	s_or_b64 exec, exec, s[38:39]
	v_mov_b32_e32 v5, 0x11990
	v_lshl_add_u32 v5, v13, 2, v5
	ds_read_b32 v5, v5
	v_lshlrev_b32_e32 v13, 13, v13
	s_waitcnt lgkmcnt(1)
	v_sub_u32_e32 v11, v11, v12
	s_waitcnt lgkmcnt(0)
	v_add3_u32 v12, v11, v13, v5

.Lw1b118:
	v_ashrrev_i32_e32 v13, 31, v12
	v_lshl_add_u64 v[12:13], v[12:13], 2, s[28:29]
	global_load_dword v19, v[12:13], off
.LBB1_214:
	s_or_b64 exec, exec, s[34:35]
	s_waitcnt vmcnt(0)
	v_cmp_ne_u32_e32 vcc, -1, v3
	s_waitcnt lgkmcnt(0)
	v_mov_b32_e32 v5, 0
	v_mov_b32_e32 v15, 0
	s_and_saveexec_b64 s[34:35], vcc
	v_lshrrev_b32_e32 v11, 15, v3
	v_and_b32_e32 v11, 0x1fffc, v11
.Lw1t119:
	s_cbranch_execz .Lw1c119
.Lw1b119:
	v_add_u32_e32 v11, 0x10000, v11
	v_mov_b32_e32 v12, 1
	ds_add_rtn_u32 v15, v11, v12
	s_or_b64 exec, exec, s[34:35]
	v_cmp_ne_u32_e32 vcc, -1, v4
	s_and_saveexec_b64 s[34:35], vcc
	v_lshrrev_b32_e32 v5, 15, v4
	v_and_b32_e32 v5, 0x1fffc, v5
	v_add_u32_e32 v5, 0x10000, v5
	v_mov_b32_e32 v11, 1

.Lw1b120:
	ds_add_rtn_u32 v5, v5, v11
	s_or_b64 exec, exec, s[34:35]
	v_cmp_ne_u32_e32 vcc, -1, v6
	v_mov_b32_e32 v11, 0
	v_mov_b32_e32 v16, 0
	s_and_saveexec_b64 s[34:35], vcc
	v_lshrrev_b32_e32 v12, 15, v6
	v_and_b32_e32 v12, 0x1fffc, v12
	v_add_u32_e32 v12, 0x10000, v12
	v_mov_b32_e32 v13, 1
	ds_add_rtn_u32 v16, v12, v13

.Lw1b121:
	s_or_b64 exec, exec, s[34:35]
	v_cmp_ne_u32_e32 vcc, -1, v7
	s_and_saveexec_b64 s[34:35], vcc
	v_lshrrev_b32_e32 v11, 15, v7
	v_and_b32_e32 v11, 0x1fffc, v11
	v_add_u32_e32 v11, 0x10000, v11
	v_mov_b32_e32 v12, 1
	ds_add_rtn_u32 v11, v11, v12
	s_or_b64 exec, exec, s[34:35]
	v_cmp_ne_u32_e32 vcc, -1, v8
	v_mov_b32_e32 v12, 0
	v_mov_b32_e32 v17, 0

.Lw1b122:
	s_and_saveexec_b64 s[34:35], vcc
	v_lshrrev_b32_e32 v13, 15, v8
	v_and_b32_e32 v13, 0x1fffc, v13
	v_add_u32_e32 v13, 0x10000, v13
	v_mov_b32_e32 v14, 1
	ds_add_rtn_u32 v17, v13, v14
	s_or_b64 exec, exec, s[34:35]
	v_cmp_ne_u32_e32 vcc, -1, v9
	s_and_saveexec_b64 s[34:35], vcc
	v_lshrrev_b32_e32 v12, 15, v9
	v_and_b32_e32 v12, 0x1fffc, v12

.Lw1b123:
	v_add_u32_e32 v12, 0x10000, v12
	v_mov_b32_e32 v13, 1
	ds_add_rtn_u32 v12, v12, v13
	s_or_b64 exec, exec, s[34:35]
	v_cmp_ne_u32_e32 vcc, -1, v10
	v_mov_b32_e32 v14, 0
	v_mov_b32_e32 v18, 0
	s_and_saveexec_b64 s[34:35], vcc
	v_lshrrev_b32_e32 v13, 15, v10
	v_and_b32_e32 v13, 0x1fffc, v13
	v_add_u32_e32 v13, 0x10000, v13

.Lw1b124:
	v_mov_b32_e32 v18, 1
	ds_add_rtn_u32 v18, v13, v18
	s_or_b64 exec, exec, s[34:35]
	v_mov_b32_e32 v13, -1
	v_cmp_ne_u32_e32 vcc, -1, v19
	s_and_saveexec_b64 s[34:35], vcc
	s_cbranch_execz .LBB1_230
	v_lshrrev_b32_e32 v13, 15, v19
	v_and_b32_e32 v13, 0x1fffc, v13
	v_add_u32_e32 v13, 0x10000, v13
	v_mov_b32_e32 v14, 1
	ds_add_rtn_u32 v14, v13, v14

.Lw1b125:
	v_mov_b32_e32 v13, v19

.LBB1_232:
	v_cmp_lt_i32_e32 vcc, s57, v2
	v_mov_b32_e32 v2, 0
	s_waitcnt lgkmcnt(0)
.Lw1t126:
	s_cbranch_execz .Lw1c126
.Lw1b126:
	s_barrier
	s_and_saveexec_b64 s[34:35], s[22:23]
	v_mov_b32_e32 v2, 0x10000
	v_lshl_or_b32 v2, v0, 2, v2
	ds_read_b32 v2, v2
	s_or_b64 exec, exec, s[34:35]
	s_waitcnt lgkmcnt(0)
	v_add_u32_dpp v19, v2, v2 row_shr:1 row_mask:0xf bank_mask:0xf bound_ctrl:1
	s_nop 1
	v_add_u32_dpp v19, v19, v19 row_shr:2 row_mask:0xf bank_mask:0xf bound_ctrl:1

.Lw1b127:
	s_nop 1
	v_add_u32_dpp v19, v19, v19 row_shr:4 row_mask:0xf bank_mask:0xf bound_ctrl:1
	s_nop 1
	v_add_u32_dpp v19, v19, v19 row_shr:8 row_mask:0xf bank_mask:0xf bound_ctrl:1
	s_nop 1
	v_add_u32_dpp v19, v19, v19 row_bcast:15 row_mask:0xa bank_mask:0xf
	s_nop 1
	v_add_u32_dpp v19, v19, v19 row_bcast:31 row_mask:0xc bank_mask:0xf
	s_and_saveexec_b64 s[34:35], s[4:5]
	v_mov_b32_e32 v20, 0x11b60

.Lw1b128:
	v_lshl_add_u32 v1, v1, 2, v20
	ds_write_b32 v1, v19
	s_or_b64 exec, exec, s[34:35]
	s_add_i32 s41, s41, s40
	s_add_i32 s42, s42, s41
	s_add_i32 s43, s43, s42
	s_add_i32 s44, s44, s43
	s_add_i32 s45, s45, s44
	s_add_i32 s46, s46, s45
	s_add_i32 s47, s47, s46
	s_add_i32 s48, s48, s47
	s_add_i32 s49, s49, s48
	s_add_i32 s50, s50, s49

.Lw1b129:
	s_add_i32 s51, s51, s50
	s_add_i32 s52, s52, s51
	s_add_i32 s53, s53, s52
	s_add_i32 s54, s54, s53
	s_add_i32 s34, s55, s54
	s_waitcnt lgkmcnt(0)
	s_barrier
	s_and_saveexec_b64 s[36:37], s[22:23]
	s_cbranch_execz .LBB1_239
	v_mov_b32_e32 v1, 0x11b98
	v_mov_b32_e32 v20, 0x11b70
	ds_read_b32 v1, v1

.Lw1b130:
	ds_read_b96 v[24:26], v20
	v_mov_b32_e32 v20, 0x11b60
	ds_read_b128 v[20:23], v20
	v_sub_u32_e32 v2, v19, v2
	s_waitcnt lgkmcnt(2)
	v_cndmask_b32_e64 v1, 0, v1, s[20:21]
	s_waitcnt lgkmcnt(1)
	v_cndmask_b32_e64 v24, 0, v24, s[14:15]
	v_cndmask_b32_e64 v26, 0, v26, s[18:19]

.Lw1b131:
	s_waitcnt lgkmcnt(0)
	v_cndmask_b32_e64 v22, 0, v22, s[10:11]
	v_cndmask_b32_e64 v21, 0, v21, s[8:9]
	v_cndmask_b32_e64 v20, v20, 0, s[6:7]
	v_cndmask_b32_e64 v23, 0, v23, s[12:13]
	v_add3_u32 v20, v21, v20, v22
	v_cndmask_b32_e64 v25, 0, v25, s[16:17]
	v_add3_u32 v20, v23, v20, v24

.Lw1b132:
	v_add3_u32 v20, v25, v20, v26
	v_add3_u32 v1, v1, v20, v2
	v_mov_b32_e32 v2, 0x11000
	v_lshl_or_b32 v2, v0, 2, v2
	ds_write_b32 v2, v1
	v_lshl_or_b32 v2, s33, 9, v0
	s_mov_b32 s4, 0x186a0
	v_cmp_gt_u32_e64 s[4:5], s4, v2

.Lw1b133:
	s_and_b64 exec, exec, s[4:5]
	s_cbranch_execz .LBB1_239
	s_and_b64 s[4:5], s[30:31], exec
	s_cselect_b32 s4, 0x186a1, 0
	v_add_u32_e32 v20, s4, v2
	v_mov_b32_e32 v21, 0
	v_lshl_add_u64 v[20:21], v[20:21], 2, s[24:25]
	v_add_u32_e32 v1, s34, v1
	global_store_dword v[20:21], v1, off
.LBB1_239:
	s_or_b64 exec, exec, s[36:37]
	s_cmpk_eq_i32 s33, 0xc3
	s_cselect_b64 s[6:7], -1, 0
.Lw1t134:
	s_cbranch_execz .Lw1c134
.Lw1b134:
	v_cmp_eq_u32_e64 s[4:5], 0, v0
	s_and_b64 s[6:7], s[4:5], s[6:7]
	s_and_saveexec_b64 s[4:5], s[6:7]
	s_cbranch_execz .LBB1_241
	s_and_b64 s[6:7], s[30:31], exec
	s_cselect_b32 s6, 0x61a84, 0
	s_add_u32 s6, s24, s6
	s_addc_u32 s7, s25, 0
	v_mov_b32_e32 v1, 0x61000
	v_mov_b32_e32 v2, 0xc3500

.Lw1b135:
	global_store_dword v1, v2, s[6:7] offset:2688
.LBB1_241:
	s_or_b64 exec, exec, s[4:5]
	s_add_u32 s6, s26, s56
	s_addc_u32 s7, s27, 0
	s_ashr_i32 s35, s34, 31
	s_lshl_b64 s[4:5], s[34:35], 2
	s_add_u32 s8, s6, s4
	s_addc_u32 s9, s7, s5
	s_mov_b64 s[4:5], -1
	s_and_b64 vcc, exec, vcc
	s_waitcnt lgkmcnt(0)
	s_barrier
	s_cbranch_vccz .LBB1_265
	v_mov_b32_e32 v1, 0x11900

.Lw1b136:
	ds_read_b32 v1, v1
	s_mov_b64 s[4:5], 0
	v_mov_b32_e32 v2, 0x11880
	s_movk_i32 s12, 0x51
	s_movk_i32 s13, 0x52
	s_movk_i32 s14, 0x59
	s_movk_i32 s15, 0x5a
	s_movk_i32 s16, 0x5d
	s_movk_i32 s17, 0x5e
	s_movk_i32 s18, 0x5f
	s_movk_i32 s19, 0x60
	s_movk_i32 s20, 0x61

.Lw1b137:
	v_mov_b32_e32 v19, 0x11990
	v_mov_b32_e32 v20, 1
	v_mov_b32_e32 v21, 0x11840
	v_mov_b32_e32 v22, 0x11820
	v_mov_b32_e32 v23, 0x11810
	v_mov_b32_e32 v24, 0x11808
	v_mov_b32_e32 v25, 0x11804
	v_mov_b32_e32 v26, 0x11800

.Lw1b138:
	v_mov_b32_e32 v27, v0
	s_branch .LBB1_244
.LBB1_243:
	s_or_b64 exec, exec, s[10:11]
	v_lshl_add_u32 v28, v30, 2, v19
	ds_read_b32 v28, v28
	s_waitcnt lgkmcnt(0)
	v_lshl_add_u32 v28, v30, 13, v28
	v_sub_u32_e32 v28, v28, v29
	v_add_u32_e32 v28, v27, v28
	v_ashrrev_i32_e32 v29, 31, v28
	v_lshl_add_u64 v[28:29], v[28:29], 2, s[28:29]

.Lw1b139:
	global_load_dword v28, v[28:29], off
	v_add_u32_e32 v27, 0x400, v27
	v_cmp_le_i32_e32 vcc, s3, v27
	s_or_b64 s[4:5], vcc, s[4:5]
	s_waitcnt vmcnt(0)
	v_lshrrev_b32_e32 v29, 15, v28
	v_and_b32_e32 v29, 0x1fffc, v29
	v_add_u32_e32 v30, 0x11000, v29
	v_add_u32_e32 v29, 0x10800, v29
	ds_read_b32 v30, v30

.Lw1b140:
	ds_add_rtn_u32 v29, v29, v20
	v_and_b32_e32 v31, 0x1fffff, v28
	s_waitcnt lgkmcnt(0)
	v_add_u32_e32 v28, v29, v30
	v_ashrrev_i32_e32 v29, 31, v28
	v_lshl_add_u64 v[28:29], v[28:29], 2, s[8:9]
	global_store_dword v[28:29], v31, off
	s_andn2_b64 exec, exec, s[4:5]
	s_cbranch_execz .LBB1_264
.LBB1_244:
	s_waitcnt lgkmcnt(0)
.Lw1t141:
	s_cbranch_execz .Lw1c141
.Lw1b141:
	v_cmp_gt_i32_e32 vcc, v1, v27
	s_nop 1
	v_cndmask_b32_e64 v28, 64, 0, vcc
	v_lshl_or_b32 v29, v28, 2, v2
	ds_read_b32 v29, v29
	v_or_b32_e32 v30, 32, v28
	s_waitcnt lgkmcnt(0)
	v_cmp_gt_i32_e32 vcc, v29, v27
	s_nop 1
	v_cndmask_b32_e32 v29, v30, v28, vcc
	v_cmp_lt_u32_e64 s[6:7], s12, v29

.Lw1b142:
	v_cmp_gt_u32_e32 vcc, s13, v29
	s_and_saveexec_b64 s[10:11], vcc
	s_cbranch_execz .LBB1_246
	v_lshl_add_u32 v28, v29, 2, v21
	ds_read_b32 v30, v28
	s_andn2_b64 s[6:7], s[6:7], exec
	v_or_b32_e32 v28, 16, v29
	s_waitcnt lgkmcnt(0)
	v_cmp_gt_i32_e32 vcc, v30, v27
	s_and_b64 s[22:23], vcc, exec
	s_or_b64 s[6:7], s[6:7], s[22:23]
.LBB1_246:
	s_or_b64 exec, exec, s[10:11]
	s_and_saveexec_b64 s[10:11], s[6:7]
.Lw1t143:
	s_cbranch_execz .Lw1c143
.Lw1b143:
	v_mov_b32_e32 v28, v29
	s_or_b64 exec, exec, s[10:11]
	v_cmp_lt_u32_e64 s[6:7], s14, v28
	v_cmp_gt_u32_e32 vcc, s15, v28
	s_and_saveexec_b64 s[10:11], vcc
	s_cbranch_execz .LBB1_250
	v_lshl_add_u32 v29, v28, 2, v22
	ds_read_b32 v30, v29
	s_andn2_b64 s[6:7], s[6:7], exec
	v_add_u32_e32 v29, 8, v28
	s_waitcnt lgkmcnt(0)
	v_cmp_gt_i32_e32 vcc, v30, v27

.Lw1b144:
	s_and_b64 s[22:23], vcc, exec
	s_or_b64 s[6:7], s[6:7], s[22:23]
.LBB1_250:
	s_or_b64 exec, exec, s[10:11]
	s_and_saveexec_b64 s[10:11], s[6:7]
	v_mov_b32_e32 v29, v28
	s_or_b64 exec, exec, s[10:11]
	v_cmp_lt_u32_e64 s[6:7], s16, v29
	v_cmp_gt_u32_e32 vcc, s17, v29
	s_and_saveexec_b64 s[10:11], vcc
	s_cbranch_execz .LBB1_254
	v_lshl_add_u32 v28, v29, 2, v23
	ds_read_b32 v28, v28

.Lw1b145:
	s_andn2_b64 s[6:7], s[6:7], exec
	v_add_u32_e32 v30, 4, v29
	s_waitcnt lgkmcnt(0)
	v_cmp_gt_i32_e32 vcc, v28, v27
	s_and_b64 s[22:23], vcc, exec
	s_or_b64 s[6:7], s[6:7], s[22:23]
.LBB1_254:
	s_or_b64 exec, exec, s[10:11]
	s_and_saveexec_b64 s[10:11], s[6:7]
	v_mov_b32_e32 v30, v29
	s_or_b64 exec, exec, s[10:11]
	v_cmp_lt_u32_e64 s[6:7], s18, v30
	v_cmp_gt_u32_e32 vcc, s19, v30
	s_and_saveexec_b64 s[10:11], vcc
	s_cbranch_execz .LBB1_258
.Lw1t146:
	s_cbranch_execz .Lw1c146
.Lw1b146:
	v_lshl_add_u32 v28, v30, 2, v24
	ds_read_b32 v29, v28
	s_andn2_b64 s[6:7], s[6:7], exec
	v_add_u32_e32 v28, 2, v30
	s_waitcnt lgkmcnt(0)
	v_cmp_gt_i32_e32 vcc, v29, v27
	s_and_b64 s[22:23], vcc, exec
	s_or_b64 s[6:7], s[6:7], s[22:23]
.LBB1_258:
	s_or_b64 exec, exec, s[10:11]
	s_and_saveexec_b64 s[10:11], s[6:7]
	v_mov_b32_e32 v28, v30
	s_or_b64 exec, exec, s[10:11]
	v_cmp_lt_u32_e64 s[6:7], s19, v28
.Lw1t147:
	s_cbranch_execz .Lw1c147
.Lw1b147:
	v_cmp_gt_u32_e32 vcc, s20, v28
	s_and_saveexec_b64 s[10:11], vcc
	s_cbranch_execz .LBB1_262
	v_lshl_add_u32 v29, v28, 2, v25
	ds_read_b32 v29, v29
	s_andn2_b64 s[6:7], s[6:7], exec
	v_add_u32_e32 v30, 1, v28
	s_waitcnt lgkmcnt(0)
	v_cmp_gt_i32_e32 vcc, v29, v27
	s_and_b64 s[22:23], vcc, exec
	s_or_b64 s[6:7], s[6:7], s[22:23]
.LBB1_262:
	s_or_b64 exec, exec, s[10:11]
.Lw1t148:
	s_cbranch_execz .Lw1c148
.Lw1b148:
	s_and_saveexec_b64 s[10:11], s[6:7]
	s_cbranch_execz .LBB1_243
	v_lshl_add_u32 v29, v28, 2, v26
	ds_read_b32 v29, v29
	v_mov_b32_e32 v30, v28
	s_branch .LBB1_243

.LBB1_265:
	s_and_b64 vcc, exec, s[4:5]
	s_cbranch_vccz .LBB1_390
	v_cmp_ne_u32_e32 vcc, -1, v3
	s_and_saveexec_b64 s[4:5], vcc
	s_cbranch_execz .LBB1_274
.Lw1t149:
	s_cbranch_execz .Lw1c149
.Lw1b149:
	v_lshrrev_b32_e32 v1, 15, v3
	v_and_b32_e32 v1, 0x1fffc, v1
	v_add_u32_e32 v1, 0x11000, v1
	ds_read_b32 v1, v1
	v_lshlrev_b32_e32 v2, 2, v15
	s_waitcnt lgkmcnt(0)
	v_lshl_add_u32 v1, v1, 2, v2
	ds_write_b32 v1, v3
	s_or_b64 exec, exec, s[4:5]
	v_cmp_ne_u32_e32 vcc, -1, v4

.Lw1b150:
	s_and_saveexec_b64 s[4:5], vcc
	s_cbranch_execnz .LBB1_275
.LBB1_268:
	s_or_b64 exec, exec, s[4:5]
	v_cmp_ne_u32_e32 vcc, -1, v6
	s_and_saveexec_b64 s[4:5], vcc
	s_cbranch_execz .LBB1_276
.LBB1_269:
	v_lshrrev_b32_e32 v1, 15, v6
	v_and_b32_e32 v1, 0x1fffc, v1
	v_add_u32_e32 v1, 0x11000, v1
	ds_read_b32 v1, v1
	v_lshlrev_b32_e32 v2, 2, v16
	s_waitcnt lgkmcnt(0)
.Lw1t151:
	s_cbranch_execz .Lw1c151
.Lw1b151:
	v_lshl_add_u32 v1, v1, 2, v2
	ds_write_b32 v1, v6
	s_or_b64 exec, exec, s[4:5]
	v_cmp_ne_u32_e32 vcc, -1, v7
	s_and_saveexec_b64 s[4:5], vcc
	s_cbranch_execnz .LBB1_277

.LBB1_271:
	v_lshrrev_b32_e32 v1, 15, v8
	v_and_b32_e32 v1, 0x1fffc, v1
.Lw1t152:
	s_cbranch_execz .Lw1c152
.Lw1b152:
	v_add_u32_e32 v1, 0x11000, v1
	ds_read_b32 v1, v1
	v_lshlrev_b32_e32 v2, 2, v17
	s_waitcnt lgkmcnt(0)
	v_lshl_add_u32 v1, v1, 2, v2
	ds_write_b32 v1, v8
	s_or_b64 exec, exec, s[4:5]
	v_cmp_ne_u32_e32 vcc, -1, v9
	s_and_saveexec_b64 s[4:5], vcc
	s_cbranch_execnz .LBB1_279

.Lw1b153:
	v_cmp_ne_u32_e32 vcc, -1, v10
	s_and_saveexec_b64 s[4:5], vcc
	s_cbranch_execz .LBB1_280
.LBB1_273:
	v_lshrrev_b32_e32 v1, 15, v10
	v_and_b32_e32 v1, 0x1fffc, v1
	v_add_u32_e32 v1, 0x11000, v1
	ds_read_b32 v1, v1
	v_lshlrev_b32_e32 v2, 2, v18
	s_waitcnt lgkmcnt(0)
	v_lshl_add_u32 v1, v1, 2, v2
	ds_write_b32 v1, v10

.Lw1b154:
	s_or_b64 exec, exec, s[4:5]
	v_cmp_ne_u32_e32 vcc, -1, v13
	s_and_saveexec_b64 s[4:5], vcc
	s_cbranch_execnz .LBB1_281
	s_branch .LBB1_282

.LBB1_275:
	v_lshrrev_b32_e32 v1, 15, v4
	v_and_b32_e32 v1, 0x1fffc, v1
	v_add_u32_e32 v1, 0x11000, v1
.Lw1t155:
	s_cbranch_execz .Lw1c155
.Lw1b155:
	ds_read_b32 v1, v1
	v_lshlrev_b32_e32 v2, 2, v5
	s_waitcnt lgkmcnt(0)
	v_lshl_add_u32 v1, v1, 2, v2
	ds_write_b32 v1, v4
	s_or_b64 exec, exec, s[4:5]
	v_cmp_ne_u32_e32 vcc, -1, v6
	s_and_saveexec_b64 s[4:5], vcc
	s_cbranch_execnz .LBB1_269
.LBB1_276:
	s_or_b64 exec, exec, s[4:5]
	v_cmp_ne_u32_e32 vcc, -1, v7
	s_and_saveexec_b64 s[4:5], vcc
.Lw1t156:
	s_cbranch_execz .Lw1c156

.LBB1_277:
	v_lshrrev_b32_e32 v1, 15, v7
	v_and_b32_e32 v1, 0x1fffc, v1
	v_add_u32_e32 v1, 0x11000, v1
	ds_read_b32 v1, v1
	v_lshlrev_b32_e32 v2, 2, v11
	s_waitcnt lgkmcnt(0)
	v_lshl_add_u32 v1, v1, 2, v2
	ds_write_b32 v1, v7
	s_or_b64 exec, exec, s[4:5]

.Lw1b157:
	v_cmp_ne_u32_e32 vcc, -1, v8
	s_and_saveexec_b64 s[4:5], vcc
	s_cbranch_execnz .LBB1_271

.LBB1_279:
	v_lshrrev_b32_e32 v1, 15, v9
	v_and_b32_e32 v1, 0x1fffc, v1
	v_add_u32_e32 v1, 0x11000, v1
	ds_read_b32 v1, v1
	v_lshlrev_b32_e32 v2, 2, v12
.Lw1t158:
	s_cbranch_execz .Lw1c158
.Lw1b158:
	s_waitcnt lgkmcnt(0)
	v_lshl_add_u32 v1, v1, 2, v2
	ds_write_b32 v1, v9
	s_or_b64 exec, exec, s[4:5]
	v_cmp_ne_u32_e32 vcc, -1, v10
	s_and_saveexec_b64 s[4:5], vcc
	s_cbranch_execnz .LBB1_273

.LBB1_281:
	v_lshrrev_b32_e32 v1, 15, v13
	v_and_b32_e32 v1, 0x1fffc, v1
.Lw1t159:
	s_cbranch_execz .Lw1c159
.Lw1b159:
	v_add_u32_e32 v1, 0x11000, v1
	ds_read_b32 v1, v1
	v_lshlrev_b32_e32 v2, 2, v14
	s_waitcnt lgkmcnt(0)
	v_lshl_add_u32 v1, v1, 2, v2
	ds_write_b32 v1, v13
.LBB1_282:
	s_or_b64 exec, exec, s[4:5]
	v_mov_b32_e32 v1, 0x11ba0
	v_mov_b32_e32 v2, -1

.Lw1b160:
	ds_write_b32 v1, v2
	s_cmp_lt_i32 s3, 1
	s_waitcnt lgkmcnt(0)
	s_barrier
	s_cbranch_scc1 .LBB1_332
	v_lshlrev_b32_e32 v1, 2, v0
	s_lshl_b32 s18, s3, 2
	s_mov_b32 s19, 0x1fffc
	s_mov_b32 s20, 0x10000
	v_mov_b32_e32 v7, 0x11ba0
	v_mov_b32_e32 v2, v0

.Lw1b161:
	v_cmp_gt_i32_e64 s[10:11], s3, v2
	ds_read_b32 v17, v1
	v_mov_b32_e32 v16, v1
	v_add_u32_e32 v2, 1024, v0
	v_cmp_gt_i32_e64 s[12:13], s3, v2
	ds_read_b32 v19, v1 offset:4096
	v_add_u32_e32 v18, 4096, v1
	v_add_u32_e32 v2, 2048, v0

.Lw1b162:
	v_cmp_gt_i32_e64 s[14:15], s3, v2
	ds_read_b32 v21, v1 offset:8192
	v_add_u32_e32 v20, 8192, v1
	v_add_u32_e32 v2, 3072, v0
	v_cmp_gt_i32_e64 s[16:17], s3, v2
	ds_read_b32 v23, v1 offset:12288
	v_add_u32_e32 v22, 12288, v1
	s_waitcnt lgkmcnt(0)

.Lw1b163:
	v_lshrrev_b32_e32 v2, 15, v17
	v_and_b32_e32 v2, s19, v2
	v_lshrrev_b32_e32 v3, 15, v19
	v_and_b32_e32 v3, s19, v3
	v_lshrrev_b32_e32 v4, 15, v21
	v_and_b32_e32 v4, s19, v4
	v_lshrrev_b32_e32 v5, 15, v23
	v_and_b32_e32 v5, s19, v5
	v_cndmask_b32_e64 v2, 0, v2, s[10:11]
	v_add_u32_e32 v2, s20, v2
	v_cndmask_b32_e64 v3, 0, v3, s[12:13]
	v_add_u32_e32 v3, s20, v3
	v_cndmask_b32_e64 v4, 0, v4, s[14:15]

.Lw1b164:
	v_add_u32_e32 v4, s20, v4
	v_cndmask_b32_e64 v5, 0, v5, s[16:17]
	v_add_u32_e32 v5, s20, v5
	ds_read_b32 v24, v2
	ds_read_b32 v28, v2 offset:4096
	ds_read_b32 v25, v3
	ds_read_b32 v29, v3 offset:4096
	ds_read_b32 v26, v4

.Lw1b165:
	ds_read_b32 v30, v4 offset:4096
	ds_read_b32 v27, v5
	ds_read_b32 v31, v5 offset:4096
	s_waitcnt lgkmcnt(0)
	v_cndmask_b32_e64 v2, 0, v24, s[10:11]
	v_lshlrev_b32_e32 v28, 2, v28
	v_mov_b32_e32 v8, v28
	v_mov_b32_e32 v24, 0
	v_cndmask_b32_e64 v3, 0, v25, s[12:13]
	v_lshlrev_b32_e32 v29, 2, v29

.Lw1b166:
	v_mov_b32_e32 v10, v29
	v_mov_b32_e32 v25, 0
	v_cndmask_b32_e64 v4, 0, v26, s[14:15]
	v_lshlrev_b32_e32 v30, 2, v30
	v_mov_b32_e32 v12, v30
	v_mov_b32_e32 v26, 0
	v_cndmask_b32_e64 v5, 0, v27, s[16:17]
	v_lshlrev_b32_e32 v31, 2, v31
	v_mov_b32_e32 v14, v31
	v_mov_b32_e32 v27, 0
	v_max_u32_e32 v6, v2, v3
	v_max3_u32 v6, v6, v4, v5

.Lw1b167:
	s_mov_b32 s21, 0
.Lrs0_loop:
	v_cmp_lt_u32_e32 vcc, s21, v6
	s_cbranch_vccz .Lrs0_done
	v_cmp_gt_u32_e64 s[22:23], s18, v8
	v_cmp_gt_u32_e64 s[24:25], s18, v10
	v_cmp_gt_u32_e64 s[26:27], s18, v12
	v_cmp_gt_u32_e64 s[28:29], s18, v14
	v_cndmask_b32_e64 v2, v7, v8, s[22:23]
	v_cndmask_b32_e64 v3, v7, v10, s[24:25]

.Lw1b168:
	v_cndmask_b32_e64 v4, v7, v12, s[26:27]
	v_cndmask_b32_e64 v5, v7, v14, s[28:29]
	ds_read_b32 v9, v2
	ds_read_b32 v11, v3
	ds_read_b32 v13, v4
	ds_read_b32 v15, v5
	s_waitcnt lgkmcnt(3)
	v_cmp_lt_u64_e64 s[22:23], v[8:9], v[16:17]

.Lw1b169:
	s_waitcnt lgkmcnt(2)
	v_cmp_lt_u64_e64 s[24:25], v[10:11], v[18:19]
	s_waitcnt lgkmcnt(1)
	v_cmp_lt_u64_e64 s[26:27], v[12:13], v[20:21]
	s_waitcnt lgkmcnt(0)
	v_cmp_lt_u64_e64 s[28:29], v[14:15], v[22:23]
	v_addc_co_u32_e64 v24, s[4:5], 0, v24, s[22:23]
	v_addc_co_u32_e64 v25, s[4:5], 0, v25, s[24:25]
	v_addc_co_u32_e64 v26, s[4:5], 0, v26, s[26:27]

.Lw1b170:
	v_addc_co_u32_e64 v27, s[4:5], 0, v27, s[28:29]
	v_add_u32_e32 v8, 4, v8
	v_add_u32_e32 v10, 4, v10
	v_add_u32_e32 v12, 4, v12
	v_add_u32_e32 v14, 4, v14
	s_add_i32 s21, s21, 1
	s_branch .Lrs0_loop
.Lrs0_done:
	v_and_b32_e32 v2, 0x1fffff, v17
	v_lshl_add_u32 v28, v24, 2, v28
	v_and_b32_e32 v3, 0x1fffff, v19
	v_lshl_add_u32 v29, v25, 2, v29

.Lw1b171:
	v_and_b32_e32 v4, 0x1fffff, v21
	v_lshl_add_u32 v30, v26, 2, v30
	v_and_b32_e32 v5, 0x1fffff, v23
	v_lshl_add_u32 v31, v27, 2, v31
	s_mov_b64 exec, s[10:11]
	ds_write_b32 v28, v2 offset:32768
	s_mov_b64 exec, s[12:13]
	ds_write_b32 v29, v3 offset:32768

.Lw1b172:
	s_mov_b64 exec, s[14:15]
	ds_write_b32 v30, v4 offset:32768
	s_mov_b64 exec, s[16:17]
	ds_write_b32 v31, v5 offset:32768
	s_mov_b64 exec, -1
.LBB1_332:
	s_cmpk_lt_i32 s3, 0x1001
	s_cbranch_scc1 .LBB1_382
	v_add_u32_e32 v2, 4096, v0
	v_cmp_gt_i32_e64 s[10:11], s3, v2
	ds_read_b32 v17, v1 offset:16384

.Lw1b173:
	v_add_u32_e32 v16, 16384, v1
	v_add_u32_e32 v2, 5120, v0
	v_cmp_gt_i32_e64 s[12:13], s3, v2
	ds_read_b32 v19, v1 offset:20480
	v_add_u32_e32 v18, 20480, v1
	v_add_u32_e32 v2, 6144, v0
	v_cmp_gt_i32_e64 s[14:15], s3, v2
	ds_read_b32 v21, v1 offset:24576

.Lw1b174:
	v_add_u32_e32 v20, 24576, v1
	v_add_u32_e32 v2, 7168, v0
	v_cmp_gt_i32_e64 s[16:17], s3, v2
	ds_read_b32 v23, v1 offset:28672
	v_add_u32_e32 v22, 28672, v1
	s_waitcnt lgkmcnt(0)
	v_lshrrev_b32_e32 v2, 15, v17
	v_and_b32_e32 v2, s19, v2
	v_lshrrev_b32_e32 v3, 15, v19

.Lw1b175:
	v_and_b32_e32 v3, s19, v3
	v_lshrrev_b32_e32 v4, 15, v21
	v_and_b32_e32 v4, s19, v4
	v_lshrrev_b32_e32 v5, 15, v23
	v_and_b32_e32 v5, s19, v5
	v_cndmask_b32_e64 v2, 0, v2, s[10:11]
	v_add_u32_e32 v2, s20, v2
	v_cndmask_b32_e64 v3, 0, v3, s[12:13]
	v_add_u32_e32 v3, s20, v3
	v_cndmask_b32_e64 v4, 0, v4, s[14:15]
	v_add_u32_e32 v4, s20, v4
	v_cndmask_b32_e64 v5, 0, v5, s[16:17]

.Lw1b176:
	v_add_u32_e32 v5, s20, v5
	ds_read_b32 v24, v2
	ds_read_b32 v28, v2 offset:4096
	ds_read_b32 v25, v3
	ds_read_b32 v29, v3 offset:4096
	ds_read_b32 v26, v4
	ds_read_b32 v30, v4 offset:4096
	ds_read_b32 v27, v5

.Lw1b177:
	ds_read_b32 v31, v5 offset:4096
	s_waitcnt lgkmcnt(0)
	v_cndmask_b32_e64 v2, 0, v24, s[10:11]
	v_lshlrev_b32_e32 v28, 2, v28
	v_mov_b32_e32 v8, v28
	v_mov_b32_e32 v24, 0
	v_cndmask_b32_e64 v3, 0, v25, s[12:13]
	v_lshlrev_b32_e32 v29, 2, v29
	v_mov_b32_e32 v10, v29
	v_mov_b32_e32 v25, 0
	v_cndmask_b32_e64 v4, 0, v26, s[14:15]

.Lw1b178:
	v_lshlrev_b32_e32 v30, 2, v30
	v_mov_b32_e32 v12, v30
	v_mov_b32_e32 v26, 0
	v_cndmask_b32_e64 v5, 0, v27, s[16:17]
	v_lshlrev_b32_e32 v31, 2, v31
	v_mov_b32_e32 v14, v31
	v_mov_b32_e32 v27, 0
	v_max_u32_e32 v6, v2, v3
	v_max3_u32 v6, v6, v4, v5
	s_mov_b32 s21, 0
.Lrs4_loop:
	v_cmp_lt_u32_e32 vcc, s21, v6
	s_cbranch_vccz .Lrs4_done

.Lw1b179:
	v_cmp_gt_u32_e64 s[22:23], s18, v8
	v_cmp_gt_u32_e64 s[24:25], s18, v10
	v_cmp_gt_u32_e64 s[26:27], s18, v12
	v_cmp_gt_u32_e64 s[28:29], s18, v14
	v_cndmask_b32_e64 v2, v7, v8, s[22:23]
	v_cndmask_b32_e64 v3, v7, v10, s[24:25]
	v_cndmask_b32_e64 v4, v7, v12, s[26:27]
	v_cndmask_b32_e64 v5, v7, v14, s[28:29]

.Lw1b180:
	ds_read_b32 v9, v2
	ds_read_b32 v11, v3
	ds_read_b32 v13, v4
	ds_read_b32 v15, v5
	s_waitcnt lgkmcnt(3)
	v_cmp_lt_u64_e64 s[22:23], v[8:9], v[16:17]
	s_waitcnt lgkmcnt(2)
	v_cmp_lt_u64_e64 s[24:25], v[10:11], v[18:19]

.Lw1b181:
	s_waitcnt lgkmcnt(1)
	v_cmp_lt_u64_e64 s[26:27], v[12:13], v[20:21]
	s_waitcnt lgkmcnt(0)
	v_cmp_lt_u64_e64 s[28:29], v[14:15], v[22:23]
	v_addc_co_u32_e64 v24, s[4:5], 0, v24, s[22:23]
	v_addc_co_u32_e64 v25, s[4:5], 0, v25, s[24:25]
	v_addc_co_u32_e64 v26, s[4:5], 0, v26, s[26:27]
	v_addc_co_u32_e64 v27, s[4:5], 0, v27, s[28:29]
	v_add_u32_e32 v8, 4, v8

.Lw1b182:
	v_add_u32_e32 v10, 4, v10
	v_add_u32_e32 v12, 4, v12
	v_add_u32_e32 v14, 4, v14
	s_add_i32 s21, s21, 1
	s_branch .Lrs4_loop
.Lrs4_done:
	v_and_b32_e32 v2, 0x1fffff, v17
	v_lshl_add_u32 v28, v24, 2, v28
	v_and_b32_e32 v3, 0x1fffff, v19
	v_lshl_add_u32 v29, v25, 2, v29
	v_and_b32_e32 v4, 0x1fffff, v21

.Lw1b183:
	v_lshl_add_u32 v30, v26, 2, v30
	v_and_b32_e32 v5, 0x1fffff, v23
	v_lshl_add_u32 v31, v27, 2, v31
	s_mov_b64 exec, s[10:11]
	ds_write_b32 v28, v2 offset:32768
	s_mov_b64 exec, s[12:13]
	ds_write_b32 v29, v3 offset:32768
	s_mov_b64 exec, s[14:15]
	ds_write_b32 v30, v4 offset:32768

.Lw1b184:
	s_mov_b64 exec, s[16:17]
	ds_write_b32 v31, v5 offset:32768
	s_mov_b64 exec, -1
.LBB1_382:
	s_sub_i32 s4, 0, s34
	s_and_b32 s4, s4, 3
	s_min_i32 s4, s4, s3
	v_cmp_gt_i32_e32 vcc, s4, v0
	s_waitcnt lgkmcnt(0)
	s_barrier
	s_and_saveexec_b64 s[6:7], vcc
	s_cbranch_execz .LBB1_384
	v_lshlrev_b32_e32 v1, 2, v0
	ds_read_b32 v2, v1 offset:32768
.Lw1t185:
	s_cbranch_execz .Lw1c185
.Lw1b185:
	s_waitcnt lgkmcnt(0)
	global_store_dword v1, v2, s[8:9]
.LBB1_384:
	s_or_b64 exec, exec, s[6:7]
	s_sub_i32 s14, s3, s4
	s_ashr_i32 s15, s14, 2
	v_cmp_gt_i32_e32 vcc, s15, v0
	s_and_saveexec_b64 s[6:7], vcc
	s_cbranch_execz .LBB1_387
	s_ashr_i32 s5, s4, 31
	s_lshl_b64 s[10:11], s[4:5], 2
	s_add_u32 s10, s8, s10
	v_lshlrev_b32_e32 v4, 4, v0
	s_addc_u32 s11, s9, s11
	v_mov_b32_e32 v5, 0

.Lw1b186:
	v_lshl_add_u32 v1, s4, 2, v4
	v_lshl_add_u64 v[2:3], s[10:11], 0, v[4:5]
	v_add_u32_e32 v1, 0x8000, v1
	s_mov_b64 s[10:11], 0
	s_mov_b64 s[12:13], 0x4000
	v_mov_b32_e32 v4, v0
.LBB1_386:
	ds_read2_b32 v[6:7], v1 offset1:1
	ds_read2_b32 v[8:9], v1 offset0:2 offset1:3
	v_add_u32_e32 v4, 0x400, v4
.Lw1t187:
	s_cbranch_execz .Lw1c187
.Lw1b187:
	v_cmp_le_i32_e32 vcc, s15, v4
	v_add_u32_e32 v1, 0x4000, v1
	s_or_b64 s[10:11], vcc, s[10:11]
	s_waitcnt lgkmcnt(0)
	global_store_dwordx4 v[2:3], v[6:9], off sc1
	v_lshl_add_u64 v[2:3], v[2:3], 0, s[12:13]
	s_andn2_b64 exec, exec, s[10:11]
	s_cbranch_execnz .LBB1_386
.LBB1_387:
	s_or_b64 exec, exec, s[6:7]
	s_and_b32 s6, s14, -4
	s_add_i32 s6, s6, s4
.Lw1t188:
	s_cbranch_execz .Lw1c188
.Lw1b188:
	s_sub_i32 s3, s3, s6
	v_cmp_gt_i32_e32 vcc, s3, v0
	s_and_saveexec_b64 s[4:5], vcc
	s_cbranch_execz .LBB1_389
	v_add_u32_e32 v2, s6, v0
	v_lshlrev_b32_e32 v1, 2, v2
	ds_read_b32 v1, v1 offset:32768
	v_ashrrev_i32_e32 v3, 31, v2
	v_lshl_add_u64 v[2:3], v[2:3], 2, s[8:9]
	s_waitcnt lgkmcnt(0)
	global_store_dword v[2:3], v1, off

.LBB1_390:
.LBB1_394:
.Lw1t189:
	s_cbranch_execz .Lw1c189

.Lmy_cvt1:
	s_waitcnt lgkmcnt(0)
	s_load_dwordx4 s[20:23], s[0:1], 0x28
	s_sub_i32 s3, s2, 392
	s_cmp_ge_u32 s3, 291
	s_cbranch_scc1 .Lmy_cvt1_end
	v_and_b32_e32 v1, 0x3c0, v0
	v_and_b32_e32 v2, 63, v0
	v_lshlrev_b32_e32 v3, 5, v1
	v_lshl_or_b32 v3, v2, 4, v3

.Lw1b190:
	v_and_b32_e32 v4, 1, v0
	v_lshrrev_b32_e32 v5, 1, v2
	v_lshl_or_b32 v5, v4, 5, v5
	v_add_u32_e32 v5, v5, v1
	v_lshlrev_b32_e32 v5, 4, v5
	v_cmp_eq_u32_e32 vcc, 0, v4
	s_waitcnt lgkmcnt(0)
	s_add_i32 s8, s3, 400
	s_lshl_b32 s9, s8, 10
	s_sub_i32 s9, 0x1869c0, s9
	v_cmp_ge_i32_e64 s[24:25], s9, v1

.Lw1b191:
	s_add_i32 s8, s3, 691
	s_lshl_b32 s9, s8, 10
	s_sub_i32 s9, 0x1869c0, s9
	v_cmp_ge_i32_e64 s[26:27], s9, v1
	s_add_i32 s8, s3, 982
	s_lshl_b32 s9, s8, 10
	s_sub_i32 s9, 0x1869c0, s9
	v_cmp_ge_i32_e64 s[28:29], s9, v1
	s_add_i32 s8, s3, 1273

.Lw1b192:
	s_lshl_b32 s9, s8, 10
	s_sub_i32 s9, 0x1869c0, s9
	v_cmp_ge_i32_e64 s[30:31], s9, v1
	s_add_i32 s8, s3, 400
	s_lshl_b32 s9, s8, 15
	s_add_u32 s10, s20, s9
	s_addc_u32 s11, s21, 0
	s_mov_b64 exec, s[24:25]
	global_load_dwordx4 v[8:11], v3, s[10:11] nt
	global_load_dwordx4 v[12:15], v3, s[10:11] offset:1024 nt

.Lw1b193:
	s_add_i32 s8, s3, 691
	s_lshl_b32 s9, s8, 15
	s_add_u32 s10, s20, s9
	s_addc_u32 s11, s21, 0
	s_mov_b64 exec, s[26:27]
	global_load_dwordx4 v[16:19], v3, s[10:11] nt
	global_load_dwordx4 v[20:23], v3, s[10:11] offset:1024 nt
	s_add_i32 s8, s3, 982
	s_lshl_b32 s9, s8, 15
	s_add_u32 s10, s20, s9
	s_addc_u32 s11, s21, 0

.Lw1b194:
	s_mov_b64 exec, s[28:29]
	global_load_dwordx4 v[24:27], v3, s[10:11] nt
	global_load_dwordx4 v[28:31], v3, s[10:11] offset:1024 nt
	s_add_i32 s8, s3, 1273
	s_lshl_b32 s9, s8, 15
	s_add_u32 s10, s20, s9
	s_addc_u32 s11, s21, 0
	s_mov_b64 exec, s[30:31]
	global_load_dwordx4 v[32:35], v3, s[10:11] nt
	global_load_dwordx4 v[36:39], v3, s[10:11] offset:1024 nt

.Lw1b195:
	s_waitcnt vmcnt(6)
	s_add_i32 s8, s3, 400
	s_lshl_b32 s9, s8, 14
	s_add_u32 s10, s22, s9
	s_addc_u32 s11, s23, 0
	s_mov_b64 exec, s[24:25]
	v_cvt_pk_f16_f32 v8, v8, v9
	v_cvt_pk_f16_f32 v9, v10, v11
	v_cvt_pk_f16_f32 v10, v12, v13
	v_cvt_pk_f16_f32 v11, v14, v15

.Lw1b196:
	v_cndmask_b32_e32 v12, v8, v10, vcc
	v_cndmask_b32_e32 v13, v9, v11, vcc
	s_nop 1
	v_mov_b32_dpp v12, v12 quad_perm:[1,0,3,2] row_mask:0xf bank_mask:0xf bound_ctrl:1
	v_mov_b32_dpp v13, v13 quad_perm:[1,0,3,2] row_mask:0xf bank_mask:0xf bound_ctrl:1
	v_cndmask_b32_e32 v8, v12, v8, vcc
	v_cndmask_b32_e32 v9, v13, v9, vcc
	v_cndmask_b32_e32 v10, v10, v12, vcc
	v_cndmask_b32_e32 v11, v11, v13, vcc
	global_store_dwordx4 v5, v[8:11], s[10:11] sc1
	s_waitcnt vmcnt(5)

.Lw1b197:
	s_add_i32 s8, s3, 691
	s_lshl_b32 s9, s8, 14
	s_add_u32 s10, s22, s9
	s_addc_u32 s11, s23, 0
	s_mov_b64 exec, s[26:27]
	v_cvt_pk_f16_f32 v16, v16, v17
	v_cvt_pk_f16_f32 v17, v18, v19
	v_cvt_pk_f16_f32 v18, v20, v21
	v_cvt_pk_f16_f32 v19, v22, v23
	v_cndmask_b32_e32 v20, v16, v18, vcc

.Lw1b198:
	v_cndmask_b32_e32 v21, v17, v19, vcc
	s_nop 1
	v_mov_b32_dpp v20, v20 quad_perm:[1,0,3,2] row_mask:0xf bank_mask:0xf bound_ctrl:1
	v_mov_b32_dpp v21, v21 quad_perm:[1,0,3,2] row_mask:0xf bank_mask:0xf bound_ctrl:1
	v_cndmask_b32_e32 v16, v20, v16, vcc
	v_cndmask_b32_e32 v17, v21, v17, vcc
	v_cndmask_b32_e32 v18, v18, v20, vcc
	v_cndmask_b32_e32 v19, v19, v21, vcc
	global_store_dwordx4 v5, v[16:19], s[10:11] sc1
	s_waitcnt vmcnt(4)
	s_add_i32 s8, s3, 982

.Lw1b199:
	s_lshl_b32 s9, s8, 14
	s_add_u32 s10, s22, s9
	s_addc_u32 s11, s23, 0
	s_mov_b64 exec, s[28:29]
	v_cvt_pk_f16_f32 v24, v24, v25
	v_cvt_pk_f16_f32 v25, v26, v27
	v_cvt_pk_f16_f32 v26, v28, v29
	v_cvt_pk_f16_f32 v27, v30, v31
	v_cndmask_b32_e32 v28, v24, v26, vcc
	v_cndmask_b32_e32 v29, v25, v27, vcc
	s_nop 1

.Lw1b200:
	v_mov_b32_dpp v28, v28 quad_perm:[1,0,3,2] row_mask:0xf bank_mask:0xf bound_ctrl:1
	v_mov_b32_dpp v29, v29 quad_perm:[1,0,3,2] row_mask:0xf bank_mask:0xf bound_ctrl:1
	v_cndmask_b32_e32 v24, v28, v24, vcc
	v_cndmask_b32_e32 v25, v29, v25, vcc
	v_cndmask_b32_e32 v26, v26, v28, vcc
	v_cndmask_b32_e32 v27, v27, v29, vcc
	global_store_dwordx4 v5, v[24:27], s[10:11] sc1
	s_waitcnt vmcnt(3)
	s_add_i32 s8, s3, 1273
	s_lshl_b32 s9, s8, 14
	s_add_u32 s10, s22, s9
	s_addc_u32 s11, s23, 0

.Lw1b201:
	s_mov_b64 exec, s[30:31]
	v_cvt_pk_f16_f32 v32, v32, v33
	v_cvt_pk_f16_f32 v33, v34, v35
	v_cvt_pk_f16_f32 v34, v36, v37
	v_cvt_pk_f16_f32 v35, v38, v39
	v_cndmask_b32_e32 v36, v32, v34, vcc
	v_cndmask_b32_e32 v37, v33, v35, vcc
	s_nop 1
	v_mov_b32_dpp v36, v36 quad_perm:[1,0,3,2] row_mask:0xf bank_mask:0xf bound_ctrl:1

.Lw1b202:
	v_mov_b32_dpp v37, v37 quad_perm:[1,0,3,2] row_mask:0xf bank_mask:0xf bound_ctrl:1
	v_cndmask_b32_e32 v32, v36, v32, vcc
	v_cndmask_b32_e32 v33, v37, v33, vcc
	v_cndmask_b32_e32 v34, v34, v36, vcc
	v_cndmask_b32_e32 v35, v35, v37, vcc
	global_store_dwordx4 v5, v[32:35], s[10:11] sc1

	.amdhsa_kernel _Z8k_bucketPKiS0_PKjPiS3_PK15HIP_vector_typeIfLj4EEPS4_IjLj4EE
		.amdhsa_group_segment_fixed_size 72624
		.amdhsa_private_segment_fixed_size 0
		.amdhsa_kernarg_size 56
		.amdhsa_user_sgpr_count 2
		.amdhsa_user_sgpr_dispatch_ptr 0
		.amdhsa_user_sgpr_queue_ptr 0
		.amdhsa_user_sgpr_kernarg_segment_ptr 1
		.amdhsa_user_sgpr_dispatch_id 0
		.amdhsa_user_sgpr_kernarg_preload_length 0
		.amdhsa_user_sgpr_kernarg_preload_offset 0
		.amdhsa_user_sgpr_private_segment_size 0
		.amdhsa_uses_dynamic_stack 0
		.amdhsa_enable_private_segment 0
		.amdhsa_system_sgpr_workgroup_id_x 1
		.amdhsa_system_sgpr_workgroup_id_y 0
		.amdhsa_system_sgpr_workgroup_id_z 0
		.amdhsa_system_sgpr_workgroup_info 0
		.amdhsa_system_vgpr_workitem_id 0
		.amdhsa_next_free_vgpr 40
		.amdhsa_next_free_sgpr 68
		.amdhsa_accum_offset 40
		.amdhsa_reserve_vcc 1
		.amdhsa_float_round_mode_32 0
		.amdhsa_float_round_mode_16_64 0
		.amdhsa_float_denorm_mode_32 3
		.amdhsa_float_denorm_mode_16_64 3
		.amdhsa_dx10_clamp 1
		.amdhsa_ieee_mode 1
		.amdhsa_fp16_overflow 0
		.amdhsa_tg_split 0
		.amdhsa_exception_fp_ieee_invalid_op 0
		.amdhsa_exception_fp_denorm_src 0
		.amdhsa_exception_fp_ieee_div_zero 0
		.amdhsa_exception_fp_ieee_overflow 0
		.amdhsa_exception_fp_ieee_underflow 0
		.amdhsa_exception_fp_ieee_inexact 0
		.amdhsa_exception_int_div_zero 0
	.end_amdhsa_kernel

_Z10k_layer_a2ILi0ELi13EEvPKDF16_PKiS3_PK15HIP_vector_typeIjLj4EES7_PKfS9_S9_S9_S9_S9_PDF16_Pf:
	s_load_dword s42, s[0:1], 0x0
	s_load_dword s43, s[0:1], 0x40
	v_lshrrev_b32_e32 v1, 6, v0
	s_nop 0
	v_readfirstlane_b32 s41, v1
	s_movk_i32 s40, 0x5aa5
	s_mov_b64 exec, 0
	s_cmpk_lt_u32 s41, 6
	s_cbranch_scc1 .Lw2s0d0_13
	s_cmpk_lt_u32 s41, 9
	s_cbranch_scc1 .Lw2s0d6_13
	s_cmpk_lt_u32 s41, 11
	s_cbranch_scc1 .Lw2s0d9_13
	s_cmpk_lt_u32 s41, 12
	s_cbranch_scc1 .Lw2s0d11_13
	s_branch .Lw2t12

.Lw2b0:
	s_load_dwordx4 s[4:7], s[0:1], 0x28
	s_load_dwordx2 s[10:11], s[0:1], 0x38
	v_lshlrev_b32_e32 v2, 4, v0
	v_mov_b32_e32 v3, 0
	s_waitcnt lgkmcnt(0)
	v_lshl_add_u64 v[4:5], s[8:9], 0, v[2:3]
	s_movk_i32 s3, 0x3000
	v_add_co_u32_e32 v14, vcc, s3, v4
	s_movk_i32 s3, 0x6000
	s_nop 0

.Lw2b1:
	v_addc_co_u32_e32 v15, vcc, 0, v5, vcc
	v_add_co_u32_e32 v16, vcc, s3, v4
	v_min_u32_e32 v1, 0x7f, v0
	s_nop 0
	v_addc_co_u32_e32 v17, vcc, 0, v5, vcc
	global_load_dwordx4 v[6:9], v[14:15], off offset:1024
	global_load_dwordx4 v[10:13], v[16:17], off offset:2048
	v_add_co_u32_e32 v22, vcc, 0x9000, v4
	v_lshlrev_b32_e32 v24, 2, v1
	s_nop 0
	v_addc_co_u32_e32 v23, vcc, 0, v5, vcc

.Lw2b2:
	global_load_dwordx4 v[14:17], v2, s[8:9]
	global_load_dwordx4 v[18:21], v[22:23], off offset:3072
	global_load_dword v4, v24, s[4:5]
	global_load_dword v5, v24, s[4:5] offset:512
	global_load_dword v1, v24, s[6:7]
	global_load_dword v3, v24, s[10:11]
	s_movk_i32 s4, 0x300
	v_readfirstlane_b32 s3, v0
	v_cmp_gt_u32_e32 vcc, s4, v0

.Lw2b3:
	s_waitcnt vmcnt(5)
	ds_write_b128 v2, v[14:17]
	ds_write_b128 v2, v[6:9] offset:13312
	ds_write_b128 v2, v[10:13] offset:26624
	s_waitcnt vmcnt(4)
	ds_write_b128 v2, v[18:21] offset:39936
	s_and_saveexec_b64 s[4:5], vcc
	s_cbranch_execz .LBB2_2
	v_add_u32_e32 v6, 0xd00, v0
	v_min_u32_e32 v6, 0xfff, v6

.Lw2b4:
	v_lshlrev_b32_e32 v6, 4, v6
	global_load_dwordx4 v[6:9], v6, s[8:9]
	s_waitcnt vmcnt(0)
	ds_write_b128 v2, v[6:9] offset:53248
.LBB2_2:
	s_or_b64 exec, exec, s[4:5]
	s_movk_i32 s4, 0x80
	v_cmp_gt_u32_e32 vcc, s4, v0
	s_and_saveexec_b64 s[4:5], vcc
	s_cbranch_execz .LBB2_4
	s_waitcnt vmcnt(2)
	v_add_f32_e32 v2, v4, v5
	v_mov_b32_e32 v4, 0x1dd00
.Lw2t5:
	s_cbranch_execz .Lw2c5
.Lw2b5:
	v_lshl_add_u32 v4, v0, 2, v4
	s_waitcnt vmcnt(1)
	ds_write2st64_b32 v4, v2, v1 offset1:2
	s_waitcnt vmcnt(0)
	ds_write_b32 v4, v3 offset:1024
.LBB2_4:
	s_or_b64 exec, exec, s[4:5]
	s_load_dwordx4 s[8:11], s[0:1], 0x0
	s_load_dwordx2 s[6:7], s[0:1], 0x10
	s_load_dwordx2 s[14:15], s[0:1], 0x58
.Lw2t6:
	s_cbranch_execz .Lw2c6
.Lw2b6:
	s_mov_b32 s13, 0
	v_cmp_eq_u32_e32 vcc, 0, v0
	s_and_saveexec_b64 s[4:5], vcc
	s_cbranch_execz .LBB2_6
	s_waitcnt vmcnt(1)
	v_mov_b32_e32 v1, 0
	v_mov_b32_e32 v2, 0x1e900
	ds_write_b32 v2, v1
.LBB2_6:
	s_or_b64 exec, exec, s[4:5]
	s_waitcnt vmcnt(1)
	v_bfe_u32 v1, v0, 4, 2
.Lw2t7:
	s_cbranch_execz .Lw2c7
.Lw2b7:
	v_bfe_u32 v2, v0, 2, 2
	v_cmp_eq_u32_e32 vcc, v1, v2
	v_and_b32_e32 v2, 3, v0
	v_cmp_eq_u32_e64 s[4:5], 0, v2
	s_waitcnt vmcnt(0)
	v_mov_b32_e32 v3, 0x3c00
	s_and_b64 s[4:5], vcc, s[4:5]
	v_cndmask_b32_e64 v4, 0, v3, s[4:5]
	v_cmp_eq_u32_e64 s[4:5], 1, v2
	s_and_b64 s[4:5], vcc, s[4:5]

.Lw2b8:
	s_lshr_b32 s12, s3, 6
	v_cndmask_b32_e64 v5, 0, v3, s[4:5]
	v_cmp_eq_u32_e64 s[4:5], 2, v2
	s_and_b64 s[4:5], vcc, s[4:5]
	v_and_b32_e32 v77, 63, v0
	v_cndmask_b32_e64 v6, 0, v3, s[4:5]
	v_cmp_eq_u32_e64 s[4:5], 3, v2
	s_and_b64 vcc, vcc, s[4:5]
	v_cndmask_b32_e32 v2, 0, v3, vcc
	v_pack_b32_f16 v73, v6, v2

.Lw2b9:
	v_lshlrev_b32_e32 v2, 2, v0
	s_waitcnt lgkmcnt(0)
	s_barrier
	v_and_b32_e32 v82, 15, v0
	v_pack_b32_f16 v72, v4, v5
	s_load_dword s3, s[0:1], 0x68
	v_and_b32_e32 v84, 0xc0, v2
	s_mul_i32 s0, s12, 0x1100
	v_and_b32_e32 v2, 48, v0
	v_bfe_u32 v5, v0, 2, 4

.Lw2b10:
	v_lshlrev_b32_e32 v0, 6, v0
	s_add_i32 s4, s0, 0x10000
	v_mul_u32_u24_e32 v5, 0x110, v5
	v_and_b32_e32 v0, 0xc0, v0
	v_mov_b32_e32 v3, 0
	s_movk_i32 s20, 0x110
	v_add3_u32 v85, s4, v5, v0
	v_mov_b32_e32 v0, s4
	v_lshlrev_b32_e32 v4, 7, v1
	v_mad_u32_u24 v5, v82, s20, v0

.Lw2b11:
	v_lshlrev_b32_e32 v86, 5, v1
	v_lshlrev_b32_e32 v0, 6, v1
	v_mov_b32_e32 v1, v3
	v_lshlrev_b32_e32 v83, 4, v82
	v_lshl_add_u64 v[78:79], s[14:15], 0, v[0:1]
	v_mbcnt_lo_u32_b32 v0, -1, 0
	v_cmp_eq_u32_e64 s[0:1], 0, v77
	v_lshl_add_u64 v[74:75], s[10:11], 0, v[2:3]
	v_or_b32_e32 v76, s4, v83
	v_or_b32_e32 v87, 28, v84
	v_or_b32_e32 v88, 32, v84

.Lw2b12:
	v_or_b32_e32 v89, 36, v84
	v_or_b32_e32 v90, 40, v84
	v_or_b32_e32 v91, 44, v84
	v_or_b32_e32 v92, 48, v84
	v_or_b32_e32 v93, 52, v84
	v_or_b32_e32 v94, 56, v84
	v_or_b32_e32 v95, 60, v84
	v_mov_b32_e32 v96, 0x1e900
	v_add_u32_e32 v97, 0x1dd00, v4
	s_mov_b32 s21, 0x1ffff00
	v_add_u32_e32 v98, v5, v2
	v_lshrrev_b32_e32 v125, 1, v86

.Lw2b13:
	v_lshrrev_b32_e32 v126, 5, v86
	v_add3_u32 v125, v98, v86, v125
	v_mad_u32_u24 v126, v126, s20, v76
	v_mov_b32_e32 v99, 0x3727c5ac
	s_mov_b32 s22, 0x800000
	v_mov_b32_e32 v100, 0xc0135761
	v_mbcnt_hi_u32_b32 v101, -1, v0
	v_mov_b32_e32 v102, 0x1dd00

.LBB2_7:
	v_mov_b32_e32 v32, v28
	v_mov_b32_e32 v33, v24
	v_mov_b32_e32 v34, v29
	v_mov_b32_e32 v35, v25
	v_pk_add_f32 v[32:33], v[32:33], v[34:35]
	v_mov_b32_e32 v34, v30
	v_mov_b32_e32 v35, v26
	v_mov_b32_e32 v36, v31
	v_mov_b32_e32 v37, v27
	v_pk_add_f32 v[34:35], v[34:35], v[36:37]
	v_mov_b32_e32 v36, v20
	v_pk_add_f32 v[32:33], v[32:33], v[34:35]

.Lw2b15:
	v_mov_b32_e32 v34, v21
	v_mov_b32_e32 v35, v22
	v_mov_b32_e32 v37, v23
	v_pk_add_f32 v[34:35], v[34:35], v[36:37]
	v_add_f32_e32 v32, 0, v32
	v_pk_add_f32 v[34:35], v[34:35], v[34:35] op_sel:[0,1] op_sel_hi:[1,0]
	v_add_f32_e32 v32, v32, v33
	v_add_f32_e32 v36, v16, v17
	v_add_f32_e32 v38, v18, v19
	v_mov_b32_e32 v33, v12
	v_mov_b32_e32 v35, v13
	v_mov_b32_e32 v37, v14

.Lw2b16:
	v_mov_b32_e32 v39, v15
	v_pk_add_f32 v[32:33], v[32:33], v[34:35]
	v_pk_add_f32 v[34:35], v[36:37], v[38:39]
	v_mov_b32_e32 v36, v8
	v_pk_add_f32 v[32:33], v[32:33], v[34:35]
	v_mov_b32_e32 v34, v9
	v_mov_b32_e32 v35, v10
	v_mov_b32_e32 v37, v11
	v_pk_add_f32 v[34:35], v[34:35], v[36:37]
	v_pk_add_f32 v[32:33], v[32:33], v[32:33] op_sel:[0,1] op_sel_hi:[1,0]

.Lw2b17:
	v_pk_add_f32 v[34:35], v[34:35], v[34:35] op_sel:[0,1] op_sel_hi:[1,0]
	v_add_f32_e32 v36, v4, v5
	v_add_f32_e32 v38, v6, v7
	v_mov_b32_e32 v33, v0
	v_mov_b32_e32 v35, v1
	v_mov_b32_e32 v37, v2
	v_mov_b32_e32 v39, v3
	v_pk_add_f32 v[32:33], v[32:33], v[34:35]
	v_pk_add_f32 v[34:35], v[36:37], v[38:39]
	s_nop 0
	v_pk_add_f32 v[32:33], v[32:33], v[34:35]

.Lw2b18:
	v_and_b32_e32 v34, 64, v101
	v_add_f32_e32 v32, v32, v33
	v_xor_b32_e32 v33, 16, v101
	v_add_u32_e32 v34, 64, v34
	v_cmp_lt_i32_e32 vcc, v33, v34
	s_nop 1
	v_cndmask_b32_e32 v33, v101, v33, vcc
	v_lshlrev_b32_e32 v42, 2, v33
	ds_bpermute_b32 v33, v42, v32
	s_waitcnt lgkmcnt(0)
	v_add_f32_e32 v32, v32, v33
	v_xor_b32_e32 v33, 32, v101
	v_cmp_lt_i32_e32 vcc, v33, v34
	s_nop 1

.Lw2b19:
	v_cndmask_b32_e32 v33, v101, v33, vcc
	v_lshlrev_b32_e32 v43, 2, v33
	ds_bpermute_b32 v33, v43, v32
	s_waitcnt lgkmcnt(0)
	v_add_f32_e32 v44, v32, v33
	v_fmamk_f32 v29, v44, 0xbc000000, v29
	v_fmamk_f32 v25, v44, 0xbc000000, v25
	v_fmamk_f32 v41, v44, 0xbc000000, v31
	v_fmamk_f32 v40, v44, 0xbc000000, v30
	v_fmac_f32_e32 v28, 0xbc000000, v44

.Lw2b20:
	v_fmamk_f32 v39, v44, 0xbc000000, v27
	v_fmac_f32_e32 v24, 0xbc000000, v44
	v_mov_b32_e32 v30, v29
	v_mov_b32_e32 v31, v25
	v_fmamk_f32 v38, v44, 0xbc000000, v26
	v_mov_b32_e32 v26, v28
	v_mov_b32_e32 v27, v24
	v_pk_mul_f32 v[30:31], v[30:31], v[30:31]
	v_mov_b32_e32 v32, v41
	v_mov_b32_e32 v33, v39

.Lw2b21:
	v_pk_fma_f32 v[26:27], v[26:27], v[26:27], v[30:31]
	v_mov_b32_e32 v30, v40
	v_mov_b32_e32 v31, v38
	v_pk_mul_f32 v[32:33], v[32:33], v[32:33]
	v_fmamk_f32 v37, v44, 0xbc000000, v21
	v_pk_fma_f32 v[30:31], v[30:31], v[30:31], v[32:33]
	v_fmamk_f32 v36, v44, 0xbc000000, v20
	v_fmamk_f32 v23, v44, 0xbc000000, v23
	v_fmac_f32_e32 v22, 0xbc000000, v44

.Lw2b22:
	v_pk_add_f32 v[26:27], v[26:27], v[30:31]
	v_pk_mul_f32 v[20:21], v[22:23], v[22:23]
	v_pk_mul_f32 v[30:31], v[36:37], v[36:37]
	v_fmac_f32_e32 v12, 0xbc000000, v44
	v_pk_mov_b32 v[32:33], v[30:31], v[20:21] op_sel:[1,0]
	v_mov_b32_e32 v31, v21
	v_pk_add_f32 v[20:21], v[32:33], v[30:31]
	v_fmamk_f32 v34, v44, 0xbc000000, v18

.Lw2b23:
	v_fmamk_f32 v31, v44, 0xbc000000, v15
	v_fmamk_f32 v30, v44, 0xbc000000, v14
	v_fmamk_f32 v13, v44, 0xbc000000, v13
	v_mul_f32_e32 v18, v12, v12
	v_pk_add_f32 v[14:15], v[26:27], v[26:27] op_sel:[0,1] op_sel_hi:[1,0]
	v_fmamk_f32 v35, v44, 0xbc000000, v19
	v_mul_f32_e32 v32, v13, v13
	v_mov_b32_e32 v15, v18
	v_pk_add_f32 v[18:19], v[20:21], v[20:21] op_sel:[0,1] op_sel_hi:[1,0]

.Lw2b24:
	v_fmamk_f32 v17, v44, 0xbc000000, v17
	v_mov_b32_e32 v19, v32
	v_fmac_f32_e32 v16, 0xbc000000, v44
	v_pk_add_f32 v[14:15], v[14:15], v[18:19]
	v_mul_f32_e32 v18, v17, v17
	v_mul_f32_e32 v20, v35, v35
	v_mul_f32_e32 v33, v30, v30
	v_mul_f32_e32 v45, v31, v31
	v_pk_fma_f32 v[18:19], v[16:17], v[16:17], v[18:19] op_sel_hi:[1,1,0]
	v_pk_fma_f32 v[20:21], v[34:35], v[34:35], v[20:21] op_sel_hi:[1,1,0]

.Lw2b25:
	v_mov_b32_e32 v19, v33
	v_mov_b32_e32 v21, v45
	v_pk_add_f32 v[18:19], v[18:19], v[20:21]
	v_fmamk_f32 v33, v44, 0xbc000000, v9
	v_fmamk_f32 v32, v44, 0xbc000000, v8
	v_fmamk_f32 v11, v44, 0xbc000000, v11
	v_fmac_f32_e32 v10, 0xbc000000, v44
	v_pk_add_f32 v[14:15], v[14:15], v[18:19]

.Lw2b26:
	v_pk_mul_f32 v[8:9], v[10:11], v[10:11]
	v_pk_mul_f32 v[18:19], v[32:33], v[32:33]
	v_fmamk_f32 v1, v44, 0xbc000000, v1
	v_pk_mov_b32 v[20:21], v[18:19], v[8:9] op_sel:[1,0]
	v_mov_b32_e32 v19, v9
	v_pk_add_f32 v[8:9], v[20:21], v[18:19]
	v_fmac_f32_e32 v0, 0xbc000000, v44
	v_fmamk_f32 v19, v44, 0xbc000000, v7

.Lw2b27:
	v_fmamk_f32 v18, v44, 0xbc000000, v6
	v_mul_f32_e32 v20, v0, v0
	v_mul_f32_e32 v21, v1, v1
	v_pk_add_f32 v[6:7], v[14:15], v[14:15] op_sel:[0,1] op_sel_hi:[1,0]
	v_pk_add_f32 v[8:9], v[8:9], v[8:9] op_sel:[0,1] op_sel_hi:[1,0]
	v_fmamk_f32 v5, v44, 0xbc000000, v5
	v_mov_b32_e32 v7, v20
	v_mov_b32_e32 v9, v21
	v_fmac_f32_e32 v4, 0xbc000000, v44
	v_fmamk_f32 v3, v44, 0xbc000000, v3

.Lw2b28:
	v_fmamk_f32 v2, v44, 0xbc000000, v2
	v_pk_add_f32 v[6:7], v[6:7], v[8:9]
	v_mul_f32_e32 v8, v5, v5
	v_mul_f32_e32 v14, v19, v19
	v_mul_f32_e32 v26, v2, v2
	v_mul_f32_e32 v27, v3, v3
	v_pk_fma_f32 v[8:9], v[4:5], v[4:5], v[8:9] op_sel_hi:[1,1,0]
	v_pk_fma_f32 v[14:15], v[18:19], v[18:19], v[14:15] op_sel_hi:[1,1,0]
	v_mov_b32_e32 v9, v26
	v_mov_b32_e32 v15, v27

.Lw2b29:
	v_pk_add_f32 v[8:9], v[8:9], v[14:15]
	s_nop 0
	v_pk_add_f32 v[6:7], v[6:7], v[8:9]
	s_nop 0
	v_add_f32_e32 v6, v6, v7
	ds_bpermute_b32 v7, v42, v6
	s_waitcnt lgkmcnt(0)
	v_add_f32_e32 v6, v6, v7
	ds_bpermute_b32 v7, v43, v6
	s_waitcnt lgkmcnt(0)
	v_add_f32_e32 v6, v6, v7

.Lw2b30:
	v_fmamk_f32 v6, v6, 0x3c000000, v99
	v_mul_f32_e32 v7, 0x4b800000, v6
	v_cmp_gt_f32_e32 vcc, s22, v6
	s_nop 1
	v_cndmask_b32_e32 v6, v6, v7, vcc
	v_rsq_f32_e32 v14, v6
	ds_read_b128 v[6:9], v97 offset:512
	ds_read_b128 v[42:45], v97 offset:528
	ds_read_b128 v[46:49], v97 offset:1024
	ds_read_b128 v[50:53], v97 offset:1040

.Lw2b31:
	v_mul_f32_e32 v15, 0x45800000, v14
	v_cndmask_b32_e32 v20, v14, v15, vcc
	v_pk_mul_f32 v[26:27], v[20:21], v[28:29] op_sel_hi:[0,1]
	s_waitcnt lgkmcnt(1)
	v_pk_fma_f32 v[6:7], v[6:7], v[26:27], v[46:47]
	v_or_b32_e32 v14, s4, v82
	v_pk_mul_f32 v[26:27], v[6:7], v[6:7]
	v_ashrrev_i32_e32 v15, 31, v14
	v_fmamk_f32 v21, v26, 0xbdd2d3e8, v100

.Lw2b32:
	v_mul_f32_e32 v21, v6, v21
	v_fmamk_f32 v26, v27, 0xbdd2d3e8, v100
	v_exp_f32_e32 v21, v21
	v_mul_f32_e32 v26, v7, v26
	v_exp_f32_e32 v26, v26
	v_lshlrev_b64 v[14:15], 8, v[14:15]
	v_add_f32_e32 v21, 1.0, v21
	v_rcp_f32_e32 v28, v21
	v_add_f32_e32 v21, 1.0, v26
	v_pk_mul_f32 v[26:27], v[20:21], v[40:41] op_sel_hi:[0,1]
	v_pk_fma_f32 v[8:9], v[8:9], v[26:27], v[48:49]

.Lw2b33:
	v_rcp_f32_e32 v29, v21
	v_pk_mul_f32 v[40:41], v[8:9], v[8:9]
	v_mad_u32_u24 v104, v86, 6, v83
	s_lshl_b32 s12, s4, 8
	v_mov_b32_e32 v105, 0
	v_add_u32_e32 v104, s12, v104
	s_nop 0
	v_lshl_add_u64 v[104:105], v[78:79], 0, v[104:105]
	v_fmamk_f32 v21, v40, 0xbdd2d3e8, v100
	v_mul_f32_e32 v21, v8, v21
	v_exp_f32_e32 v21, v21

.Lw2b55:
	v_pk_mul_f32 v[24:25], v[28:29], v[30:31]
	s_nop 0
	v_cvt_pk_f16_f32 v23, v24, v25
	v_cvt_pk_f16_f32 v24, v12, v13
	v_pk_mul_f32 v[4:5], v[20:21], v[4:5] op_sel_hi:[0,1]
	s_waitcnt lgkmcnt(0)
	v_pk_fma_f32 v[4:5], v[40:41], v[4:5], v[48:49]
	ds_write_b128 v125, v[6:9]
	v_pk_mul_f32 v[12:13], v[4:5], v[4:5]

.Lw2b58:
	v_cvt_pk_f16_f32 v4, v4, v5
	v_pk_mul_f32 v[8:9], v[6:7], v[6:7]
	s_mov_b64 s[4:5], 0
	v_fmamk_f32 v8, v8, 0xbdd2d3e8, v100
	v_mul_f32_e32 v8, v6, v8
	v_fmamk_f32 v9, v9, 0xbdd2d3e8, v100
	v_exp_f32_e32 v8, v8
	v_mul_f32_e32 v9, v7, v9
	v_exp_f32_e32 v9, v9
	ds_write_b128 v125, v[14:17] offset:16

.Lw2b60:
	v_add_f32_e32 v5, 1.0, v5
	v_rcp_f32_e32 v8, v5
	v_add_f32_e32 v5, 1.0, v10
	v_pk_mul_f32 v[10:11], v[2:3], v[2:3]
	ds_write_b128 v125, v[22:25] offset:32
	v_fmamk_f32 v9, v10, 0xbdd2d3e8, v100
	v_mul_f32_e32 v9, v2, v9
	v_exp_f32_e32 v10, v9
	v_fmamk_f32 v9, v11, 0xbdd2d3e8, v100
	v_mul_f32_e32 v9, v3, v9
	v_exp_f32_e32 v11, v9

.Lw2b62:
	ds_write_b128 v125, v[4:7] offset:48
	ds_read_b128 v[4:7], v126
	ds_read_b128 v[8:11], v126 offset:1088
	ds_read_b128 v[12:15], v126 offset:2176
	ds_read_b128 v[16:19], v126 offset:3264
	s_waitcnt lgkmcnt(3)
	global_store_dwordx4 v[104:105], v[4:7], off
	s_waitcnt lgkmcnt(2)

.Lw2b63:
	global_store_dwordx4 v[104:105], v[8:11], off offset:1024
	s_waitcnt lgkmcnt(1)
	global_store_dwordx4 v[104:105], v[12:15], off offset:2048
	s_waitcnt lgkmcnt(0)
	global_store_dwordx4 v[104:105], v[16:19], off offset:3072

.LBB2_9:
	v_mov_b32_e32 v0, 0
	s_and_saveexec_b64 s[4:5], s[0:1]
	s_cbranch_execz .LBB2_13
	s_mov_b64 s[14:15], exec
	v_mbcnt_lo_u32_b32 v0, s14, 0
.Lw2t64:
	s_cbranch_execz .Lw2c64
.Lw2b64:
	v_mbcnt_hi_u32_b32 v0, s15, v0
	v_cmp_eq_u32_e32 vcc, 0, v0
	s_and_saveexec_b64 s[10:11], vcc
	s_bcnt1_i32_b64 s12, s[14:15]
	v_mov_b32_e32 v1, s12
	ds_add_rtn_u32 v1, v96, v1
	s_or_b64 exec, exec, s[10:11]
	s_waitcnt lgkmcnt(0)
	v_readfirstlane_b32 s10, v1
	s_nop 1
	v_add_u32_e32 v0, s10, v0

.Lw2b65:
	v_readfirstlane_b32 s4, v0
	s_waitcnt lgkmcnt(0)
	s_mul_i32 s10, s4, s3
	s_add_i32 s10, s10, s2
	s_cmpk_gt_i32 s10, 0x1869
	s_mov_b64 s[4:5], -1
	s_cbranch_scc1 .LBB2_8
	ds_read_b128 v[28:31], v97
	ds_read_b128 v[24:27], v97 offset:16
	ds_read_b128 v[20:23], v97 offset:32
	ds_read_b128 v[16:19], v97 offset:48

.Lw2b66:
	ds_read_b128 v[12:15], v97 offset:64
	ds_read_b128 v[8:11], v97 offset:80
	ds_read_b128 v[4:7], v97 offset:96
	ds_read_b128 v[0:3], v97 offset:112
	s_lshl_b32 s4, s10, 4
	s_ashr_i32 s5, s4, 31
	v_lshl_add_u64 v[80:81], s[4:5], 2, v[74:75]
	s_mov_b32 s5, 0
	s_mov_b64 s[18:19], -1
	s_branch .LBB2_16

.Lw2b67:
	s_or_b64 exec, exec, s[14:15]
	v_mov_b32_e32 v48, v77
	ds_read_b128 v[32:35], v98
	ds_read_b128 v[36:39], v98 offset:64
	ds_read_b128 v[40:43], v98 offset:128
	ds_read_b128 v[44:47], v98 offset:192
	s_nop 0
	v_lshlrev_b32_e32 v48, 4, v48
	v_lshl_add_u32 v103, s5, 15, v48
	ds_read_b128 v[48:51], v103

.Lw2b68:
	ds_read_b128 v[52:55], v103 offset:1024
	ds_read_b128 v[56:59], v103 offset:2048
	ds_read_b128 v[60:63], v103 offset:3072
	ds_read_b128 v[64:67], v103 offset:4096
	ds_read_b128 v[68:71], v103 offset:5120
	ds_read_b128 v[104:107], v103 offset:6144
	ds_read_b128 v[108:111], v103 offset:7168

.Lw2b69:
	s_waitcnt lgkmcnt(7)
	v_mfma_f32_16x16x32_f16 v[28:31], v[48:51], v[32:35], v[28:31]
	s_waitcnt lgkmcnt(6)
	v_mfma_f32_16x16x32_f16 v[24:27], v[52:55], v[32:35], v[24:27]
	s_waitcnt lgkmcnt(5)
	v_mfma_f32_16x16x32_f16 v[20:23], v[56:59], v[32:35], v[20:23]
	s_waitcnt lgkmcnt(4)
	v_mfma_f32_16x16x32_f16 v[16:19], v[60:63], v[32:35], v[16:19]
	ds_read_b128 v[48:51], v103 offset:8192
	ds_read_b128 v[52:55], v103 offset:9216

.Lw2b70:
	ds_read_b128 v[56:59], v103 offset:10240
	ds_read_b128 v[60:63], v103 offset:11264
	s_waitcnt lgkmcnt(7)
	v_mfma_f32_16x16x32_f16 v[12:15], v[64:67], v[32:35], v[12:15]
	s_waitcnt lgkmcnt(6)
	v_mfma_f32_16x16x32_f16 v[8:11], v[68:71], v[32:35], v[8:11]
	s_waitcnt lgkmcnt(5)
	v_mfma_f32_16x16x32_f16 v[4:7], v[104:107], v[32:35], v[4:7]
	s_waitcnt lgkmcnt(4)

.Lw2b71:
	v_mfma_f32_16x16x32_f16 v[0:3], v[108:111], v[32:35], v[0:3]
	ds_read_b128 v[32:35], v103 offset:12288
	ds_read_b128 v[64:67], v103 offset:13312
	ds_read_b128 v[68:71], v103 offset:14336
	ds_read_b128 v[104:107], v103 offset:15360
	s_waitcnt lgkmcnt(7)
	v_mfma_f32_16x16x32_f16 v[28:31], v[48:51], v[36:39], v[28:31]
	s_waitcnt lgkmcnt(6)
	v_mfma_f32_16x16x32_f16 v[24:27], v[52:55], v[36:39], v[24:27]

.Lw2b72:
	s_waitcnt lgkmcnt(5)
	v_mfma_f32_16x16x32_f16 v[20:23], v[56:59], v[36:39], v[20:23]
	s_waitcnt lgkmcnt(4)
	v_mfma_f32_16x16x32_f16 v[16:19], v[60:63], v[36:39], v[16:19]
	ds_read_b128 v[48:51], v103 offset:16384
	ds_read_b128 v[52:55], v103 offset:17408
	ds_read_b128 v[56:59], v103 offset:18432
	ds_read_b128 v[60:63], v103 offset:19456

.Lw2b73:
	s_waitcnt lgkmcnt(7)
	v_mfma_f32_16x16x32_f16 v[12:15], v[32:35], v[36:39], v[12:15]
	s_waitcnt lgkmcnt(6)
	v_mfma_f32_16x16x32_f16 v[8:11], v[64:67], v[36:39], v[8:11]
	s_waitcnt lgkmcnt(5)
	v_mfma_f32_16x16x32_f16 v[4:7], v[68:71], v[36:39], v[4:7]
	s_waitcnt lgkmcnt(4)
	v_mfma_f32_16x16x32_f16 v[0:3], v[104:107], v[36:39], v[0:3]
	ds_read_b128 v[32:35], v103 offset:20480
	ds_read_b128 v[36:39], v103 offset:21504

.Lw2b74:
	ds_read_b128 v[64:67], v103 offset:22528
	ds_read_b128 v[68:71], v103 offset:23552
	s_waitcnt lgkmcnt(7)
	v_mfma_f32_16x16x32_f16 v[28:31], v[48:51], v[40:43], v[28:31]
	s_waitcnt lgkmcnt(6)
	v_mfma_f32_16x16x32_f16 v[24:27], v[52:55], v[40:43], v[24:27]
	s_waitcnt lgkmcnt(5)
	v_mfma_f32_16x16x32_f16 v[20:23], v[56:59], v[40:43], v[20:23]
	s_waitcnt lgkmcnt(4)

.Lw2b75:
	v_mfma_f32_16x16x32_f16 v[16:19], v[60:63], v[40:43], v[16:19]
	ds_read_b128 v[48:51], v103 offset:24576
	ds_read_b128 v[52:55], v103 offset:25600
	ds_read_b128 v[56:59], v103 offset:26624
	ds_read_b128 v[60:63], v103 offset:27648
	s_waitcnt lgkmcnt(7)
	v_mfma_f32_16x16x32_f16 v[12:15], v[32:35], v[40:43], v[12:15]
	s_waitcnt lgkmcnt(6)
	v_mfma_f32_16x16x32_f16 v[8:11], v[36:39], v[40:43], v[8:11]

.Lw2b76:
	s_waitcnt lgkmcnt(5)
	v_mfma_f32_16x16x32_f16 v[4:7], v[64:67], v[40:43], v[4:7]
	s_waitcnt lgkmcnt(4)
	v_mfma_f32_16x16x32_f16 v[0:3], v[68:71], v[40:43], v[0:3]
	ds_read_b128 v[32:35], v103 offset:28672
	ds_read_b128 v[36:39], v103 offset:29696
	ds_read_b128 v[40:43], v103 offset:30720
	ds_read_b128 v[64:67], v103 offset:31744

.Lw2b77:
	s_waitcnt lgkmcnt(7)
	v_mfma_f32_16x16x32_f16 v[28:31], v[48:51], v[44:47], v[28:31]
	s_waitcnt lgkmcnt(6)
	v_mfma_f32_16x16x32_f16 v[24:27], v[52:55], v[44:47], v[24:27]
	s_waitcnt lgkmcnt(5)
	v_mfma_f32_16x16x32_f16 v[20:23], v[56:59], v[44:47], v[20:23]
	s_waitcnt lgkmcnt(4)
	v_mfma_f32_16x16x32_f16 v[16:19], v[60:63], v[44:47], v[16:19]
	s_waitcnt lgkmcnt(3)
	v_mfma_f32_16x16x32_f16 v[12:15], v[32:35], v[44:47], v[12:15]

.Lw2b78:
	s_waitcnt lgkmcnt(2)
	v_mfma_f32_16x16x32_f16 v[8:11], v[36:39], v[44:47], v[8:11]
	s_waitcnt lgkmcnt(1)
	v_mfma_f32_16x16x32_f16 v[4:7], v[40:43], v[44:47], v[4:7]
	s_waitcnt lgkmcnt(0)
	v_mfma_f32_16x16x32_f16 v[0:3], v[64:67], v[44:47], v[0:3]
	s_mov_b32 s5, 1
	s_mov_b64 s[18:19], 0
	s_and_b64 vcc, exec, s[10:11]
	s_cbranch_vccnz .LBB2_7
.LBB2_16:
	s_mul_i32 s12, s5, 0x186a1
.Lw2t79:
	s_cbranch_execz .Lw2c79
.Lw2b79:
	v_lshl_add_u64 v[32:33], s[12:13], 2, v[80:81]
	global_load_dword v113, v[32:33], off
	global_load_dword v103, v[32:33], off offset:16
	s_mov_b32 s14, s13
	s_mov_b32 s15, s13
	s_mul_i32 s12, s5, 0xc3500
	s_lshl_b64 s[10:11], s[12:13], 2
	s_mov_b32 s12, s13
	v_mov_b64_e32 v[34:35], s[14:15]
	v_mov_b64_e32 v[32:33], s[12:13]
	s_add_u32 s16, s6, s10
	ds_write_b128 v85, v[32:35]
	ds_write_b128 v85, v[32:35] offset:16
	ds_write_b128 v85, v[32:35] offset:32
	ds_write_b128 v85, v[32:35] offset:48
	s_addc_u32 s17, s7, s11

.Lw2b80:
	v_mov_b32_e32 v116, 0x3f86a0
	s_waitcnt vmcnt(1)
	v_add_u32_e32 v32, v113, v82
	s_waitcnt vmcnt(0)
	v_cmp_lt_i32_e32 vcc, v32, v103
.Lw2t81:
	s_cbranch_execz .Lw2c81
.Lw2b81:
	s_and_saveexec_b64 s[10:11], vcc
	s_cbranch_execz .LBB2_18
	v_ashrrev_i32_e32 v33, 31, v32
	v_lshl_add_u64 v[32:33], v[32:33], 2, s[16:17]
	global_load_dword v116, v[32:33], off
.LBB2_18:
	s_or_b64 exec, exec, s[10:11]
	v_mov_b32_e32 v56, 0
	s_xor_b64 s[10:11], s[18:19], -1
	v_mov_b32_e32 v115, 31
	v_mov_b32_e32 v57, v56
	v_mov_b32_e32 v58, v56
	v_mov_b32_e32 v59, v56
	v_mov_b32_e32 v60, v56
.Lw2t82:
	s_cbranch_execz .Lw2c82
.Lw2b82:
	v_mov_b32_e32 v61, v56
	v_mov_b32_e32 v62, v56
	v_mov_b32_e32 v63, v56
	s_branch .LBB2_20
.LBB2_19:
	s_waitcnt vmcnt(0)
	v_mov_b32_e32 v116, v114
	s_cbranch_execnz .LBB2_90
.LBB2_20:
	s_nop 2
	v_mov_b32_e32 v104, v63
	v_mov_b32_e32 v106, v62
	v_mov_b32_e32 v105, v61
	v_mov_b32_e32 v108, v60
	v_mov_b32_e32 v109, v59
	v_mov_b32_e32 v111, v58
	v_mov_b32_e32 v110, v57
.Lw2t83:
	s_cbranch_execz .Lw2c83
.Lw2b83:
	v_mov_b32_e32 v112, v56
	v_mov_b32_e32 v107, v115
	v_cmp_lt_i32_e32 vcc, v113, v103
	s_cbranch_vccz .LBB2_19
	v_or_b32_e32 v32, 4, v84
	s_waitcnt vmcnt(0)
	ds_bpermute_b32 v66, v84, v116
	ds_bpermute_b32 v123, v32, v116
	v_or_b32_e32 v32, 8, v84
	v_or_b32_e32 v34, 12, v84
	ds_bpermute_b32 v122, v32, v116
	ds_bpermute_b32 v121, v34, v116

.Lw2b84:
	v_or_b32_e32 v34, 16, v84
	ds_bpermute_b32 v120, v34, v116
	v_or_b32_e32 v34, 20, v84
	ds_bpermute_b32 v119, v34, v116
	s_waitcnt lgkmcnt(5)
	v_lshlrev_b32_e32 v32, 8, v66
	s_waitcnt lgkmcnt(4)
	v_lshlrev_b32_e32 v33, 8, v123
	v_or_b32_e32 v34, 24, v84
	v_and_or_b32 v32, v32, s21, v83
	v_and_or_b32 v33, v33, s21, v83

.Lw2b85:
	ds_bpermute_b32 v118, v34, v116
	ds_bpermute_b32 v117, v87, v116
	global_load_dwordx4 v[60:63], v32, s[8:9]
	global_load_dwordx4 v[56:59], v33, s[8:9]
	s_waitcnt lgkmcnt(5)
	v_lshlrev_b32_e32 v32, 8, v122
	s_waitcnt lgkmcnt(4)
	v_lshlrev_b32_e32 v33, 8, v121
	v_and_or_b32 v32, v32, s21, v83

.Lw2b86:
	v_and_or_b32 v33, v33, s21, v83
	global_load_dwordx4 v[52:55], v32, s[8:9]
	global_load_dwordx4 v[48:51], v33, s[8:9]
	s_waitcnt lgkmcnt(3)
	v_lshlrev_b32_e32 v32, 8, v120
	s_waitcnt lgkmcnt(2)
	v_lshlrev_b32_e32 v33, 8, v119
	v_and_or_b32 v32, v32, s21, v83
	v_and_or_b32 v33, v33, s21, v83
	global_load_dwordx4 v[44:47], v32, s[8:9]

.Lw2b87:
	global_load_dwordx4 v[40:43], v33, s[8:9]
	s_waitcnt lgkmcnt(1)
	v_lshlrev_b32_e32 v32, 8, v118
	s_waitcnt lgkmcnt(0)
	v_lshlrev_b32_e32 v33, 8, v117
	v_and_or_b32 v32, v32, s21, v83
	v_and_or_b32 v33, v33, s21, v83
	global_load_dwordx4 v[36:39], v32, s[8:9]
	s_nop 0
	global_load_dwordx4 v[32:35], v33, s[8:9]

.Lw2b88:
	v_or_b32_e32 v64, 16, v82
	v_add_u32_e32 v64, v64, v113
	v_cmp_lt_i32_e32 vcc, v64, v103
	v_mov_b32_e32 v114, 0x3f86a0
	s_and_saveexec_b64 s[14:15], vcc
	s_cbranch_execz .LBB2_23
	v_ashrrev_i32_e32 v65, 31, v64
	v_lshl_add_u64 v[64:65], v[64:65], 2, s[16:17]
	global_load_dword v114, v[64:65], off
.LBB2_23:
	s_or_b64 exec, exec, s[14:15]
	v_ashrrev_i32_e32 v124, 17, v66
.Lw2t89:
	s_cbranch_execz .Lw2c89
.Lw2b89:
	v_cmp_ne_u32_e32 vcc, v124, v107
	s_cmp_lg_u64 vcc, 0
	s_cselect_b64 s[14:15], -1, 0
	s_and_b64 s[18:19], s[14:15], vcc
	v_mov_b32_e32 v115, v107
	v_mov_b32_e32 v68, v112
	v_mov_b32_e32 v69, v110
	v_mov_b32_e32 v70, v111
	v_mov_b32_e32 v71, v109
	v_mov_b32_e32 v64, v108
	v_mov_b32_e32 v65, v105
	v_mov_b32_e32 v66, v106
	v_mov_b32_e32 v67, v104
	s_and_saveexec_b64 s[14:15], s[18:19]
	s_cbranch_execz .LBB2_27

.Lw2b90:
	v_cmp_gt_i32_e32 vcc, 16, v107
	s_and_saveexec_b64 s[18:19], vcc
	s_cbranch_execz .LBB2_26
	v_cvt_pk_f16_f32 v67, v111, v109
	v_cvt_pk_f16_f32 v66, v112, v110
	v_cvt_pk_f16_f32 v65, v106, v104
	v_cvt_pk_f16_f32 v64, v108, v105
	v_mad_u64_u32 v[68:69], s[24:25], v107, s20, v[76:77]
	ds_write_b128 v68, v[64:67]

.LBB2_27:
	s_or_b64 exec, exec, s[14:15]
	v_ashrrev_i32_e32 v123, 17, v123
	s_waitcnt vmcnt(7)
	v_mfma_f32_16x16x16_f16 v[64:67], v[72:73], v[60:61], v[64:67]
.Lw2t92:
	s_cbranch_execz .Lw2c92
.Lw2b92:
	v_cmp_ne_u32_e32 vcc, v123, v115
	s_cmp_lg_u64 vcc, 0
	s_cselect_b64 s[14:15], -1, 0
	v_mfma_f32_16x16x16_f16 v[60:63], v[72:73], v[62:63], v[68:71]
	s_and_b64 s[18:19], s[14:15], vcc
	s_and_saveexec_b64 s[14:15], s[18:19]
	s_cbranch_execz .LBB2_31
	v_cmp_gt_i32_e32 vcc, 16, v115
	s_and_saveexec_b64 s[18:19], vcc
	s_cbranch_execz .LBB2_30
	s_nop 1
	v_cvt_pk_f16_f32 v63, v62, v63
	v_cvt_pk_f16_f32 v62, v60, v61

.Lw2b93:
	v_cvt_pk_f16_f32 v61, v66, v67
	v_cvt_pk_f16_f32 v60, v64, v65
	v_mad_u64_u32 v[64:65], s[24:25], v115, s20, v[76:77]
	ds_write_b128 v64, v[60:63]
.LBB2_30:
	s_or_b64 exec, exec, s[18:19]
	s_nop 0
	v_mov_b32_e32 v60, 0
	v_mov_b32_e32 v115, v123
	v_mov_b32_e32 v61, v60
	v_mov_b32_e32 v62, v60
.Lw2t94:
	s_cbranch_execz .Lw2c94
.Lw2b94:
	v_mov_b32_e32 v63, v60
	v_mov_b32_e32 v64, v60
	v_mov_b32_e32 v65, v60
	v_mov_b32_e32 v66, v60
	v_mov_b32_e32 v67, v60
.LBB2_31:
	s_or_b64 exec, exec, s[14:15]
	v_ashrrev_i32_e32 v68, 17, v122
	s_waitcnt vmcnt(6)
	v_mfma_f32_16x16x16_f16 v[64:67], v[72:73], v[56:57], v[64:67]
	v_cmp_ne_u32_e32 vcc, v68, v115
	s_cmp_lg_u64 vcc, 0
	s_cselect_b64 s[14:15], -1, 0
	v_mfma_f32_16x16x16_f16 v[56:59], v[72:73], v[58:59], v[60:63]
.Lw2t95:
	s_cbranch_execz .Lw2c95
.Lw2b95:
	s_and_b64 s[18:19], s[14:15], vcc
	s_and_saveexec_b64 s[14:15], s[18:19]
	s_cbranch_execz .LBB2_35
	v_cmp_gt_i32_e32 vcc, 16, v115
	s_and_saveexec_b64 s[18:19], vcc
	s_cbranch_execz .LBB2_34
	s_nop 1
	v_cvt_pk_f16_f32 v59, v58, v59
	v_cvt_pk_f16_f32 v58, v56, v57
	v_cvt_pk_f16_f32 v57, v66, v67
	v_cvt_pk_f16_f32 v56, v64, v65

.Lw2b96:
	v_mad_u64_u32 v[60:61], s[24:25], v115, s20, v[76:77]
	ds_write_b128 v60, v[56:59]

.Lw2b97:
	s_or_b64 exec, exec, s[14:15]
	v_ashrrev_i32_e32 v68, 17, v121
	s_waitcnt vmcnt(5)
	v_mfma_f32_16x16x16_f16 v[60:63], v[72:73], v[52:53], v[64:67]
	v_cmp_ne_u32_e32 vcc, v68, v115
	s_cmp_lg_u64 vcc, 0
	s_cselect_b64 s[14:15], -1, 0
	v_mfma_f32_16x16x16_f16 v[52:55], v[72:73], v[54:55], v[56:59]
	s_and_b64 s[18:19], s[14:15], vcc
	s_and_saveexec_b64 s[14:15], s[18:19]
	s_cbranch_execz .LBB2_39
	v_cmp_gt_i32_e32 vcc, 16, v115
	s_and_saveexec_b64 s[18:19], vcc

.Lw2b98:
	s_cbranch_execz .LBB2_38
	s_nop 1
	v_cvt_pk_f16_f32 v55, v54, v55
	v_cvt_pk_f16_f32 v54, v52, v53
	v_cvt_pk_f16_f32 v53, v62, v63
	v_cvt_pk_f16_f32 v52, v60, v61
	v_mad_u64_u32 v[56:57], s[24:25], v115, s20, v[76:77]
	ds_write_b128 v56, v[52:55]

.Lw2b99:
	s_nop 0
	v_mov_b32_e32 v52, 0
	v_mov_b32_e32 v115, v68
	v_mov_b32_e32 v53, v52
	v_mov_b32_e32 v54, v52
	v_mov_b32_e32 v55, v52
	v_mov_b32_e32 v60, v52
	v_mov_b32_e32 v61, v52
	v_mov_b32_e32 v62, v52
	v_mov_b32_e32 v63, v52
.LBB2_39:
	s_or_b64 exec, exec, s[14:15]
	v_ashrrev_i32_e32 v64, 17, v120
	s_waitcnt vmcnt(4)
	v_mfma_f32_16x16x16_f16 v[56:59], v[72:73], v[48:49], v[60:63]
.Lw2t100:
	s_cbranch_execz .Lw2c100
.Lw2b100:
	v_cmp_ne_u32_e32 vcc, v64, v115
	s_cmp_lg_u64 vcc, 0
	s_cselect_b64 s[14:15], -1, 0
	v_mfma_f32_16x16x16_f16 v[48:51], v[72:73], v[50:51], v[52:55]
	s_and_b64 s[18:19], s[14:15], vcc
	s_and_saveexec_b64 s[14:15], s[18:19]
	s_cbranch_execz .LBB2_43
	v_cmp_gt_i32_e32 vcc, 16, v115
	s_and_saveexec_b64 s[18:19], vcc
	s_cbranch_execz .LBB2_42
	s_nop 1
	v_cvt_pk_f16_f32 v51, v50, v51
	v_cvt_pk_f16_f32 v50, v48, v49

.Lw2b101:
	v_cvt_pk_f16_f32 v49, v58, v59
	v_cvt_pk_f16_f32 v48, v56, v57
	v_mad_u64_u32 v[52:53], s[24:25], v115, s20, v[76:77]
	ds_write_b128 v52, v[48:51]
.LBB2_42:
	s_or_b64 exec, exec, s[18:19]
	s_nop 0
	v_mov_b32_e32 v48, 0
	v_mov_b32_e32 v115, v64
	v_mov_b32_e32 v49, v48
	v_mov_b32_e32 v50, v48
.Lw2t102:
	s_cbranch_execz .Lw2c102
.Lw2b102:
	v_mov_b32_e32 v51, v48
	v_mov_b32_e32 v56, v48
	v_mov_b32_e32 v57, v48
	v_mov_b32_e32 v58, v48
	v_mov_b32_e32 v59, v48
.LBB2_43:
	s_or_b64 exec, exec, s[14:15]
	v_ashrrev_i32_e32 v60, 17, v119
	s_waitcnt vmcnt(3)
	v_mfma_f32_16x16x16_f16 v[52:55], v[72:73], v[44:45], v[56:59]
	v_cmp_ne_u32_e32 vcc, v60, v115
	s_cmp_lg_u64 vcc, 0
	s_cselect_b64 s[14:15], -1, 0
	v_mfma_f32_16x16x16_f16 v[44:47], v[72:73], v[46:47], v[48:51]
.Lw2t103:
	s_cbranch_execz .Lw2c103
.Lw2b103:
	s_and_b64 s[18:19], s[14:15], vcc
	s_and_saveexec_b64 s[14:15], s[18:19]
	s_cbranch_execz .LBB2_47
	v_cmp_gt_i32_e32 vcc, 16, v115
	s_and_saveexec_b64 s[18:19], vcc
	s_cbranch_execz .LBB2_46
	s_nop 1
	v_cvt_pk_f16_f32 v47, v46, v47
	v_cvt_pk_f16_f32 v46, v44, v45
	v_cvt_pk_f16_f32 v45, v54, v55
	v_cvt_pk_f16_f32 v44, v52, v53

.Lw2b104:
	v_mad_u64_u32 v[48:49], s[24:25], v115, s20, v[76:77]
	ds_write_b128 v48, v[44:47]

.Lw2b105:
	s_or_b64 exec, exec, s[14:15]
	v_ashrrev_i32_e32 v56, 17, v118
	s_waitcnt vmcnt(2)
	v_mfma_f32_16x16x16_f16 v[48:51], v[72:73], v[40:41], v[52:55]
	v_cmp_ne_u32_e32 vcc, v56, v115
	s_cmp_lg_u64 vcc, 0
	s_cselect_b64 s[14:15], -1, 0
	v_mfma_f32_16x16x16_f16 v[40:43], v[72:73], v[42:43], v[44:47]
	s_and_b64 s[18:19], s[14:15], vcc
	s_and_saveexec_b64 s[14:15], s[18:19]
	s_cbranch_execz .LBB2_51
	v_cmp_gt_i32_e32 vcc, 16, v115
	s_and_saveexec_b64 s[18:19], vcc

.Lw2b106:
	s_cbranch_execz .LBB2_50
	s_nop 1
	v_cvt_pk_f16_f32 v43, v42, v43
	v_cvt_pk_f16_f32 v42, v40, v41
	v_cvt_pk_f16_f32 v41, v50, v51
	v_cvt_pk_f16_f32 v40, v48, v49
	v_mad_u64_u32 v[44:45], s[24:25], v115, s20, v[76:77]
	ds_write_b128 v44, v[40:43]

.Lw2b107:
	s_nop 0
	v_mov_b32_e32 v40, 0
	v_mov_b32_e32 v115, v56
	v_mov_b32_e32 v41, v40
	v_mov_b32_e32 v42, v40
	v_mov_b32_e32 v43, v40
	v_mov_b32_e32 v48, v40
	v_mov_b32_e32 v49, v40
	v_mov_b32_e32 v50, v40
	v_mov_b32_e32 v51, v40
.LBB2_51:
	s_or_b64 exec, exec, s[14:15]
	v_ashrrev_i32_e32 v52, 17, v117
	s_waitcnt vmcnt(1)
	v_mfma_f32_16x16x16_f16 v[44:47], v[72:73], v[36:37], v[48:51]
.Lw2t108:
	s_cbranch_execz .Lw2c108
.Lw2b108:
	v_cmp_ne_u32_e32 vcc, v52, v115
	s_cmp_lg_u64 vcc, 0
	s_cselect_b64 s[14:15], -1, 0
	v_mfma_f32_16x16x16_f16 v[36:39], v[72:73], v[38:39], v[40:43]
	s_and_b64 s[18:19], s[14:15], vcc
	s_and_saveexec_b64 s[14:15], s[18:19]
	s_cbranch_execz .LBB2_55
	v_cmp_gt_i32_e32 vcc, 16, v115
	s_and_saveexec_b64 s[18:19], vcc
	s_cbranch_execz .LBB2_54
	s_nop 1
	v_cvt_pk_f16_f32 v39, v38, v39
	v_cvt_pk_f16_f32 v38, v36, v37

.Lw2b109:
	v_cvt_pk_f16_f32 v37, v46, v47
	v_cvt_pk_f16_f32 v36, v44, v45
	v_mad_u64_u32 v[40:41], s[24:25], v115, s20, v[76:77]
	ds_write_b128 v40, v[36:39]
.LBB2_54:
	s_or_b64 exec, exec, s[18:19]
	s_nop 0
	v_mov_b32_e32 v36, 0
	v_mov_b32_e32 v115, v52
	v_mov_b32_e32 v37, v36
	v_mov_b32_e32 v38, v36
.Lw2t110:
	s_cbranch_execz .Lw2c110
.Lw2b110:
	v_mov_b32_e32 v39, v36
	v_mov_b32_e32 v44, v36
	v_mov_b32_e32 v45, v36
	v_mov_b32_e32 v46, v36
	v_mov_b32_e32 v47, v36
.LBB2_55:
	s_or_b64 exec, exec, s[14:15]
	s_waitcnt vmcnt(0)
	v_mfma_f32_16x16x16_f16 v[60:63], v[72:73], v[32:33], v[44:47]
	v_add_u32_e32 v32, 8, v113
	v_cmp_lt_i32_e32 vcc, v32, v103
	v_mfma_f32_16x16x16_f16 v[56:59], v[72:73], v[34:35], v[36:39]
	s_cbranch_vccz .LBB2_89
	ds_bpermute_b32 v123, v88, v116
.Lw2t111:
	s_cbranch_execz .Lw2c111
.Lw2b111:
	ds_bpermute_b32 v122, v89, v116
	ds_bpermute_b32 v121, v90, v116
	ds_bpermute_b32 v120, v91, v116
	ds_bpermute_b32 v119, v92, v116
	ds_bpermute_b32 v118, v93, v116
	s_waitcnt lgkmcnt(5)
	v_lshlrev_b32_e32 v32, 8, v123
	s_waitcnt lgkmcnt(4)
	v_lshlrev_b32_e32 v33, 8, v122

.Lw2b112:
	v_and_or_b32 v32, v32, s21, v83
	v_and_or_b32 v33, v33, s21, v83
	ds_bpermute_b32 v117, v94, v116
	ds_bpermute_b32 v116, v95, v116
	global_load_dwordx4 v[68:71], v32, s[8:9]
	global_load_dwordx4 v[64:67], v33, s[8:9]
	s_waitcnt lgkmcnt(5)
	v_lshlrev_b32_e32 v32, 8, v121
	s_waitcnt lgkmcnt(4)

.Lw2b113:
	v_lshlrev_b32_e32 v33, 8, v120
	v_and_or_b32 v32, v32, s21, v83
	v_and_or_b32 v33, v33, s21, v83
	global_load_dwordx4 v[52:55], v32, s[8:9]
	global_load_dwordx4 v[48:51], v33, s[8:9]
	s_waitcnt lgkmcnt(3)
	v_lshlrev_b32_e32 v32, 8, v119
	s_waitcnt lgkmcnt(2)
	v_lshlrev_b32_e32 v33, 8, v118
	v_and_or_b32 v32, v32, s21, v83

.Lw2b114:
	v_and_or_b32 v33, v33, s21, v83
	global_load_dwordx4 v[44:47], v32, s[8:9]
	global_load_dwordx4 v[40:43], v33, s[8:9]
	s_waitcnt lgkmcnt(1)
	v_lshlrev_b32_e32 v32, 8, v117
	s_waitcnt lgkmcnt(0)
	v_lshlrev_b32_e32 v33, 8, v116
	v_and_or_b32 v32, v32, s21, v83
	v_and_or_b32 v33, v33, s21, v83
	global_load_dwordx4 v[36:39], v32, s[8:9]

.Lw2b115:
	s_nop 0
	global_load_dwordx4 v[32:35], v33, s[8:9]
	v_ashrrev_i32_e32 v123, 17, v123
	v_cmp_ne_u32_e32 vcc, v123, v115
	s_cmp_lg_u64 vcc, 0
	s_cselect_b64 s[14:15], -1, 0
	s_and_b64 s[18:19], s[14:15], vcc
	s_and_saveexec_b64 s[14:15], s[18:19]
	s_cbranch_execz .LBB2_60
	v_cmp_gt_i32_e32 vcc, 16, v115
	s_and_saveexec_b64 s[18:19], vcc
	s_cbranch_execz .LBB2_59
	v_cvt_pk_f16_f32 v59, v58, v59

.Lw2b116:
	v_cvt_pk_f16_f32 v58, v56, v57
	v_cvt_pk_f16_f32 v57, v62, v63
	v_cvt_pk_f16_f32 v56, v60, v61
	v_mad_u64_u32 v[60:61], s[24:25], v115, s20, v[76:77]
	ds_write_b128 v60, v[56:59]
.LBB2_59:
	s_or_b64 exec, exec, s[18:19]
	v_mov_b32_e32 v56, 0
	v_mov_b32_e32 v115, v123
	v_mov_b32_e32 v57, v56
.Lw2t117:
	s_cbranch_execz .Lw2c117
.Lw2b117:
	v_mov_b32_e32 v58, v56
	v_mov_b32_e32 v59, v56
	v_mov_b32_e32 v60, v56
	v_mov_b32_e32 v61, v56
	v_mov_b32_e32 v62, v56
	v_mov_b32_e32 v63, v56
.LBB2_60:
	s_or_b64 exec, exec, s[14:15]
	v_ashrrev_i32_e32 v122, 17, v122
	s_waitcnt vmcnt(7)
	v_mfma_f32_16x16x16_f16 v[60:63], v[72:73], v[68:69], v[60:63]
	v_cmp_ne_u32_e32 vcc, v122, v115
	s_cmp_lg_u64 vcc, 0
	s_cselect_b64 s[14:15], -1, 0
	v_mfma_f32_16x16x16_f16 v[56:59], v[72:73], v[70:71], v[56:59]
.Lw2t118:
	s_cbranch_execz .Lw2c118
.Lw2b118:
	s_and_b64 s[18:19], s[14:15], vcc
	s_and_saveexec_b64 s[14:15], s[18:19]
	s_cbranch_execz .LBB2_64
	v_cmp_gt_i32_e32 vcc, 16, v115
	s_and_saveexec_b64 s[18:19], vcc
	s_cbranch_execz .LBB2_63
	s_nop 1
	v_cvt_pk_f16_f32 v59, v58, v59
	v_cvt_pk_f16_f32 v58, v56, v57
	v_cvt_pk_f16_f32 v57, v62, v63
	v_cvt_pk_f16_f32 v56, v60, v61

.LBB2_63:
	s_or_b64 exec, exec, s[18:19]
	s_nop 0
	v_mov_b32_e32 v56, 0
	v_mov_b32_e32 v115, v122
	v_mov_b32_e32 v57, v56
	v_mov_b32_e32 v58, v56
	v_mov_b32_e32 v59, v56
	v_mov_b32_e32 v60, v56
	v_mov_b32_e32 v61, v56
	v_mov_b32_e32 v62, v56
.Lw2t120:
	s_cbranch_execz .Lw2c120

.LBB2_64:
	s_or_b64 exec, exec, s[14:15]
	v_ashrrev_i32_e32 v68, 17, v121
	s_waitcnt vmcnt(6)
	v_mfma_f32_16x16x16_f16 v[60:63], v[72:73], v[64:65], v[60:63]
	v_cmp_ne_u32_e32 vcc, v68, v115
	s_cmp_lg_u64 vcc, 0
	s_cselect_b64 s[14:15], -1, 0
	v_mfma_f32_16x16x16_f16 v[56:59], v[72:73], v[66:67], v[56:59]
	s_and_b64 s[18:19], s[14:15], vcc
	s_and_saveexec_b64 s[14:15], s[18:19]
	s_cbranch_execz .LBB2_68
	v_cmp_gt_i32_e32 vcc, 16, v115

.LBB2_68:
	s_or_b64 exec, exec, s[14:15]
	v_ashrrev_i32_e32 v64, 17, v120
	s_waitcnt vmcnt(5)
	v_mfma_f32_16x16x16_f16 v[60:63], v[72:73], v[52:53], v[60:63]
.Lw2t123:
	s_cbranch_execz .Lw2c123
.Lw2b123:
	v_cmp_ne_u32_e32 vcc, v64, v115
	s_cmp_lg_u64 vcc, 0
	s_cselect_b64 s[14:15], -1, 0
	v_mfma_f32_16x16x16_f16 v[52:55], v[72:73], v[54:55], v[56:59]
	s_and_b64 s[18:19], s[14:15], vcc
	s_and_saveexec_b64 s[14:15], s[18:19]
	s_cbranch_execz .LBB2_72
	v_cmp_gt_i32_e32 vcc, 16, v115
	s_and_saveexec_b64 s[18:19], vcc
	s_cbranch_execz .LBB2_71
	s_nop 1
	v_cvt_pk_f16_f32 v55, v54, v55

.Lw2b124:
	v_cvt_pk_f16_f32 v54, v52, v53
	v_cvt_pk_f16_f32 v53, v62, v63
	v_cvt_pk_f16_f32 v52, v60, v61
	v_mad_u64_u32 v[56:57], s[24:25], v115, s20, v[76:77]
	ds_write_b128 v56, v[52:55]
.LBB2_71:
	s_or_b64 exec, exec, s[18:19]
	s_nop 0
	v_mov_b32_e32 v52, 0
	v_mov_b32_e32 v115, v64
	v_mov_b32_e32 v53, v52
.Lw2t125:
	s_cbranch_execz .Lw2c125
.Lw2b125:
	v_mov_b32_e32 v54, v52
	v_mov_b32_e32 v55, v52
	v_mov_b32_e32 v60, v52
	v_mov_b32_e32 v61, v52
	v_mov_b32_e32 v62, v52
	v_mov_b32_e32 v63, v52
.LBB2_72:
	s_or_b64 exec, exec, s[14:15]
	v_ashrrev_i32_e32 v64, 17, v119
	s_waitcnt vmcnt(4)
	v_mfma_f32_16x16x16_f16 v[56:59], v[72:73], v[48:49], v[60:63]
	v_cmp_ne_u32_e32 vcc, v64, v115
	s_cmp_lg_u64 vcc, 0
	s_cselect_b64 s[14:15], -1, 0
	v_mfma_f32_16x16x16_f16 v[48:51], v[72:73], v[50:51], v[52:55]
.Lw2t126:
	s_cbranch_execz .Lw2c126

.LBB2_75:
	s_or_b64 exec, exec, s[18:19]
	s_nop 0
	v_mov_b32_e32 v48, 0
	v_mov_b32_e32 v115, v64
	v_mov_b32_e32 v49, v48
	v_mov_b32_e32 v50, v48
	v_mov_b32_e32 v51, v48
	v_mov_b32_e32 v56, v48
	v_mov_b32_e32 v57, v48
	v_mov_b32_e32 v58, v48
.Lw2t128:
	s_cbranch_execz .Lw2c128
.Lw2b128:
	v_mov_b32_e32 v59, v48
.LBB2_76:
	s_or_b64 exec, exec, s[14:15]
	v_ashrrev_i32_e32 v60, 17, v118
	s_waitcnt vmcnt(3)
	v_mfma_f32_16x16x16_f16 v[52:55], v[72:73], v[44:45], v[56:59]
	v_cmp_ne_u32_e32 vcc, v60, v115
	s_cmp_lg_u64 vcc, 0
	s_cselect_b64 s[14:15], -1, 0
	v_mfma_f32_16x16x16_f16 v[44:47], v[72:73], v[46:47], v[48:51]
	s_and_b64 s[18:19], s[14:15], vcc
	s_and_saveexec_b64 s[14:15], s[18:19]
	s_cbranch_execz .LBB2_80
	v_cmp_gt_i32_e32 vcc, 16, v115

.Lw2b129:
	s_and_saveexec_b64 s[18:19], vcc
	s_cbranch_execz .LBB2_79
	s_nop 1
	v_cvt_pk_f16_f32 v47, v46, v47
	v_cvt_pk_f16_f32 v46, v44, v45
	v_cvt_pk_f16_f32 v45, v54, v55
	v_cvt_pk_f16_f32 v44, v52, v53
	v_mad_u64_u32 v[48:49], s[24:25], v115, s20, v[76:77]
	ds_write_b128 v48, v[44:47]

.LBB2_80:
	s_or_b64 exec, exec, s[14:15]
	v_ashrrev_i32_e32 v56, 17, v117
	s_waitcnt vmcnt(2)
	v_mfma_f32_16x16x16_f16 v[48:51], v[72:73], v[40:41], v[52:55]
.Lw2t131:
	s_cbranch_execz .Lw2c131
.Lw2b131:
	v_cmp_ne_u32_e32 vcc, v56, v115
	s_cmp_lg_u64 vcc, 0
	s_cselect_b64 s[14:15], -1, 0
	v_mfma_f32_16x16x16_f16 v[40:43], v[72:73], v[42:43], v[44:47]
	s_and_b64 s[18:19], s[14:15], vcc
	s_and_saveexec_b64 s[14:15], s[18:19]
	s_cbranch_execz .LBB2_84
	v_cmp_gt_i32_e32 vcc, 16, v115
	s_and_saveexec_b64 s[18:19], vcc
	s_cbranch_execz .LBB2_83
	s_nop 1
	v_cvt_pk_f16_f32 v43, v42, v43
.Lw2t132:
	s_cbranch_execz .Lw2c132
.Lw2b132:
	v_cvt_pk_f16_f32 v42, v40, v41
	v_cvt_pk_f16_f32 v41, v50, v51
	v_cvt_pk_f16_f32 v40, v48, v49
	v_mad_u64_u32 v[44:45], s[24:25], v115, s20, v[76:77]
	ds_write_b128 v44, v[40:43]
.LBB2_83:
	s_or_b64 exec, exec, s[18:19]
	s_nop 0
	v_mov_b32_e32 v40, 0
	v_mov_b32_e32 v115, v56
	v_mov_b32_e32 v41, v40
.Lw2t133:
	s_cbranch_execz .Lw2c133
.Lw2b133:
	v_mov_b32_e32 v42, v40
	v_mov_b32_e32 v43, v40
	v_mov_b32_e32 v48, v40
	v_mov_b32_e32 v49, v40
	v_mov_b32_e32 v50, v40
	v_mov_b32_e32 v51, v40
.LBB2_84:
	s_or_b64 exec, exec, s[14:15]
	v_ashrrev_i32_e32 v52, 17, v116
	s_waitcnt vmcnt(1)
	v_mfma_f32_16x16x16_f16 v[44:47], v[72:73], v[36:37], v[48:51]
	v_cmp_ne_u32_e32 vcc, v52, v115
	s_cmp_lg_u64 vcc, 0
	s_cselect_b64 s[14:15], -1, 0
	v_mfma_f32_16x16x16_f16 v[36:39], v[72:73], v[38:39], v[40:43]
.Lw2t134:
	s_cbranch_execz .Lw2c134

.LBB2_87:
	s_or_b64 exec, exec, s[18:19]
	s_nop 0
	v_mov_b32_e32 v36, 0
	v_mov_b32_e32 v115, v52
	v_mov_b32_e32 v37, v36
	v_mov_b32_e32 v38, v36
	v_mov_b32_e32 v39, v36
	v_mov_b32_e32 v44, v36
	v_mov_b32_e32 v45, v36
	v_mov_b32_e32 v46, v36
.Lw2t136:
	s_cbranch_execz .Lw2c136
.Lw2b136:
	v_mov_b32_e32 v47, v36

.LBB2_90:
	v_cmp_gt_i32_e32 vcc, 16, v107
	s_and_saveexec_b64 s[14:15], vcc
	s_cbranch_execz .LBB2_15
	v_cvt_pk_f16_f32 v35, v111, v109
.Lw2t137:
	s_cbranch_execz .Lw2c137
.Lw2b137:
	v_cvt_pk_f16_f32 v34, v112, v110
	v_cvt_pk_f16_f32 v33, v106, v104
	v_cvt_pk_f16_f32 v32, v108, v105
	v_mad_u64_u32 v[36:37], s[16:17], v107, s20, v[76:77]
	ds_write_b128 v36, v[32:35]
	s_branch .LBB2_15

	.amdhsa_kernel _Z10k_layer_a2ILi0ELi13EEvPKDF16_PKiS3_PK15HIP_vector_typeIjLj4EES7_PKfS9_S9_S9_S9_S9_PDF16_Pf
		.amdhsa_group_segment_fixed_size 125188
		.amdhsa_private_segment_fixed_size 0
		.amdhsa_kernarg_size 360
		.amdhsa_user_sgpr_count 2
		.amdhsa_user_sgpr_dispatch_ptr 0
		.amdhsa_user_sgpr_queue_ptr 0
		.amdhsa_user_sgpr_kernarg_segment_ptr 1
		.amdhsa_user_sgpr_dispatch_id 0
		.amdhsa_user_sgpr_kernarg_preload_length 0
		.amdhsa_user_sgpr_kernarg_preload_offset 0
		.amdhsa_user_sgpr_private_segment_size 0
		.amdhsa_uses_dynamic_stack 0
		.amdhsa_enable_private_segment 0
		.amdhsa_system_sgpr_workgroup_id_x 1
		.amdhsa_system_sgpr_workgroup_id_y 0
		.amdhsa_system_sgpr_workgroup_id_z 0
		.amdhsa_system_sgpr_workgroup_info 0
		.amdhsa_system_vgpr_workitem_id 0
		.amdhsa_next_free_vgpr 128
		.amdhsa_next_free_sgpr 96
		.amdhsa_accum_offset 128
		.amdhsa_reserve_vcc 1
		.amdhsa_float_round_mode_32 0
		.amdhsa_float_round_mode_16_64 0
		.amdhsa_float_denorm_mode_32 3
		.amdhsa_float_denorm_mode_16_64 3
		.amdhsa_dx10_clamp 1
		.amdhsa_ieee_mode 1
		.amdhsa_fp16_overflow 0
		.amdhsa_tg_split 0
		.amdhsa_exception_fp_ieee_invalid_op 0
		.amdhsa_exception_fp_denorm_src 0
		.amdhsa_exception_fp_ieee_div_zero 0
		.amdhsa_exception_fp_ieee_overflow 0
		.amdhsa_exception_fp_ieee_underflow 0
		.amdhsa_exception_fp_ieee_inexact 0
		.amdhsa_exception_int_div_zero 0
	.end_amdhsa_kernel

_Z10k_layer_a2ILi1ELi13EEvPKDF16_PKiS3_PK15HIP_vector_typeIjLj4EES7_PKfS9_S9_S9_S9_S9_PDF16_Pf:
	s_load_dword s42, s[0:1], 0x0
	s_load_dword s43, s[0:1], 0x40
	v_lshrrev_b32_e32 v1, 6, v0
	s_nop 0
	v_readfirstlane_b32 s41, v1
	s_movk_i32 s40, 0x5aa5
	s_mov_b64 exec, 0
	s_cmpk_lt_u32 s41, 6
	s_cbranch_scc1 .Lw3s0d0_13
	s_cmpk_lt_u32 s41, 9
	s_cbranch_scc1 .Lw3s0d6_13
	s_cmpk_lt_u32 s41, 11
	s_cbranch_scc1 .Lw3s0d9_13
	s_cmpk_lt_u32 s41, 12
	s_cbranch_scc1 .Lw3s0d11_13
	s_branch .Lw3t12

.Lw3b0:
	s_load_dwordx8 s[4:11], s[0:1], 0x18
	v_mov_b32_e32 v3, 0
	v_lshlrev_b32_e32 v2, 4, v0
	s_movk_i32 s3, 0x3000
	v_min_u32_e32 v1, 0x7f, v0
	s_waitcnt lgkmcnt(0)
	v_lshl_add_u64 v[4:5], s[4:5], 0, v[2:3]
	v_add_co_u32_e32 v6, vcc, s3, v4
	s_movk_i32 s3, 0x6000
	s_nop 0

.Lw3b1:
	v_addc_co_u32_e32 v7, vcc, 0, v5, vcc
	v_add_co_u32_e32 v16, vcc, s3, v4
	v_lshlrev_b32_e32 v26, 2, v1
	s_nop 0
	v_addc_co_u32_e32 v17, vcc, 0, v5, vcc
	global_load_dwordx4 v[8:11], v[6:7], off offset:1024
	global_load_dwordx4 v[12:15], v[16:17], off offset:2048
	v_add_co_u32_e32 v24, vcc, 0x9000, v4
	v_readfirstlane_b32 s3, v0
	s_nop 0
	v_addc_co_u32_e32 v25, vcc, 0, v5, vcc
	global_load_dwordx4 v[16:19], v2, s[4:5]

.Lw3b2:
	global_load_dwordx4 v[20:23], v[24:25], off offset:3072
	global_load_dword v5, v26, s[8:9]
	global_load_dword v7, v26, s[8:9] offset:512
	global_load_dword v1, v26, s[10:11]
	global_load_dword v4, v26, s[12:13]
	global_load_dword v6, v26, s[14:15]
	s_movk_i32 s8, 0x300
	v_cmp_gt_u32_e32 vcc, s8, v0

.Lw3b3:
	s_waitcnt vmcnt(6)
	ds_write_b128 v2, v[16:19]
	ds_write_b128 v2, v[8:11] offset:13312
	ds_write_b128 v2, v[12:15] offset:26624
	s_waitcnt vmcnt(5)
	ds_write_b128 v2, v[20:23] offset:39936
	s_and_saveexec_b64 s[8:9], vcc
	s_cbranch_execz .LBB3_2
	v_add_u32_e32 v8, 0xd00, v0
	v_min_u32_e32 v8, 0xfff, v8

.Lw3b4:
	v_lshlrev_b32_e32 v8, 4, v8
	global_load_dwordx4 v[8:11], v8, s[4:5]
	s_waitcnt vmcnt(0)
	ds_write_b128 v2, v[8:11] offset:53248
.LBB3_2:
	s_or_b64 exec, exec, s[8:9]
	v_lshl_add_u64 v[8:9], s[6:7], 0, v[2:3]
	v_add_co_u32_e32 v16, vcc, 0x3000, v8
	s_movk_i32 s4, 0x280
	s_nop 0
	v_addc_co_u32_e32 v17, vcc, 0, v9, vcc
.Lw3t5:
	s_cbranch_execz .Lw3c5
.Lw3b5:
	global_load_dwordx4 v[8:11], v2, s[6:7]
	global_load_dwordx4 v[12:15], v[16:17], off offset:1024
	v_mov_b32_e32 v2, 0x1dd00
	v_lshl_add_u32 v2, v0, 4, v2
	v_cmp_gt_u32_e32 vcc, s4, v0
	s_waitcnt vmcnt(1)
	ds_write_b128 v2, v[8:11]
	s_waitcnt vmcnt(0)
	ds_write_b128 v2, v[12:15] offset:13312

.Lw3b6:
	s_and_saveexec_b64 s[4:5], vcc
	s_cbranch_execz .LBB3_4
	v_add_u32_e32 v3, 0x680, v0
	v_min_u32_e32 v3, 0x8ff, v3
	v_lshlrev_b32_e32 v3, 4, v3
	global_load_dwordx4 v[8:11], v3, s[6:7]
	s_waitcnt vmcnt(0)
	ds_write_b128 v2, v[8:11] offset:26624
.LBB3_4:
	s_or_b64 exec, exec, s[4:5]
	s_movk_i32 s4, 0x80
	v_cmp_gt_u32_e32 vcc, s4, v0
.Lw3t7:
	s_cbranch_execz .Lw3c7
.Lw3b7:
	s_and_saveexec_b64 s[4:5], vcc
	s_cbranch_execz .LBB3_6
	v_mov_b32_e32 v3, 0x26d00
	v_add_f32_e32 v2, v5, v7
	v_lshl_add_u32 v3, v0, 2, v3
	ds_write2st64_b32 v3, v2, v1 offset1:2
	ds_write2st64_b32 v3, v4, v6 offset0:4 offset1:6
.LBB3_6:
	s_or_b64 exec, exec, s[4:5]
	s_load_dwordx2 s[6:7], s[0:1], 0x60
	s_load_dwordx2 s[16:17], s[0:1], 0x50
.Lw3t8:
	s_cbranch_execz .Lw3c8
.Lw3b8:
	s_load_dwordx4 s[8:11], s[0:1], 0x0
	s_load_dwordx2 s[18:19], s[0:1], 0x10
	s_mov_b32 s13, 0
	v_cmp_eq_u32_e32 vcc, 0, v0
	s_and_saveexec_b64 s[4:5], vcc
	v_mov_b32_e32 v1, 0
	v_mov_b32_e32 v2, 0x27900
	ds_write_b32 v2, v1
	s_or_b64 exec, exec, s[4:5]
	v_bfe_u32 v1, v0, 4, 2

.Lw3b9:
	v_bfe_u32 v2, v0, 2, 2
	v_cmp_eq_u32_e32 vcc, v1, v2
	v_and_b32_e32 v2, 3, v0
	v_cmp_eq_u32_e64 s[4:5], 0, v2
	v_mov_b32_e32 v3, 0x3c00
	s_and_b64 s[4:5], vcc, s[4:5]
	v_cndmask_b32_e64 v4, 0, v3, s[4:5]
	v_cmp_eq_u32_e64 s[4:5], 1, v2
	s_and_b64 s[4:5], vcc, s[4:5]

.Lw3b11:
	v_lshlrev_b32_e32 v2, 2, v0
	v_and_b32_e32 v82, 0xc0, v2
	v_and_b32_e32 v2, 48, v0
	v_mov_b32_e32 v3, 0
	s_waitcnt lgkmcnt(0)
	s_barrier
	v_and_b32_e32 v80, 15, v0
	s_load_dword s3, s[0:1], 0x68
	s_mul_i32 s0, s12, 0x1100
	v_lshl_add_u64 v[74:75], s[10:11], 0, v[2:3]
	v_bfe_u32 v3, v0, 2, 4

.Lw3b12:
	v_lshlrev_b32_e32 v0, 6, v0
	s_add_i32 s4, s0, 0x10000
	v_mul_u32_u24_e32 v3, 0x110, v3
	v_and_b32_e32 v0, 0xc0, v0
	s_movk_i32 s26, 0x110
	v_add3_u32 v83, s4, v3, v0
	v_mov_b32_e32 v0, s4
	v_mad_u32_u24 v0, v80, s26, v0
	v_pack_b32_f16 v72, v4, v5

.Lw3b13:
	v_lshlrev_b32_e32 v81, 4, v80
	v_lshlrev_b32_e32 v4, 7, v1
	v_add_u32_e32 v97, v0, v2
	v_mbcnt_lo_u32_b32 v0, -1, 0
	v_cmp_eq_u32_e64 s[0:1], 0, v77
	v_or_b32_e32 v76, s4, v81
	v_lshlrev_b32_e32 v84, 5, v1
	v_cmp_gt_u32_e64 s[4:5], 16, v77
	v_or_b32_e32 v85, 24, v82
	v_or_b32_e32 v86, 28, v82
	v_or_b32_e32 v87, 32, v82

.Lw3b14:
	v_or_b32_e32 v88, 36, v82
	v_or_b32_e32 v89, 40, v82
	v_or_b32_e32 v90, 44, v82
	v_or_b32_e32 v91, 48, v82
	v_or_b32_e32 v92, 52, v82
	v_or_b32_e32 v93, 56, v82
	v_or_b32_e32 v94, 60, v82
	v_mov_b32_e32 v95, 0x27900
	v_add_u32_e32 v96, 0x26d00, v4
	s_mov_b32 s27, 0x1ffff00
	v_mov_b32_e32 v98, 0x3727c5ac

.Lw3b15:
	s_mov_b32 s28, 0x800000
	v_mov_b32_e32 v99, 0xc0135761
	v_mbcnt_hi_u32_b32 v100, -1, v0
	v_mov_b32_e32 v101, 0x26d00
	v_mov_b32_e32 v102, 0x1dd00
	s_branch .LBB3_11

.LBB3_10:
	s_and_b64 vcc, exec, s[10:11]
	s_cbranch_vccnz .LBB3_96
.LBB3_11:
.Lw3t16:
	s_cbranch_execz .Lw3c16
.Lw3b16:
	s_nop 0
	v_mov_b32_e32 v0, 0
	s_and_saveexec_b64 s[10:11], s[0:1]
	s_cbranch_execz .LBB3_15
	s_mov_b64 s[20:21], exec
	v_mbcnt_lo_u32_b32 v0, s20, 0
	v_mbcnt_hi_u32_b32 v0, s21, v0
	v_cmp_eq_u32_e32 vcc, 0, v0
	s_and_saveexec_b64 s[14:15], vcc
	s_bcnt1_i32_b64 s12, s[20:21]
	v_mov_b32_e32 v1, s12
	ds_add_rtn_u32 v1, v95, v1

.Lw3b17:
	s_or_b64 exec, exec, s[14:15]
	s_waitcnt lgkmcnt(0)
	v_readfirstlane_b32 s12, v1
	s_nop 1
	v_add_u32_e32 v0, s12, v0
.LBB3_15:
	s_or_b64 exec, exec, s[10:11]
	v_readfirstlane_b32 s10, v0
	s_waitcnt lgkmcnt(0)
	s_mul_i32 s12, s10, s3
	s_add_i32 s12, s12, s2
	s_cmpk_gt_i32 s12, 0x1869
	s_mov_b64 s[10:11], -1
	s_cbranch_scc1 .LBB3_10
	ds_read_b128 v[28:31], v96
.Lw3t18:
	s_cbranch_execz .Lw3c18
.Lw3b18:
	ds_read_b128 v[24:27], v96 offset:16
	ds_read_b128 v[20:23], v96 offset:32
	ds_read_b128 v[16:19], v96 offset:48
	ds_read_b128 v[12:15], v96 offset:64
	ds_read_b128 v[8:11], v96 offset:80
	ds_read_b128 v[4:7], v96 offset:96
	ds_read_b128 v[0:3], v96 offset:112
	s_lshl_b32 s10, s12, 4

.Lw3b19:
	s_ashr_i32 s11, s10, 31
	v_lshl_add_u64 v[78:79], s[10:11], 2, v[74:75]
	s_mov_b32 s11, 0
	s_mov_b64 s[22:23], -1
	s_branch .LBB3_18
.LBB3_17:
	s_or_b64 exec, exec, s[20:21]
	v_mov_b32_e32 v48, v77
	ds_read_b128 v[32:35], v97
	ds_read_b128 v[36:39], v97 offset:64
	ds_read_b128 v[40:43], v97 offset:128
	ds_read_b128 v[44:47], v97 offset:192
.Lw3t20:
	s_cbranch_execz .Lw3c20
.Lw3b20:
	s_nop 0
	v_lshlrev_b32_e32 v48, 4, v48
	v_lshl_add_u32 v103, s11, 15, v48
	ds_read_b128 v[48:51], v103
	ds_read_b128 v[52:55], v103 offset:1024
	ds_read_b128 v[56:59], v103 offset:2048
	ds_read_b128 v[60:63], v103 offset:3072
	ds_read_b128 v[64:67], v103 offset:4096

.Lw3b21:
	ds_read_b128 v[68:71], v103 offset:5120
	ds_read_b128 v[104:107], v103 offset:6144
	ds_read_b128 v[108:111], v103 offset:7168
	s_waitcnt lgkmcnt(7)
	v_mfma_f32_16x16x32_f16 v[28:31], v[48:51], v[32:35], v[28:31]
	s_waitcnt lgkmcnt(6)
	v_mfma_f32_16x16x32_f16 v[24:27], v[52:55], v[32:35], v[24:27]
	s_waitcnt lgkmcnt(5)
	v_mfma_f32_16x16x32_f16 v[20:23], v[56:59], v[32:35], v[20:23]

.Lw3b22:
	s_waitcnt lgkmcnt(4)
	v_mfma_f32_16x16x32_f16 v[16:19], v[60:63], v[32:35], v[16:19]
	ds_read_b128 v[48:51], v103 offset:8192
	ds_read_b128 v[52:55], v103 offset:9216
	ds_read_b128 v[56:59], v103 offset:10240
	ds_read_b128 v[60:63], v103 offset:11264
	s_waitcnt lgkmcnt(7)
	v_mfma_f32_16x16x32_f16 v[12:15], v[64:67], v[32:35], v[12:15]
	s_waitcnt lgkmcnt(6)

.Lw3b23:
	v_mfma_f32_16x16x32_f16 v[8:11], v[68:71], v[32:35], v[8:11]
	s_waitcnt lgkmcnt(5)
	v_mfma_f32_16x16x32_f16 v[4:7], v[104:107], v[32:35], v[4:7]
	s_waitcnt lgkmcnt(4)
	v_mfma_f32_16x16x32_f16 v[0:3], v[108:111], v[32:35], v[0:3]
	ds_read_b128 v[32:35], v103 offset:12288
	ds_read_b128 v[64:67], v103 offset:13312
	ds_read_b128 v[68:71], v103 offset:14336
	ds_read_b128 v[104:107], v103 offset:15360

.Lw3b24:
	s_waitcnt lgkmcnt(7)
	v_mfma_f32_16x16x32_f16 v[28:31], v[48:51], v[36:39], v[28:31]
	s_waitcnt lgkmcnt(6)
	v_mfma_f32_16x16x32_f16 v[24:27], v[52:55], v[36:39], v[24:27]
	s_waitcnt lgkmcnt(5)
	v_mfma_f32_16x16x32_f16 v[20:23], v[56:59], v[36:39], v[20:23]
	s_waitcnt lgkmcnt(4)
	v_mfma_f32_16x16x32_f16 v[16:19], v[60:63], v[36:39], v[16:19]
	ds_read_b128 v[48:51], v103 offset:16384

.Lw3b25:
	ds_read_b128 v[52:55], v103 offset:17408
	ds_read_b128 v[56:59], v103 offset:18432
	ds_read_b128 v[60:63], v103 offset:19456
	s_waitcnt lgkmcnt(7)
	v_mfma_f32_16x16x32_f16 v[12:15], v[32:35], v[36:39], v[12:15]
	s_waitcnt lgkmcnt(6)
	v_mfma_f32_16x16x32_f16 v[8:11], v[64:67], v[36:39], v[8:11]
	s_waitcnt lgkmcnt(5)
	v_mfma_f32_16x16x32_f16 v[4:7], v[68:71], v[36:39], v[4:7]

.Lw3b26:
	s_waitcnt lgkmcnt(4)
	v_mfma_f32_16x16x32_f16 v[0:3], v[104:107], v[36:39], v[0:3]
	ds_read_b128 v[32:35], v103 offset:20480
	ds_read_b128 v[36:39], v103 offset:21504
	ds_read_b128 v[64:67], v103 offset:22528
	ds_read_b128 v[68:71], v103 offset:23552
	s_waitcnt lgkmcnt(7)
	v_mfma_f32_16x16x32_f16 v[28:31], v[48:51], v[40:43], v[28:31]
	s_waitcnt lgkmcnt(6)

.Lw3b27:
	v_mfma_f32_16x16x32_f16 v[24:27], v[52:55], v[40:43], v[24:27]
	s_waitcnt lgkmcnt(5)
	v_mfma_f32_16x16x32_f16 v[20:23], v[56:59], v[40:43], v[20:23]
	s_waitcnt lgkmcnt(4)
	v_mfma_f32_16x16x32_f16 v[16:19], v[60:63], v[40:43], v[16:19]
	ds_read_b128 v[48:51], v103 offset:24576
	ds_read_b128 v[52:55], v103 offset:25600
	ds_read_b128 v[56:59], v103 offset:26624
	ds_read_b128 v[60:63], v103 offset:27648

.Lw3b28:
	s_waitcnt lgkmcnt(7)
	v_mfma_f32_16x16x32_f16 v[12:15], v[32:35], v[40:43], v[12:15]
	s_waitcnt lgkmcnt(6)
	v_mfma_f32_16x16x32_f16 v[8:11], v[36:39], v[40:43], v[8:11]
	s_waitcnt lgkmcnt(5)
	v_mfma_f32_16x16x32_f16 v[4:7], v[64:67], v[40:43], v[4:7]
	s_waitcnt lgkmcnt(4)
	v_mfma_f32_16x16x32_f16 v[0:3], v[68:71], v[40:43], v[0:3]
	ds_read_b128 v[32:35], v103 offset:28672

.Lw3b29:
	ds_read_b128 v[36:39], v103 offset:29696
	ds_read_b128 v[40:43], v103 offset:30720
	ds_read_b128 v[64:67], v103 offset:31744
	s_waitcnt lgkmcnt(7)
	v_mfma_f32_16x16x32_f16 v[28:31], v[48:51], v[44:47], v[28:31]
	s_waitcnt lgkmcnt(6)
	v_mfma_f32_16x16x32_f16 v[24:27], v[52:55], v[44:47], v[24:27]
	s_waitcnt lgkmcnt(5)
	v_mfma_f32_16x16x32_f16 v[20:23], v[56:59], v[44:47], v[20:23]

.Lw3b30:
	s_waitcnt lgkmcnt(4)
	v_mfma_f32_16x16x32_f16 v[16:19], v[60:63], v[44:47], v[16:19]
	s_waitcnt lgkmcnt(3)
	v_mfma_f32_16x16x32_f16 v[12:15], v[32:35], v[44:47], v[12:15]
	s_waitcnt lgkmcnt(2)
	v_mfma_f32_16x16x32_f16 v[8:11], v[36:39], v[44:47], v[8:11]
	s_waitcnt lgkmcnt(1)
	v_mfma_f32_16x16x32_f16 v[4:7], v[40:43], v[44:47], v[4:7]
	s_waitcnt lgkmcnt(0)
	v_mfma_f32_16x16x32_f16 v[0:3], v[64:67], v[44:47], v[0:3]

.Lw3b31:
	s_mov_b32 s11, 1
	s_mov_b64 s[22:23], 0
	s_and_b64 vcc, exec, s[14:15]
	s_cbranch_vccnz .LBB3_94
.LBB3_18:
	s_mul_i32 s12, s11, 0x186a1
	v_lshl_add_u64 v[32:33], s[12:13], 2, v[78:79]
	global_load_dword v113, v[32:33], off
	global_load_dword v103, v[32:33], off offset:16
	s_mov_b32 s14, s13
	s_mov_b32 s15, s13
	s_mul_i32 s12, s11, 0xc3500
.Lw3t32:
	s_cbranch_execz .Lw3c32
.Lw3b32:
	s_lshl_b64 s[20:21], s[12:13], 2
	s_mov_b32 s12, s13
	v_mov_b64_e32 v[34:35], s[14:15]
	v_mov_b64_e32 v[32:33], s[12:13]
	s_add_u32 s20, s18, s20
	ds_write_b128 v83, v[32:35]
	ds_write_b128 v83, v[32:35] offset:16
	ds_write_b128 v83, v[32:35] offset:32
	ds_write_b128 v83, v[32:35] offset:48
	s_addc_u32 s21, s19, s21

.Lw3b33:
	v_mov_b32_e32 v116, 0x3f86a0
	s_waitcnt vmcnt(1)
	v_add_u32_e32 v32, v113, v80
	s_waitcnt vmcnt(0)
	v_cmp_lt_i32_e32 vcc, v32, v103
	s_and_saveexec_b64 s[14:15], vcc
	s_cbranch_execz .LBB3_20
	v_ashrrev_i32_e32 v33, 31, v32
	v_lshl_add_u64 v[32:33], v[32:33], 2, s[20:21]
	global_load_dword v116, v[32:33], off
.LBB3_20:
	s_or_b64 exec, exec, s[14:15]
	v_mov_b32_e32 v56, 0
.Lw3t34:
	s_cbranch_execz .Lw3c34
.Lw3b34:
	s_xor_b64 s[14:15], s[22:23], -1
	v_mov_b32_e32 v115, 31
	v_mov_b32_e32 v57, v56
	v_mov_b32_e32 v58, v56
	v_mov_b32_e32 v59, v56
	v_mov_b32_e32 v60, v56
	v_mov_b32_e32 v61, v56
	v_mov_b32_e32 v62, v56
	v_mov_b32_e32 v63, v56
	s_branch .LBB3_22

.LBB3_22:
	s_nop 2
	v_mov_b32_e32 v104, v63
.Lw3t35:
	s_cbranch_execz .Lw3c35
.Lw3b35:
	v_mov_b32_e32 v106, v62
	v_mov_b32_e32 v105, v61
	v_mov_b32_e32 v108, v60
	v_mov_b32_e32 v109, v59
	v_mov_b32_e32 v111, v58
	v_mov_b32_e32 v110, v57
	v_mov_b32_e32 v112, v56
	v_mov_b32_e32 v107, v115
	v_cmp_lt_i32_e32 vcc, v113, v103
	s_cbranch_vccz .LBB3_21
	v_or_b32_e32 v32, 4, v82
	s_waitcnt vmcnt(0)
	ds_bpermute_b32 v66, v82, v116
	ds_bpermute_b32 v123, v32, v116

.Lw3b36:
	v_or_b32_e32 v32, 8, v82
	v_or_b32_e32 v34, 12, v82
	ds_bpermute_b32 v122, v32, v116
	ds_bpermute_b32 v121, v34, v116
	v_or_b32_e32 v34, 16, v82
	ds_bpermute_b32 v120, v34, v116
	v_or_b32_e32 v34, 20, v82
	ds_bpermute_b32 v119, v34, v116
	s_waitcnt lgkmcnt(5)
	v_lshlrev_b32_e32 v32, 8, v66

.Lw3b37:
	s_waitcnt lgkmcnt(4)
	v_lshlrev_b32_e32 v33, 8, v123
	v_and_or_b32 v32, v32, s27, v81
	v_and_or_b32 v33, v33, s27, v81
	ds_bpermute_b32 v118, v85, v116
	ds_bpermute_b32 v117, v86, v116
	global_load_dwordx4 v[60:63], v32, s[8:9]
	global_load_dwordx4 v[56:59], v33, s[8:9]
	s_waitcnt lgkmcnt(5)

.Lw3b38:
	v_lshlrev_b32_e32 v32, 8, v122
	s_waitcnt lgkmcnt(4)
	v_lshlrev_b32_e32 v33, 8, v121
	v_and_or_b32 v32, v32, s27, v81
	v_and_or_b32 v33, v33, s27, v81
	global_load_dwordx4 v[52:55], v32, s[8:9]
	global_load_dwordx4 v[48:51], v33, s[8:9]
	s_waitcnt lgkmcnt(3)
	v_lshlrev_b32_e32 v32, 8, v120
	s_waitcnt lgkmcnt(2)
	v_lshlrev_b32_e32 v33, 8, v119

.Lw3b39:
	v_and_or_b32 v32, v32, s27, v81
	v_and_or_b32 v33, v33, s27, v81
	global_load_dwordx4 v[44:47], v32, s[8:9]
	global_load_dwordx4 v[40:43], v33, s[8:9]
	s_waitcnt lgkmcnt(1)
	v_lshlrev_b32_e32 v32, 8, v118
	s_waitcnt lgkmcnt(0)
	v_lshlrev_b32_e32 v33, 8, v117
	v_and_or_b32 v32, v32, s27, v81
	v_and_or_b32 v33, v33, s27, v81

.Lw3b40:
	global_load_dwordx4 v[36:39], v32, s[8:9]
	s_nop 0
	global_load_dwordx4 v[32:35], v33, s[8:9]
	v_or_b32_e32 v64, 16, v80
	v_add_u32_e32 v64, v64, v113
	v_cmp_lt_i32_e32 vcc, v64, v103
	v_mov_b32_e32 v114, 0x3f86a0
	s_and_saveexec_b64 s[22:23], vcc
	s_cbranch_execz .LBB3_25
	v_ashrrev_i32_e32 v65, 31, v64
	v_lshl_add_u64 v[64:65], v[64:65], 2, s[20:21]

.Lw3b41:
	global_load_dword v114, v[64:65], off
.LBB3_25:
	s_or_b64 exec, exec, s[22:23]
	v_ashrrev_i32_e32 v124, 17, v66
	v_cmp_ne_u32_e32 vcc, v124, v107
	s_cmp_lg_u64 vcc, 0
	s_cselect_b64 s[22:23], -1, 0
	s_and_b64 s[24:25], s[22:23], vcc
	v_mov_b32_e32 v115, v107
	v_mov_b32_e32 v68, v112
	v_mov_b32_e32 v69, v110
	v_mov_b32_e32 v70, v111
	v_mov_b32_e32 v71, v109
	v_mov_b32_e32 v64, v108
.Lw3t42:
	s_cbranch_execz .Lw3c42
.Lw3b42:
	v_mov_b32_e32 v65, v105
	v_mov_b32_e32 v66, v106
	v_mov_b32_e32 v67, v104
	s_and_saveexec_b64 s[22:23], s[24:25]
	s_cbranch_execz .LBB3_29
	v_cmp_gt_i32_e32 vcc, 16, v107
	s_and_saveexec_b64 s[24:25], vcc
	s_cbranch_execz .LBB3_28
	v_cvt_pk_f16_f32 v67, v111, v109
	v_cvt_pk_f16_f32 v66, v112, v110
	v_cvt_pk_f16_f32 v65, v106, v104
	v_cvt_pk_f16_f32 v64, v108, v105

.Lw3b43:
	v_mad_u64_u32 v[68:69], s[30:31], v107, s26, v[76:77]
	ds_write_b128 v68, v[64:67]
.LBB3_28:
	s_or_b64 exec, exec, s[24:25]
	v_mov_b32_e32 v68, 0
	v_mov_b32_e32 v115, v124
	v_mov_b32_e32 v69, v68
	v_mov_b32_e32 v70, v68
	v_mov_b32_e32 v71, v68
	v_mov_b32_e32 v64, v68
	v_mov_b32_e32 v65, v68
	v_mov_b32_e32 v66, v68
	v_mov_b32_e32 v67, v68
.LBB3_29:
.Lw3t44:
	s_cbranch_execz .Lw3c44
.Lw3b44:
	s_or_b64 exec, exec, s[22:23]
	v_ashrrev_i32_e32 v123, 17, v123
	s_waitcnt vmcnt(7)
	v_mfma_f32_16x16x16_f16 v[64:67], v[72:73], v[60:61], v[64:67]
	v_cmp_ne_u32_e32 vcc, v123, v115
	s_cmp_lg_u64 vcc, 0
	s_cselect_b64 s[22:23], -1, 0
	v_mfma_f32_16x16x16_f16 v[60:63], v[72:73], v[62:63], v[68:71]
	s_and_b64 s[24:25], s[22:23], vcc
	s_and_saveexec_b64 s[22:23], s[24:25]
	s_cbranch_execz .LBB3_33
	v_cmp_gt_i32_e32 vcc, 16, v115
	s_and_saveexec_b64 s[24:25], vcc

.Lw3b45:
	s_cbranch_execz .LBB3_32
	s_nop 1
	v_cvt_pk_f16_f32 v63, v62, v63
	v_cvt_pk_f16_f32 v62, v60, v61
	v_cvt_pk_f16_f32 v61, v66, v67
	v_cvt_pk_f16_f32 v60, v64, v65
	v_mad_u64_u32 v[64:65], s[30:31], v115, s26, v[76:77]
	ds_write_b128 v64, v[60:63]
.LBB3_32:
	s_or_b64 exec, exec, s[24:25]
.Lw3t46:
	s_cbranch_execz .Lw3c46
.Lw3b46:
	s_nop 0
	v_mov_b32_e32 v60, 0
	v_mov_b32_e32 v115, v123
	v_mov_b32_e32 v61, v60
	v_mov_b32_e32 v62, v60
	v_mov_b32_e32 v63, v60
	v_mov_b32_e32 v64, v60
	v_mov_b32_e32 v65, v60
	v_mov_b32_e32 v66, v60
	v_mov_b32_e32 v67, v60
.LBB3_33:
	s_or_b64 exec, exec, s[22:23]
	v_ashrrev_i32_e32 v68, 17, v122
	s_waitcnt vmcnt(6)
	v_mfma_f32_16x16x16_f16 v[64:67], v[72:73], v[56:57], v[64:67]
.Lw3t47:
	s_cbranch_execz .Lw3c47
.Lw3b47:
	v_cmp_ne_u32_e32 vcc, v68, v115
	s_cmp_lg_u64 vcc, 0
	s_cselect_b64 s[22:23], -1, 0
	v_mfma_f32_16x16x16_f16 v[56:59], v[72:73], v[58:59], v[60:63]
	s_and_b64 s[24:25], s[22:23], vcc
	s_and_saveexec_b64 s[22:23], s[24:25]
	s_cbranch_execz .LBB3_37
	v_cmp_gt_i32_e32 vcc, 16, v115
	s_and_saveexec_b64 s[24:25], vcc
	s_cbranch_execz .LBB3_36
	s_nop 1
	v_cvt_pk_f16_f32 v59, v58, v59
	v_cvt_pk_f16_f32 v58, v56, v57

.Lw3b48:
	v_cvt_pk_f16_f32 v57, v66, v67
	v_cvt_pk_f16_f32 v56, v64, v65
	v_mad_u64_u32 v[60:61], s[30:31], v115, s26, v[76:77]
	ds_write_b128 v60, v[56:59]
.LBB3_36:
	s_or_b64 exec, exec, s[24:25]
	s_nop 0
	v_mov_b32_e32 v56, 0
	v_mov_b32_e32 v115, v68
	v_mov_b32_e32 v57, v56
	v_mov_b32_e32 v58, v56
.Lw3t49:
	s_cbranch_execz .Lw3c49
.Lw3b49:
	v_mov_b32_e32 v59, v56
	v_mov_b32_e32 v64, v56
	v_mov_b32_e32 v65, v56
	v_mov_b32_e32 v66, v56
	v_mov_b32_e32 v67, v56
.LBB3_37:
	s_or_b64 exec, exec, s[22:23]
	v_ashrrev_i32_e32 v68, 17, v121
	s_waitcnt vmcnt(5)
	v_mfma_f32_16x16x16_f16 v[60:63], v[72:73], v[52:53], v[64:67]
	v_cmp_ne_u32_e32 vcc, v68, v115
	s_cmp_lg_u64 vcc, 0
	s_cselect_b64 s[22:23], -1, 0
	v_mfma_f32_16x16x16_f16 v[52:55], v[72:73], v[54:55], v[56:59]
.Lw3t50:
	s_cbranch_execz .Lw3c50
.Lw3b50:
	s_and_b64 s[24:25], s[22:23], vcc
	s_and_saveexec_b64 s[22:23], s[24:25]
	s_cbranch_execz .LBB3_41
	v_cmp_gt_i32_e32 vcc, 16, v115
	s_and_saveexec_b64 s[24:25], vcc
	s_cbranch_execz .LBB3_40
	s_nop 1
	v_cvt_pk_f16_f32 v55, v54, v55
	v_cvt_pk_f16_f32 v54, v52, v53
	v_cvt_pk_f16_f32 v53, v62, v63
	v_cvt_pk_f16_f32 v52, v60, v61

.Lw3b51:
	v_mad_u64_u32 v[56:57], s[30:31], v115, s26, v[76:77]
	ds_write_b128 v56, v[52:55]
.LBB3_40:
	s_or_b64 exec, exec, s[24:25]
	s_nop 0
	v_mov_b32_e32 v52, 0
	v_mov_b32_e32 v115, v68
	v_mov_b32_e32 v53, v52
	v_mov_b32_e32 v54, v52
	v_mov_b32_e32 v55, v52
	v_mov_b32_e32 v60, v52
	v_mov_b32_e32 v61, v52
	v_mov_b32_e32 v62, v52
	v_mov_b32_e32 v63, v52
.LBB3_41:
.Lw3t52:
	s_cbranch_execz .Lw3c52
.Lw3b52:
	s_or_b64 exec, exec, s[22:23]
	v_ashrrev_i32_e32 v64, 17, v120
	s_waitcnt vmcnt(4)
	v_mfma_f32_16x16x16_f16 v[56:59], v[72:73], v[48:49], v[60:63]
	v_cmp_ne_u32_e32 vcc, v64, v115
	s_cmp_lg_u64 vcc, 0
	s_cselect_b64 s[22:23], -1, 0
	v_mfma_f32_16x16x16_f16 v[48:51], v[72:73], v[50:51], v[52:55]
	s_and_b64 s[24:25], s[22:23], vcc
	s_and_saveexec_b64 s[22:23], s[24:25]
	s_cbranch_execz .LBB3_45
	v_cmp_gt_i32_e32 vcc, 16, v115
	s_and_saveexec_b64 s[24:25], vcc

.Lw3b53:
	s_cbranch_execz .LBB3_44
	s_nop 1
	v_cvt_pk_f16_f32 v51, v50, v51
	v_cvt_pk_f16_f32 v50, v48, v49
	v_cvt_pk_f16_f32 v49, v58, v59
	v_cvt_pk_f16_f32 v48, v56, v57
	v_mad_u64_u32 v[52:53], s[30:31], v115, s26, v[76:77]
	ds_write_b128 v52, v[48:51]
.LBB3_44:
	s_or_b64 exec, exec, s[24:25]
.Lw3t54:
	s_cbranch_execz .Lw3c54
.Lw3b54:
	s_nop 0
	v_mov_b32_e32 v48, 0
	v_mov_b32_e32 v115, v64
	v_mov_b32_e32 v49, v48
	v_mov_b32_e32 v50, v48
	v_mov_b32_e32 v51, v48
	v_mov_b32_e32 v56, v48
	v_mov_b32_e32 v57, v48
	v_mov_b32_e32 v58, v48
	v_mov_b32_e32 v59, v48
.LBB3_45:
	s_or_b64 exec, exec, s[22:23]
	v_ashrrev_i32_e32 v60, 17, v119
	s_waitcnt vmcnt(3)
	v_mfma_f32_16x16x16_f16 v[52:55], v[72:73], v[44:45], v[56:59]
.Lw3t55:
	s_cbranch_execz .Lw3c55
.Lw3b55:
	v_cmp_ne_u32_e32 vcc, v60, v115
	s_cmp_lg_u64 vcc, 0
	s_cselect_b64 s[22:23], -1, 0
	v_mfma_f32_16x16x16_f16 v[44:47], v[72:73], v[46:47], v[48:51]
	s_and_b64 s[24:25], s[22:23], vcc
	s_and_saveexec_b64 s[22:23], s[24:25]
	s_cbranch_execz .LBB3_49
	v_cmp_gt_i32_e32 vcc, 16, v115
	s_and_saveexec_b64 s[24:25], vcc
	s_cbranch_execz .LBB3_48
	s_nop 1
	v_cvt_pk_f16_f32 v47, v46, v47
	v_cvt_pk_f16_f32 v46, v44, v45

.Lw3b56:
	v_cvt_pk_f16_f32 v45, v54, v55
	v_cvt_pk_f16_f32 v44, v52, v53
	v_mad_u64_u32 v[48:49], s[30:31], v115, s26, v[76:77]
	ds_write_b128 v48, v[44:47]
.LBB3_48:
	s_or_b64 exec, exec, s[24:25]
	s_nop 0
	v_mov_b32_e32 v44, 0
	v_mov_b32_e32 v115, v60
	v_mov_b32_e32 v45, v44
	v_mov_b32_e32 v46, v44
.Lw3t57:
	s_cbranch_execz .Lw3c57
.Lw3b57:
	v_mov_b32_e32 v47, v44
	v_mov_b32_e32 v52, v44
	v_mov_b32_e32 v53, v44
	v_mov_b32_e32 v54, v44
	v_mov_b32_e32 v55, v44
.LBB3_49:
	s_or_b64 exec, exec, s[22:23]
	v_ashrrev_i32_e32 v56, 17, v118
	s_waitcnt vmcnt(2)
	v_mfma_f32_16x16x16_f16 v[48:51], v[72:73], v[40:41], v[52:55]
	v_cmp_ne_u32_e32 vcc, v56, v115
	s_cmp_lg_u64 vcc, 0
	s_cselect_b64 s[22:23], -1, 0
	v_mfma_f32_16x16x16_f16 v[40:43], v[72:73], v[42:43], v[44:47]
.Lw3t58:
	s_cbranch_execz .Lw3c58
.Lw3b58:
	s_and_b64 s[24:25], s[22:23], vcc
	s_and_saveexec_b64 s[22:23], s[24:25]
	s_cbranch_execz .LBB3_53
	v_cmp_gt_i32_e32 vcc, 16, v115
	s_and_saveexec_b64 s[24:25], vcc
	s_cbranch_execz .LBB3_52
	s_nop 1
	v_cvt_pk_f16_f32 v43, v42, v43
	v_cvt_pk_f16_f32 v42, v40, v41
	v_cvt_pk_f16_f32 v41, v50, v51
	v_cvt_pk_f16_f32 v40, v48, v49

.Lw3b59:
	v_mad_u64_u32 v[44:45], s[30:31], v115, s26, v[76:77]
	ds_write_b128 v44, v[40:43]
.LBB3_52:
	s_or_b64 exec, exec, s[24:25]
	s_nop 0
	v_mov_b32_e32 v40, 0
	v_mov_b32_e32 v115, v56
	v_mov_b32_e32 v41, v40
	v_mov_b32_e32 v42, v40
	v_mov_b32_e32 v43, v40
	v_mov_b32_e32 v48, v40
	v_mov_b32_e32 v49, v40
	v_mov_b32_e32 v50, v40
	v_mov_b32_e32 v51, v40
.LBB3_53:
.Lw3t60:
	s_cbranch_execz .Lw3c60
.Lw3b60:
	s_or_b64 exec, exec, s[22:23]
	v_ashrrev_i32_e32 v52, 17, v117
	s_waitcnt vmcnt(1)
	v_mfma_f32_16x16x16_f16 v[44:47], v[72:73], v[36:37], v[48:51]
	v_cmp_ne_u32_e32 vcc, v52, v115
	s_cmp_lg_u64 vcc, 0
	s_cselect_b64 s[22:23], -1, 0
	v_mfma_f32_16x16x16_f16 v[36:39], v[72:73], v[38:39], v[40:43]
	s_and_b64 s[24:25], s[22:23], vcc
	s_and_saveexec_b64 s[22:23], s[24:25]
	s_cbranch_execz .LBB3_57
	v_cmp_gt_i32_e32 vcc, 16, v115
	s_and_saveexec_b64 s[24:25], vcc

.Lw3b61:
	s_cbranch_execz .LBB3_56
	s_nop 1
	v_cvt_pk_f16_f32 v39, v38, v39
	v_cvt_pk_f16_f32 v38, v36, v37
	v_cvt_pk_f16_f32 v37, v46, v47
	v_cvt_pk_f16_f32 v36, v44, v45
	v_mad_u64_u32 v[40:41], s[30:31], v115, s26, v[76:77]
	ds_write_b128 v40, v[36:39]
.LBB3_56:
	s_or_b64 exec, exec, s[24:25]
.Lw3t62:
	s_cbranch_execz .Lw3c62
.Lw3b62:
	s_nop 0
	v_mov_b32_e32 v36, 0
	v_mov_b32_e32 v115, v52
	v_mov_b32_e32 v37, v36
	v_mov_b32_e32 v38, v36
	v_mov_b32_e32 v39, v36
	v_mov_b32_e32 v44, v36
	v_mov_b32_e32 v45, v36
	v_mov_b32_e32 v46, v36
	v_mov_b32_e32 v47, v36
.LBB3_57:
	s_or_b64 exec, exec, s[22:23]
	s_waitcnt vmcnt(0)
	v_mfma_f32_16x16x16_f16 v[60:63], v[72:73], v[32:33], v[44:47]
	v_add_u32_e32 v32, 8, v113
.Lw3t63:
	s_cbranch_execz .Lw3c63
.Lw3b63:
	v_cmp_lt_i32_e32 vcc, v32, v103
	v_mfma_f32_16x16x16_f16 v[56:59], v[72:73], v[34:35], v[36:39]
	s_cbranch_vccz .LBB3_91
	ds_bpermute_b32 v123, v87, v116
	ds_bpermute_b32 v122, v88, v116
	ds_bpermute_b32 v121, v89, v116
	ds_bpermute_b32 v120, v90, v116
	ds_bpermute_b32 v119, v91, v116
	ds_bpermute_b32 v118, v92, v116

.Lw3b64:
	s_waitcnt lgkmcnt(5)
	v_lshlrev_b32_e32 v32, 8, v123
	s_waitcnt lgkmcnt(4)
	v_lshlrev_b32_e32 v33, 8, v122
	v_and_or_b32 v32, v32, s27, v81
	v_and_or_b32 v33, v33, s27, v81
	ds_bpermute_b32 v117, v93, v116
	ds_bpermute_b32 v116, v94, v116
	global_load_dwordx4 v[68:71], v32, s[8:9]

.Lw3b65:
	global_load_dwordx4 v[64:67], v33, s[8:9]
	s_waitcnt lgkmcnt(5)
	v_lshlrev_b32_e32 v32, 8, v121
	s_waitcnt lgkmcnt(4)
	v_lshlrev_b32_e32 v33, 8, v120
	v_and_or_b32 v32, v32, s27, v81
	v_and_or_b32 v33, v33, s27, v81
	global_load_dwordx4 v[52:55], v32, s[8:9]
	global_load_dwordx4 v[48:51], v33, s[8:9]
	s_waitcnt lgkmcnt(3)

.Lw3b66:
	v_lshlrev_b32_e32 v32, 8, v119
	s_waitcnt lgkmcnt(2)
	v_lshlrev_b32_e32 v33, 8, v118
	v_and_or_b32 v32, v32, s27, v81
	v_and_or_b32 v33, v33, s27, v81
	global_load_dwordx4 v[44:47], v32, s[8:9]
	global_load_dwordx4 v[40:43], v33, s[8:9]
	s_waitcnt lgkmcnt(1)
	v_lshlrev_b32_e32 v32, 8, v117
	s_waitcnt lgkmcnt(0)
	v_lshlrev_b32_e32 v33, 8, v116

.Lw3b67:
	v_and_or_b32 v32, v32, s27, v81
	v_and_or_b32 v33, v33, s27, v81
	global_load_dwordx4 v[36:39], v32, s[8:9]
	s_nop 0
	global_load_dwordx4 v[32:35], v33, s[8:9]
	v_ashrrev_i32_e32 v123, 17, v123
	v_cmp_ne_u32_e32 vcc, v123, v115
	s_cmp_lg_u64 vcc, 0
	s_cselect_b64 s[22:23], -1, 0
	s_and_b64 s[24:25], s[22:23], vcc
	s_and_saveexec_b64 s[22:23], s[24:25]

.Lw3b68:
	s_cbranch_execz .LBB3_62
	v_cmp_gt_i32_e32 vcc, 16, v115
	s_and_saveexec_b64 s[24:25], vcc
	s_cbranch_execz .LBB3_61
	v_cvt_pk_f16_f32 v59, v58, v59
	v_cvt_pk_f16_f32 v58, v56, v57
	v_cvt_pk_f16_f32 v57, v62, v63
	v_cvt_pk_f16_f32 v56, v60, v61
	v_mad_u64_u32 v[60:61], s[30:31], v115, s26, v[76:77]
	ds_write_b128 v60, v[56:59]

.LBB3_62:
	s_or_b64 exec, exec, s[22:23]
	v_ashrrev_i32_e32 v122, 17, v122
	s_waitcnt vmcnt(7)
	v_mfma_f32_16x16x16_f16 v[60:63], v[72:73], v[68:69], v[60:63]
.Lw3t70:
	s_cbranch_execz .Lw3c70
.Lw3b70:
	v_cmp_ne_u32_e32 vcc, v122, v115
	s_cmp_lg_u64 vcc, 0
	s_cselect_b64 s[22:23], -1, 0
	v_mfma_f32_16x16x16_f16 v[56:59], v[72:73], v[70:71], v[56:59]
	s_and_b64 s[24:25], s[22:23], vcc
	s_and_saveexec_b64 s[22:23], s[24:25]
	s_cbranch_execz .LBB3_66
	v_cmp_gt_i32_e32 vcc, 16, v115
	s_and_saveexec_b64 s[24:25], vcc
	s_cbranch_execz .LBB3_65
	s_nop 1
	v_cvt_pk_f16_f32 v59, v58, v59

.Lw3b71:
	v_cvt_pk_f16_f32 v58, v56, v57
	v_cvt_pk_f16_f32 v57, v62, v63
	v_cvt_pk_f16_f32 v56, v60, v61
	v_mad_u64_u32 v[60:61], s[30:31], v115, s26, v[76:77]
	ds_write_b128 v60, v[56:59]
.LBB3_65:
	s_or_b64 exec, exec, s[24:25]
	s_nop 0
	v_mov_b32_e32 v56, 0
	v_mov_b32_e32 v115, v122
	v_mov_b32_e32 v57, v56
.Lw3t72:
	s_cbranch_execz .Lw3c72
.Lw3b72:
	v_mov_b32_e32 v58, v56
	v_mov_b32_e32 v59, v56
	v_mov_b32_e32 v60, v56
	v_mov_b32_e32 v61, v56
	v_mov_b32_e32 v62, v56
	v_mov_b32_e32 v63, v56
.LBB3_66:
	s_or_b64 exec, exec, s[22:23]
	v_ashrrev_i32_e32 v68, 17, v121
	s_waitcnt vmcnt(6)
	v_mfma_f32_16x16x16_f16 v[60:63], v[72:73], v[64:65], v[60:63]
	v_cmp_ne_u32_e32 vcc, v68, v115
	s_cmp_lg_u64 vcc, 0
	s_cselect_b64 s[22:23], -1, 0
	v_mfma_f32_16x16x16_f16 v[56:59], v[72:73], v[66:67], v[56:59]
.Lw3t73:
	s_cbranch_execz .Lw3c73
.Lw3b73:
	s_and_b64 s[24:25], s[22:23], vcc
	s_and_saveexec_b64 s[22:23], s[24:25]
	s_cbranch_execz .LBB3_70
	v_cmp_gt_i32_e32 vcc, 16, v115
	s_and_saveexec_b64 s[24:25], vcc
	s_cbranch_execz .LBB3_69
	s_nop 1
	v_cvt_pk_f16_f32 v59, v58, v59
	v_cvt_pk_f16_f32 v58, v56, v57
	v_cvt_pk_f16_f32 v57, v62, v63
	v_cvt_pk_f16_f32 v56, v60, v61

.Lw3b74:
	v_mad_u64_u32 v[60:61], s[30:31], v115, s26, v[76:77]
	ds_write_b128 v60, v[56:59]
.LBB3_69:
	s_or_b64 exec, exec, s[24:25]
	s_nop 0
	v_mov_b32_e32 v56, 0
	v_mov_b32_e32 v115, v68
	v_mov_b32_e32 v57, v56
	v_mov_b32_e32 v58, v56
	v_mov_b32_e32 v59, v56
	v_mov_b32_e32 v60, v56
	v_mov_b32_e32 v61, v56
	v_mov_b32_e32 v62, v56
.Lw3t75:
	s_cbranch_execz .Lw3c75

.LBB3_70:
	s_or_b64 exec, exec, s[22:23]
	v_ashrrev_i32_e32 v64, 17, v120
	s_waitcnt vmcnt(5)
	v_mfma_f32_16x16x16_f16 v[60:63], v[72:73], v[52:53], v[60:63]
	v_cmp_ne_u32_e32 vcc, v64, v115
	s_cmp_lg_u64 vcc, 0
	s_cselect_b64 s[22:23], -1, 0
	v_mfma_f32_16x16x16_f16 v[52:55], v[72:73], v[54:55], v[56:59]
	s_and_b64 s[24:25], s[22:23], vcc
	s_and_saveexec_b64 s[22:23], s[24:25]
	s_cbranch_execz .LBB3_74
	v_cmp_gt_i32_e32 vcc, 16, v115

.Lw3b76:
	s_and_saveexec_b64 s[24:25], vcc
	s_cbranch_execz .LBB3_73
	s_nop 1
	v_cvt_pk_f16_f32 v55, v54, v55
	v_cvt_pk_f16_f32 v54, v52, v53
	v_cvt_pk_f16_f32 v53, v62, v63
	v_cvt_pk_f16_f32 v52, v60, v61
	v_mad_u64_u32 v[56:57], s[30:31], v115, s26, v[76:77]
	ds_write_b128 v56, v[52:55]

.LBB3_74:
	s_or_b64 exec, exec, s[22:23]
	v_ashrrev_i32_e32 v64, 17, v119
	s_waitcnt vmcnt(4)
	v_mfma_f32_16x16x16_f16 v[56:59], v[72:73], v[48:49], v[60:63]
.Lw3t78:
	s_cbranch_execz .Lw3c78
.Lw3b78:
	v_cmp_ne_u32_e32 vcc, v64, v115
	s_cmp_lg_u64 vcc, 0
	s_cselect_b64 s[22:23], -1, 0
	v_mfma_f32_16x16x16_f16 v[48:51], v[72:73], v[50:51], v[52:55]
	s_and_b64 s[24:25], s[22:23], vcc
	s_and_saveexec_b64 s[22:23], s[24:25]
	s_cbranch_execz .LBB3_78
	v_cmp_gt_i32_e32 vcc, 16, v115
	s_and_saveexec_b64 s[24:25], vcc
	s_cbranch_execz .LBB3_77
	s_nop 1
	v_cvt_pk_f16_f32 v51, v50, v51

.Lw3b79:
	v_cvt_pk_f16_f32 v50, v48, v49
	v_cvt_pk_f16_f32 v49, v58, v59
	v_cvt_pk_f16_f32 v48, v56, v57
	v_mad_u64_u32 v[52:53], s[30:31], v115, s26, v[76:77]
	ds_write_b128 v52, v[48:51]
.LBB3_77:
	s_or_b64 exec, exec, s[24:25]
	s_nop 0
	v_mov_b32_e32 v48, 0
	v_mov_b32_e32 v115, v64
	v_mov_b32_e32 v49, v48
.Lw3t80:
	s_cbranch_execz .Lw3c80
.Lw3b80:
	v_mov_b32_e32 v50, v48
	v_mov_b32_e32 v51, v48
	v_mov_b32_e32 v56, v48
	v_mov_b32_e32 v57, v48
	v_mov_b32_e32 v58, v48
	v_mov_b32_e32 v59, v48
.LBB3_78:
	s_or_b64 exec, exec, s[22:23]
	v_ashrrev_i32_e32 v60, 17, v118
	s_waitcnt vmcnt(3)
	v_mfma_f32_16x16x16_f16 v[52:55], v[72:73], v[44:45], v[56:59]
	v_cmp_ne_u32_e32 vcc, v60, v115
	s_cmp_lg_u64 vcc, 0
	s_cselect_b64 s[22:23], -1, 0
	v_mfma_f32_16x16x16_f16 v[44:47], v[72:73], v[46:47], v[48:51]
.Lw3t81:
	s_cbranch_execz .Lw3c81
.Lw3b81:
	s_and_b64 s[24:25], s[22:23], vcc
	s_and_saveexec_b64 s[22:23], s[24:25]
	s_cbranch_execz .LBB3_82
	v_cmp_gt_i32_e32 vcc, 16, v115
	s_and_saveexec_b64 s[24:25], vcc
	s_cbranch_execz .LBB3_81
	s_nop 1
	v_cvt_pk_f16_f32 v47, v46, v47
	v_cvt_pk_f16_f32 v46, v44, v45
	v_cvt_pk_f16_f32 v45, v54, v55
	v_cvt_pk_f16_f32 v44, v52, v53

.Lw3b82:
	v_mad_u64_u32 v[48:49], s[30:31], v115, s26, v[76:77]
	ds_write_b128 v48, v[44:47]
.LBB3_81:
	s_or_b64 exec, exec, s[24:25]
	s_nop 0
	v_mov_b32_e32 v44, 0
	v_mov_b32_e32 v115, v60
	v_mov_b32_e32 v45, v44
	v_mov_b32_e32 v46, v44
	v_mov_b32_e32 v47, v44
	v_mov_b32_e32 v52, v44
	v_mov_b32_e32 v53, v44
	v_mov_b32_e32 v54, v44
.Lw3t83:
	s_cbranch_execz .Lw3c83
.Lw3b83:
	v_mov_b32_e32 v55, v44
.LBB3_82:
	s_or_b64 exec, exec, s[22:23]
	v_ashrrev_i32_e32 v56, 17, v117
	s_waitcnt vmcnt(2)
	v_mfma_f32_16x16x16_f16 v[48:51], v[72:73], v[40:41], v[52:55]
	v_cmp_ne_u32_e32 vcc, v56, v115
	s_cmp_lg_u64 vcc, 0
	s_cselect_b64 s[22:23], -1, 0
	v_mfma_f32_16x16x16_f16 v[40:43], v[72:73], v[42:43], v[44:47]
	s_and_b64 s[24:25], s[22:23], vcc
	s_and_saveexec_b64 s[22:23], s[24:25]
	s_cbranch_execz .LBB3_86
	v_cmp_gt_i32_e32 vcc, 16, v115

.Lw3b84:
	s_and_saveexec_b64 s[24:25], vcc
	s_cbranch_execz .LBB3_85
	s_nop 1
	v_cvt_pk_f16_f32 v43, v42, v43
	v_cvt_pk_f16_f32 v42, v40, v41
	v_cvt_pk_f16_f32 v41, v50, v51
	v_cvt_pk_f16_f32 v40, v48, v49
	v_mad_u64_u32 v[44:45], s[30:31], v115, s26, v[76:77]
	ds_write_b128 v44, v[40:43]

.Lw3b85:
	s_or_b64 exec, exec, s[24:25]
	s_nop 0
	v_mov_b32_e32 v40, 0
	v_mov_b32_e32 v115, v56
	v_mov_b32_e32 v41, v40
	v_mov_b32_e32 v42, v40
	v_mov_b32_e32 v43, v40
	v_mov_b32_e32 v48, v40
	v_mov_b32_e32 v49, v40
	v_mov_b32_e32 v50, v40
	v_mov_b32_e32 v51, v40
.LBB3_86:
	s_or_b64 exec, exec, s[22:23]
	v_ashrrev_i32_e32 v52, 17, v116
	s_waitcnt vmcnt(1)
	v_mfma_f32_16x16x16_f16 v[44:47], v[72:73], v[36:37], v[48:51]
.Lw3t86:
	s_cbranch_execz .Lw3c86
.Lw3b86:
	v_cmp_ne_u32_e32 vcc, v52, v115
	s_cmp_lg_u64 vcc, 0
	s_cselect_b64 s[22:23], -1, 0
	v_mfma_f32_16x16x16_f16 v[36:39], v[72:73], v[38:39], v[40:43]
	s_and_b64 s[24:25], s[22:23], vcc
	s_and_saveexec_b64 s[22:23], s[24:25]
	s_cbranch_execz .LBB3_90
	v_cmp_gt_i32_e32 vcc, 16, v115
	s_and_saveexec_b64 s[24:25], vcc
	s_cbranch_execz .LBB3_89
	s_nop 1
	v_cvt_pk_f16_f32 v39, v38, v39

.Lw3b87:
	v_cvt_pk_f16_f32 v38, v36, v37
	v_cvt_pk_f16_f32 v37, v46, v47
	v_cvt_pk_f16_f32 v36, v44, v45
	v_mad_u64_u32 v[40:41], s[30:31], v115, s26, v[76:77]
	ds_write_b128 v40, v[36:39]
.LBB3_89:
	s_or_b64 exec, exec, s[24:25]
	s_nop 0
	v_mov_b32_e32 v36, 0
	v_mov_b32_e32 v115, v52
	v_mov_b32_e32 v37, v36
.Lw3t88:
	s_cbranch_execz .Lw3c88
.Lw3b88:
	v_mov_b32_e32 v38, v36
	v_mov_b32_e32 v39, v36
	v_mov_b32_e32 v44, v36
	v_mov_b32_e32 v45, v36
	v_mov_b32_e32 v46, v36
	v_mov_b32_e32 v47, v36

.LBB3_91:
	v_mov_b32_e32 v113, v32
	v_mov_b32_e32 v116, v114
.Lw3t89:
	s_cbranch_execz .Lw3c89

.LBB3_92:
	v_cmp_gt_i32_e32 vcc, 16, v107
	s_and_saveexec_b64 s[20:21], vcc
	s_cbranch_execz .LBB3_17
	v_cvt_pk_f16_f32 v35, v111, v109
	v_cvt_pk_f16_f32 v34, v112, v110
	v_cvt_pk_f16_f32 v33, v106, v104
	v_cvt_pk_f16_f32 v32, v108, v105
	v_mad_u64_u32 v[36:37], s[22:23], v107, s26, v[76:77]
	ds_write_b128 v36, v[32:35]

.LBB3_94:
	v_mov_b32_e32 v32, v28
	v_mov_b32_e32 v33, v24
	v_mov_b32_e32 v34, v29
	v_mov_b32_e32 v35, v25
	v_pk_add_f32 v[32:33], v[32:33], v[34:35]
	v_mov_b32_e32 v34, v30
	v_mov_b32_e32 v35, v26
	v_mov_b32_e32 v36, v31
	v_mov_b32_e32 v37, v27
	v_pk_add_f32 v[34:35], v[34:35], v[36:37]
	v_mov_b32_e32 v36, v20

.Lw3b91:
	v_pk_add_f32 v[32:33], v[32:33], v[34:35]
	v_mov_b32_e32 v34, v21
	v_mov_b32_e32 v35, v22
	v_mov_b32_e32 v37, v23
	v_pk_add_f32 v[34:35], v[34:35], v[36:37]
	v_add_f32_e32 v32, 0, v32
	v_pk_add_f32 v[34:35], v[34:35], v[34:35] op_sel:[0,1] op_sel_hi:[1,0]
	v_add_f32_e32 v32, v32, v33
	v_add_f32_e32 v36, v16, v17
	v_add_f32_e32 v38, v18, v19
	v_mov_b32_e32 v33, v12
	v_mov_b32_e32 v35, v13

.Lw3b92:
	v_mov_b32_e32 v37, v14
	v_mov_b32_e32 v39, v15
	v_pk_add_f32 v[32:33], v[32:33], v[34:35]
	v_pk_add_f32 v[34:35], v[36:37], v[38:39]
	v_mov_b32_e32 v36, v8
	v_pk_add_f32 v[32:33], v[32:33], v[34:35]
	v_mov_b32_e32 v34, v9
	v_mov_b32_e32 v35, v10
	v_mov_b32_e32 v37, v11
	v_pk_add_f32 v[34:35], v[34:35], v[36:37]
	v_pk_add_f32 v[32:33], v[32:33], v[32:33] op_sel:[0,1] op_sel_hi:[1,0]

.Lw3b94:
	v_and_b32_e32 v34, 64, v100
	v_add_f32_e32 v32, v32, v33
	v_xor_b32_e32 v33, 16, v100
	v_add_u32_e32 v34, 64, v34
	v_cmp_lt_i32_e32 vcc, v33, v34
	s_nop 1
	v_cndmask_b32_e32 v33, v100, v33, vcc
	v_lshlrev_b32_e32 v40, 2, v33
	ds_bpermute_b32 v33, v40, v32
	s_waitcnt lgkmcnt(0)
	v_add_f32_e32 v32, v32, v33
	v_xor_b32_e32 v33, 32, v100
	v_cmp_lt_i32_e32 vcc, v33, v34

.Lw3b95:
	s_nop 1
	v_cndmask_b32_e32 v33, v100, v33, vcc
	v_lshlrev_b32_e32 v41, 2, v33
	ds_bpermute_b32 v33, v41, v32
	s_waitcnt lgkmcnt(0)
	v_add_f32_e32 v42, v32, v33
	v_fmamk_f32 v29, v42, 0xbc000000, v29
	v_fmamk_f32 v25, v42, 0xbc000000, v25
	v_fmamk_f32 v39, v42, 0xbc000000, v31
	v_fmamk_f32 v38, v42, 0xbc000000, v30

.Lw3b96:
	v_fmac_f32_e32 v28, 0xbc000000, v42
	v_fmamk_f32 v37, v42, 0xbc000000, v27
	v_fmac_f32_e32 v24, 0xbc000000, v42
	v_mov_b32_e32 v30, v29
	v_mov_b32_e32 v31, v25
	v_fmamk_f32 v36, v42, 0xbc000000, v26
	v_mov_b32_e32 v26, v28
	v_mov_b32_e32 v27, v24
	v_pk_mul_f32 v[30:31], v[30:31], v[30:31]
	v_mov_b32_e32 v32, v39

.Lw3b97:
	v_mov_b32_e32 v33, v37
	v_pk_fma_f32 v[26:27], v[26:27], v[26:27], v[30:31]
	v_mov_b32_e32 v30, v38
	v_mov_b32_e32 v31, v36
	v_pk_mul_f32 v[32:33], v[32:33], v[32:33]
	v_fmamk_f32 v35, v42, 0xbc000000, v21
	v_pk_fma_f32 v[30:31], v[30:31], v[30:31], v[32:33]
	v_fmamk_f32 v34, v42, 0xbc000000, v20
	v_fmamk_f32 v23, v42, 0xbc000000, v23

.Lw3b98:
	v_fmac_f32_e32 v22, 0xbc000000, v42
	v_pk_add_f32 v[26:27], v[26:27], v[30:31]
	v_pk_mul_f32 v[20:21], v[22:23], v[22:23]
	v_pk_mul_f32 v[30:31], v[34:35], v[34:35]
	v_fmamk_f32 v13, v42, 0xbc000000, v13
	v_pk_mov_b32 v[32:33], v[30:31], v[20:21] op_sel:[1,0]
	v_mov_b32_e32 v31, v21
	v_pk_add_f32 v[20:21], v[32:33], v[30:31]

.Lw3b99:
	v_fmac_f32_e32 v12, 0xbc000000, v42
	v_fmamk_f32 v33, v42, 0xbc000000, v19
	v_fmamk_f32 v32, v42, 0xbc000000, v18
	v_fmamk_f32 v19, v42, 0xbc000000, v15
	v_fmamk_f32 v18, v42, 0xbc000000, v14
	v_mul_f32_e32 v30, v12, v12
	v_mul_f32_e32 v31, v13, v13
	v_pk_add_f32 v[14:15], v[26:27], v[26:27] op_sel:[0,1] op_sel_hi:[1,0]
	v_pk_add_f32 v[20:21], v[20:21], v[20:21] op_sel:[0,1] op_sel_hi:[1,0]

.Lw3b100:
	v_fmamk_f32 v17, v42, 0xbc000000, v17
	v_mov_b32_e32 v15, v30
	v_mov_b32_e32 v21, v31
	v_fmac_f32_e32 v16, 0xbc000000, v42
	v_pk_add_f32 v[14:15], v[14:15], v[20:21]
	v_mul_f32_e32 v20, v17, v17
	v_mul_f32_e32 v26, v33, v33
	v_mul_f32_e32 v43, v18, v18
	v_mul_f32_e32 v44, v19, v19
	v_pk_fma_f32 v[20:21], v[16:17], v[16:17], v[20:21] op_sel_hi:[1,1,0]

.Lw3b101:
	v_pk_fma_f32 v[26:27], v[32:33], v[32:33], v[26:27] op_sel_hi:[1,1,0]
	v_mov_b32_e32 v21, v43
	v_mov_b32_e32 v27, v44
	v_pk_add_f32 v[20:21], v[20:21], v[26:27]
	v_fmamk_f32 v11, v42, 0xbc000000, v11
	v_pk_add_f32 v[14:15], v[14:15], v[20:21]
	v_fmamk_f32 v21, v42, 0xbc000000, v9
	v_fmamk_f32 v20, v42, 0xbc000000, v8
	v_fmac_f32_e32 v10, 0xbc000000, v42

.Lw3b102:
	v_pk_mul_f32 v[8:9], v[10:11], v[10:11]
	v_pk_mul_f32 v[26:27], v[20:21], v[20:21]
	v_fmamk_f32 v1, v42, 0xbc000000, v1
	v_pk_mov_b32 v[30:31], v[26:27], v[8:9] op_sel:[1,0]
	v_mov_b32_e32 v27, v9
	v_pk_add_f32 v[8:9], v[30:31], v[26:27]
	v_fmac_f32_e32 v0, 0xbc000000, v42
	v_fmamk_f32 v27, v42, 0xbc000000, v7

.Lw3b103:
	v_fmamk_f32 v26, v42, 0xbc000000, v6
	v_mul_f32_e32 v30, v0, v0
	v_mul_f32_e32 v31, v1, v1
	v_pk_add_f32 v[6:7], v[14:15], v[14:15] op_sel:[0,1] op_sel_hi:[1,0]
	v_pk_add_f32 v[8:9], v[8:9], v[8:9] op_sel:[0,1] op_sel_hi:[1,0]
	v_fmamk_f32 v5, v42, 0xbc000000, v5
	v_mov_b32_e32 v7, v30
	v_mov_b32_e32 v9, v31
	v_fmac_f32_e32 v4, 0xbc000000, v42

.Lw3b104:
	v_fmamk_f32 v3, v42, 0xbc000000, v3
	v_fmamk_f32 v2, v42, 0xbc000000, v2
	v_pk_add_f32 v[6:7], v[6:7], v[8:9]
	v_mul_f32_e32 v8, v5, v5
	v_mul_f32_e32 v14, v27, v27
	v_mul_f32_e32 v42, v2, v2
	v_mul_f32_e32 v43, v3, v3
	v_pk_fma_f32 v[8:9], v[4:5], v[4:5], v[8:9] op_sel_hi:[1,1,0]
	v_pk_fma_f32 v[14:15], v[26:27], v[26:27], v[14:15] op_sel_hi:[1,1,0]
	v_mov_b32_e32 v9, v42

.Lw3b105:
	v_mov_b32_e32 v15, v43
	v_pk_add_f32 v[8:9], v[8:9], v[14:15]
	s_nop 0
	v_pk_add_f32 v[6:7], v[6:7], v[8:9]
	s_nop 0
	v_add_f32_e32 v6, v6, v7
	ds_bpermute_b32 v7, v40, v6
	s_waitcnt lgkmcnt(0)
	v_add_f32_e32 v6, v6, v7
	ds_bpermute_b32 v7, v41, v6
	s_waitcnt lgkmcnt(0)

.Lw3b106:
	v_add_f32_e32 v6, v6, v7
	v_fmamk_f32 v6, v6, 0x3c000000, v98
	v_mul_f32_e32 v7, 0x4b800000, v6
	v_cmp_gt_f32_e32 vcc, s28, v6
	s_nop 1
	v_cndmask_b32_e32 v6, v6, v7, vcc
	v_rsq_f32_e32 v14, v6
	ds_read_b128 v[6:9], v96 offset:512
	ds_read_b128 v[40:43], v96 offset:528
	ds_read_b128 v[44:47], v96 offset:1024

.Lw3b107:
	ds_read_b128 v[48:51], v96 offset:1040
	v_mul_f32_e32 v15, 0x45800000, v14
	v_cndmask_b32_e32 v30, v14, v15, vcc
	v_pk_mul_f32 v[14:15], v[30:31], v[28:29] op_sel_hi:[0,1]
	s_waitcnt lgkmcnt(1)
	v_pk_fma_f32 v[6:7], v[6:7], v[14:15], v[44:45]
	v_pk_mul_f32 v[28:29], v[30:31], v[38:39] op_sel_hi:[0,1]
	v_pk_mul_f32 v[14:15], v[6:7], v[6:7]
	v_pk_fma_f32 v[8:9], v[8:9], v[28:29], v[46:47]

.Lw3b108:
	v_fmamk_f32 v14, v14, 0xbdd2d3e8, v99
	v_fmamk_f32 v15, v15, 0xbdd2d3e8, v99
	v_mul_f32_e32 v14, v6, v14
	v_mul_f32_e32 v15, v7, v15
	v_exp_f32_e32 v14, v14
	v_exp_f32_e32 v15, v15
	v_pk_mul_f32 v[28:29], v[8:9], v[8:9]
	v_add_f32_e32 v14, 1.0, v14
	v_add_f32_e32 v15, 1.0, v15
	v_rcp_f32_e32 v14, v14
	v_rcp_f32_e32 v15, v15

.Lw3b109:
	v_fmamk_f32 v28, v28, 0xbdd2d3e8, v99
	v_mul_f32_e32 v28, v8, v28
	v_exp_f32_e32 v28, v28
	v_pk_mul_f32 v[6:7], v[6:7], v[14:15]
	v_fmamk_f32 v14, v29, 0xbdd2d3e8, v99
	v_mul_f32_e32 v14, v9, v14
	v_exp_f32_e32 v29, v14
	v_pk_mul_f32 v[14:15], v[30:31], v[24:25] op_sel_hi:[0,1]
	s_waitcnt lgkmcnt(0)
	v_pk_fma_f32 v[14:15], v[40:41], v[14:15], v[48:49]

.Lw3b110:
	v_cvt_pk_f16_f32 v6, v6, v7
	v_pk_mul_f32 v[24:25], v[14:15], v[14:15]
	v_add_f32_e32 v7, 1.0, v28
	v_fmamk_f32 v24, v24, 0xbdd2d3e8, v99
	v_mul_f32_e32 v24, v14, v24
	v_exp_f32_e32 v24, v24
	v_rcp_f32_e32 v28, v7
	v_add_f32_e32 v7, 1.0, v29
	v_rcp_f32_e32 v29, v7
	v_add_f32_e32 v7, 1.0, v24
	v_fmamk_f32 v24, v25, 0xbdd2d3e8, v99

.Lw3b111:
	v_mul_f32_e32 v31, v15, v24
	v_pk_mul_f32 v[24:25], v[30:31], v[36:37] op_sel_hi:[0,1]
	v_pk_fma_f32 v[24:25], v[42:43], v[24:25], v[50:51]
	v_exp_f32_e32 v31, v31
	v_pk_mul_f32 v[36:37], v[24:25], v[24:25]
	v_rcp_f32_e32 v38, v7
	v_fmamk_f32 v36, v36, 0xbdd2d3e8, v99
	v_fmamk_f32 v37, v37, 0xbdd2d3e8, v99
	v_mul_f32_e32 v36, v24, v36
	v_mul_f32_e32 v37, v25, v37

.Lw3b112:
	v_exp_f32_e32 v36, v36
	v_exp_f32_e32 v37, v37
	v_add_f32_e32 v7, 1.0, v31
	v_mov_b32_e32 v31, v84
	v_add_f32_e32 v36, 1.0, v36
	v_add_f32_e32 v37, 1.0, v37
	v_rcp_f32_e32 v36, v36
	v_rcp_f32_e32 v37, v37
	v_rcp_f32_e32 v39, v7
	v_pk_mul_f32 v[8:9], v[8:9], v[28:29]
	v_pk_mul_f32 v[24:25], v[24:25], v[36:37]
	s_nop 0
	s_nop 0

.Lw3b113:
	v_lshl_add_u32 v7, v31, 2, v101
	v_add_u32_e32 v52, 0x420, v7
	v_add_u32_e32 v46, 0x428, v7
	v_add_u32_e32 v50, 0x430, v7
	ds_read2_b32 v[36:37], v7 offset0:138 offset1:139
	ds_read2_b32 v[40:41], v7 offset0:142 offset1:143
	ds_read2_b32 v[42:43], v7 offset0:140 offset1:141
	ds_read2_b32 v[44:45], v7 offset0:136 offset1:137

.Lw3b114:
	v_add_u32_e32 v7, 0x438, v7
	ds_read2_b32 v[46:47], v46 offset1:1
	ds_read2_b32 v[48:49], v7 offset1:1
	ds_read2_b32 v[50:51], v50 offset1:1
	ds_read2_b32 v[52:53], v52 offset1:1
	v_cvt_pk_f16_f32 v7, v8, v9
	v_pk_mul_f32 v[8:9], v[14:15], v[38:39]

.Lw3b115:
	s_nop 0
	v_cvt_pk_f16_f32 v8, v8, v9
	v_pk_mul_f32 v[14:15], v[30:31], v[34:35] op_sel_hi:[0,1]
	s_waitcnt lgkmcnt(0)
	v_pk_fma_f32 v[14:15], v[44:45], v[14:15], v[52:53]
	v_pk_mul_f32 v[22:23], v[30:31], v[22:23] op_sel_hi:[0,1]
	v_pk_mul_f32 v[28:29], v[14:15], v[14:15]
	v_pk_fma_f32 v[22:23], v[36:37], v[22:23], v[46:47]
	v_fmamk_f32 v9, v28, 0xbdd2d3e8, v99

.Lw3b116:
	v_mul_f32_e32 v9, v14, v9
	v_fmamk_f32 v28, v29, 0xbdd2d3e8, v99
	v_exp_f32_e32 v9, v9
	v_mul_f32_e32 v28, v15, v28
	v_exp_f32_e32 v29, v28
	v_pk_mul_f32 v[34:35], v[22:23], v[22:23]
	v_add_f32_e32 v9, 1.0, v9
	v_rcp_f32_e32 v28, v9
	v_add_f32_e32 v9, 1.0, v29
	v_rcp_f32_e32 v29, v9
	v_fmamk_f32 v9, v34, 0xbdd2d3e8, v99

.Lw3b117:
	v_mul_f32_e32 v9, v22, v9
	v_exp_f32_e32 v34, v9
	v_cvt_pk_f16_f32 v9, v24, v25
	v_fmamk_f32 v24, v35, 0xbdd2d3e8, v99
	v_pk_mul_f32 v[16:17], v[30:31], v[16:17] op_sel_hi:[0,1]
	v_mul_f32_e32 v24, v23, v24
	v_pk_fma_f32 v[16:17], v[42:43], v[16:17], v[50:51]
	v_pk_mul_f32 v[14:15], v[14:15], v[28:29]
	v_exp_f32_e32 v29, v24
	v_pk_mul_f32 v[24:25], v[16:17], v[16:17]

.Lw3b118:
	v_cvt_pk_f16_f32 v14, v14, v15
	v_fmamk_f32 v24, v24, 0xbdd2d3e8, v99
	v_mul_f32_e32 v24, v16, v24
	v_exp_f32_e32 v24, v24
	v_add_f32_e32 v15, 1.0, v34
	v_rcp_f32_e32 v28, v15
	v_add_f32_e32 v15, 1.0, v29
	v_rcp_f32_e32 v29, v15
	v_add_f32_e32 v15, 1.0, v24
	v_fmamk_f32 v24, v25, 0xbdd2d3e8, v99
	v_mul_f32_e32 v34, v17, v24

.Lw3b119:
	v_pk_mul_f32 v[24:25], v[30:31], v[32:33] op_sel_hi:[0,1]
	v_pk_fma_f32 v[24:25], v[40:41], v[24:25], v[48:49]
	v_exp_f32_e32 v35, v34
	v_pk_mul_f32 v[32:33], v[24:25], v[24:25]
	v_rcp_f32_e32 v34, v15
	v_fmamk_f32 v32, v32, 0xbdd2d3e8, v99
	v_fmamk_f32 v33, v33, 0xbdd2d3e8, v99
	v_mul_f32_e32 v32, v24, v32
	v_mul_f32_e32 v33, v25, v33
	v_exp_f32_e32 v32, v32

.Lw3b120:
	v_exp_f32_e32 v33, v33
	v_add_f32_e32 v15, 1.0, v35
	v_rcp_f32_e32 v35, v15
	v_add_f32_e32 v32, 1.0, v32
	v_add_f32_e32 v33, 1.0, v33
	v_rcp_f32_e32 v32, v32
	v_rcp_f32_e32 v33, v33
	v_pk_mul_f32 v[22:23], v[22:23], v[28:29]
	v_pk_mul_f32 v[16:17], v[16:17], v[34:35]
	v_pk_mul_f32 v[24:25], v[24:25], v[32:33]
	s_nop 0
	v_cvt_pk_f16_f32 v16, v16, v17

.Lw3b121:
	v_lshl_add_u32 v15, v31, 2, v101
	v_add_u32_e32 v48, 0x440, v15
	v_add_u32_e32 v42, 0x448, v15
	v_add_u32_e32 v46, 0x450, v15
	ds_read2_b32 v[32:33], v15 offset0:146 offset1:147
	ds_read2_b32 v[36:37], v15 offset0:150 offset1:151
	ds_read2_b32 v[38:39], v15 offset0:148 offset1:149

.Lw3b122:
	ds_read2_b32 v[40:41], v15 offset0:144 offset1:145
	v_add_u32_e32 v15, 0x458, v15
	ds_read2_b32 v[42:43], v42 offset1:1
	ds_read2_b32 v[44:45], v15 offset1:1
	ds_read2_b32 v[46:47], v46 offset1:1
	ds_read2_b32 v[48:49], v48 offset1:1
	v_cvt_pk_f16_f32 v15, v22, v23
	v_pk_mul_f32 v[12:13], v[30:31], v[12:13] op_sel_hi:[0,1]

.Lw3b123:
	s_waitcnt lgkmcnt(0)
	v_pk_fma_f32 v[12:13], v[40:41], v[12:13], v[48:49]
	v_pk_mul_f32 v[18:19], v[30:31], v[18:19] op_sel_hi:[0,1]
	v_pk_mul_f32 v[22:23], v[12:13], v[12:13]
	v_pk_fma_f32 v[28:29], v[32:33], v[18:19], v[42:43]
	v_fmamk_f32 v17, v22, 0xbdd2d3e8, v99
	v_mul_f32_e32 v17, v12, v17
	v_fmamk_f32 v22, v23, 0xbdd2d3e8, v99

.Lw3b124:
	v_exp_f32_e32 v17, v17
	v_mul_f32_e32 v22, v13, v22
	v_exp_f32_e32 v23, v22
	v_pk_mul_f32 v[18:19], v[28:29], v[28:29]
	v_add_f32_e32 v17, 1.0, v17
	v_rcp_f32_e32 v22, v17
	v_add_f32_e32 v17, 1.0, v23
	v_rcp_f32_e32 v23, v17
	v_fmamk_f32 v17, v18, 0xbdd2d3e8, v99
	v_pk_mul_f32 v[10:11], v[30:31], v[10:11] op_sel_hi:[0,1]
	v_mul_f32_e32 v17, v28, v17
	v_pk_mul_f32 v[12:13], v[12:13], v[22:23]

.Lw3b125:
	v_pk_fma_f32 v[10:11], v[36:37], v[10:11], v[44:45]
	v_cvt_pk_f16_f32 v18, v12, v13
	v_fmamk_f32 v12, v19, 0xbdd2d3e8, v99
	v_mul_f32_e32 v12, v29, v12
	v_exp_f32_e32 v19, v12
	v_pk_mul_f32 v[12:13], v[30:31], v[20:21] op_sel_hi:[0,1]
	v_pk_fma_f32 v[12:13], v[38:39], v[12:13], v[46:47]
	v_exp_f32_e32 v32, v17
	v_pk_mul_f32 v[20:21], v[12:13], v[12:13]

.Lw3b126:
	v_add_f32_e32 v19, 1.0, v19
	v_fmamk_f32 v20, v20, 0xbdd2d3e8, v99
	v_mul_f32_e32 v20, v12, v20
	v_exp_f32_e32 v20, v20
	v_rcp_f32_e32 v23, v19
	v_cvt_pk_f16_f32 v17, v24, v25
	v_add_f32_e32 v22, 1.0, v32
	v_add_f32_e32 v19, 1.0, v20
	v_fmamk_f32 v20, v21, 0xbdd2d3e8, v99
	v_mul_f32_e32 v24, v13, v20
	v_pk_mul_f32 v[20:21], v[10:11], v[10:11]

.Lw3b127:
	v_exp_f32_e32 v25, v24
	v_fmamk_f32 v20, v20, 0xbdd2d3e8, v99
	v_fmamk_f32 v21, v21, 0xbdd2d3e8, v99
	v_mul_f32_e32 v20, v10, v20
	v_mul_f32_e32 v21, v11, v21
	v_exp_f32_e32 v20, v20
	v_exp_f32_e32 v21, v21
	v_rcp_f32_e32 v24, v19
	v_add_f32_e32 v19, 1.0, v25
	v_add_f32_e32 v20, 1.0, v20
	v_add_f32_e32 v21, 1.0, v21
	v_rcp_f32_e32 v20, v20

.Lw3b128:
	v_rcp_f32_e32 v21, v21
	v_rcp_f32_e32 v25, v19
	v_rcp_f32_e32 v22, v22
	v_pk_mul_f32 v[10:11], v[10:11], v[20:21]
	s_nop 0
	v_pk_mul_f32 v[12:13], v[12:13], v[24:25]
	v_lshl_add_u32 v19, v31, 2, v101
	v_add_u32_e32 v21, 0x468, v19
	ds_read2_b32 v[32:33], v19 offset0:154 offset1:155
	ds_read2_b32 v[34:35], v19 offset0:158 offset1:159

.Lw3b129:
	ds_read2_b32 v[36:37], v19 offset0:156 offset1:157
	ds_read2_b32 v[38:39], v19 offset0:152 offset1:153
	v_add_u32_e32 v20, 0x460, v19
	v_add_u32_e32 v31, 0x470, v19
	v_add_u32_e32 v19, 0x478, v19
	ds_read2_b32 v[40:41], v21 offset1:1
	ds_read2_b32 v[42:43], v19 offset1:1

.Lw3b130:
	ds_read2_b32 v[44:45], v31 offset1:1
	ds_read2_b32 v[46:47], v20 offset1:1
	v_pk_mul_f32 v[20:21], v[28:29], v[22:23]
	s_nop 0
	v_cvt_pk_f16_f32 v19, v20, v21
	v_cvt_pk_f16_f32 v20, v12, v13
	v_pk_mul_f32 v[4:5], v[30:31], v[4:5] op_sel_hi:[0,1]
	s_waitcnt lgkmcnt(0)
	v_pk_fma_f32 v[4:5], v[38:39], v[4:5], v[46:47]

.Lw3b131:
	v_cvt_pk_f16_f32 v21, v10, v11
	v_pk_mul_f32 v[12:13], v[4:5], v[4:5]
	v_pk_mul_f32 v[10:11], v[30:31], v[26:27] op_sel_hi:[0,1]
	v_fmamk_f32 v12, v12, 0xbdd2d3e8, v99
	v_fmamk_f32 v13, v13, 0xbdd2d3e8, v99
	v_mul_f32_e32 v12, v4, v12
	v_mul_f32_e32 v13, v5, v13
	v_exp_f32_e32 v12, v12
	v_exp_f32_e32 v13, v13

.Lw3b132:
	v_pk_fma_f32 v[10:11], v[32:33], v[10:11], v[40:41]
	v_pk_mul_f32 v[0:1], v[30:31], v[0:1] op_sel_hi:[0,1]
	v_add_f32_e32 v12, 1.0, v12
	v_add_f32_e32 v13, 1.0, v13
	v_rcp_f32_e32 v12, v12
	v_rcp_f32_e32 v13, v13
	v_pk_fma_f32 v[0:1], v[36:37], v[0:1], v[44:45]
	v_pk_mul_f32 v[2:3], v[30:31], v[2:3] op_sel_hi:[0,1]
	v_pk_fma_f32 v[2:3], v[34:35], v[2:3], v[42:43]
	v_pk_mul_f32 v[4:5], v[4:5], v[12:13]

.Lw3b133:
	v_pk_mul_f32 v[12:13], v[10:11], v[10:11]
	v_cvt_pk_f16_f32 v24, v4, v5
	v_fmamk_f32 v12, v12, 0xbdd2d3e8, v99
	v_fmamk_f32 v13, v13, 0xbdd2d3e8, v99
	v_mul_f32_e32 v12, v10, v12
	v_mul_f32_e32 v13, v11, v13
	v_exp_f32_e32 v12, v12
	v_exp_f32_e32 v13, v13
	v_add_f32_e32 v4, 1.0, v12
	v_add_f32_e32 v5, 1.0, v13

.Lw3b134:
	v_pk_mul_f32 v[12:13], v[0:1], v[0:1]
	v_rcp_f32_e32 v4, v4
	v_fmamk_f32 v12, v12, 0xbdd2d3e8, v99
	v_fmamk_f32 v13, v13, 0xbdd2d3e8, v99
	v_mul_f32_e32 v12, v0, v12
	v_mul_f32_e32 v13, v1, v13
	v_rcp_f32_e32 v5, v5
	v_exp_f32_e32 v12, v12
	v_exp_f32_e32 v13, v13
	v_pk_mul_f32 v[4:5], v[10:11], v[4:5]
	v_add_f32_e32 v10, 1.0, v12

.Lw3b135:
	v_add_f32_e32 v11, 1.0, v13
	v_pk_mul_f32 v[12:13], v[2:3], v[2:3]
	v_rcp_f32_e32 v10, v10
	v_fmamk_f32 v12, v12, 0xbdd2d3e8, v99
	v_fmamk_f32 v13, v13, 0xbdd2d3e8, v99
	v_mul_f32_e32 v12, v2, v12
	v_mul_f32_e32 v13, v3, v13
	v_exp_f32_e32 v12, v12
	v_exp_f32_e32 v13, v13
	v_rcp_f32_e32 v11, v11
	v_cvt_pk_f16_f32 v25, v4, v5

.Lw3b136:
	v_add_f32_e32 v12, 1.0, v12
	v_add_f32_e32 v13, 1.0, v13
	v_rcp_f32_e32 v12, v12
	v_rcp_f32_e32 v13, v13
	v_pk_mul_f32 v[0:1], v[0:1], v[10:11]
	s_nop 0
	v_cvt_pk_f16_f32 v26, v0, v1
	v_pk_mul_f32 v[0:1], v[2:3], v[12:13]
	s_nop 0
	v_cvt_pk_f16_f32 v27, v0, v1
	ds_read_b128 v[0:3], v96 offset:1536

.Lw3b137:
	ds_read_b128 v[10:13], v96 offset:1552
	ds_read_b128 v[30:33], v96 offset:1568
	ds_read_b128 v[34:37], v96 offset:1584
	ds_read_b128 v[38:41], v96 offset:1600
	ds_read_b128 v[42:45], v96 offset:1616
	ds_read_b128 v[46:49], v96 offset:1632
	ds_read_b128 v[50:53], v96 offset:1648

.Lw3b138:
	v_mov_b32_e32 v4, v77
	s_nop 0
	v_lshl_add_u32 v28, v4, 4, v102
	ds_read_b128 v[54:57], v28
	ds_read_b128 v[58:61], v28 offset:1024
	ds_read_b128 v[62:65], v28 offset:2048
	ds_read_b128 v[66:69], v28 offset:3072
	ds_read_b128 v[104:107], v28 offset:4096
	ds_read_b128 v[108:111], v28 offset:5120

.Lw3b139:
	ds_read_b128 v[112:115], v28 offset:6144
	ds_read_b128 v[116:119], v28 offset:7168
	s_waitcnt lgkmcnt(7)
	v_mfma_f32_16x16x32_f16 v[0:3], v[54:57], v[6:9], v[0:3]
	s_waitcnt lgkmcnt(6)
	v_mfma_f32_16x16x32_f16 v[10:13], v[58:61], v[6:9], v[10:13]
	s_waitcnt lgkmcnt(5)
	v_mfma_f32_16x16x32_f16 v[30:33], v[62:65], v[6:9], v[30:33]
	s_waitcnt lgkmcnt(4)

.Lw3b140:
	v_mfma_f32_16x16x32_f16 v[34:37], v[66:69], v[6:9], v[34:37]
	ds_read_b128 v[54:57], v28 offset:8192
	ds_read_b128 v[58:61], v28 offset:9216
	ds_read_b128 v[62:65], v28 offset:10240
	ds_read_b128 v[66:69], v28 offset:11264
	s_waitcnt lgkmcnt(7)
	v_mfma_f32_16x16x32_f16 v[38:41], v[104:107], v[6:9], v[38:41]
	s_waitcnt lgkmcnt(6)
	v_mfma_f32_16x16x32_f16 v[42:45], v[108:111], v[6:9], v[42:45]

.Lw3b141:
	s_waitcnt lgkmcnt(5)
	v_mfma_f32_16x16x32_f16 v[46:49], v[112:115], v[6:9], v[46:49]
	s_waitcnt lgkmcnt(4)
	v_mfma_f32_16x16x32_f16 v[4:7], v[116:119], v[6:9], v[50:53]
	s_nop 2
	ds_read_b128 v[50:53], v28 offset:12288
	ds_read_b128 v[104:107], v28 offset:13312
	ds_read_b128 v[108:111], v28 offset:14336
	ds_read_b128 v[112:115], v28 offset:15360

.Lw3b142:
	s_waitcnt lgkmcnt(7)
	v_mfma_f32_16x16x32_f16 v[0:3], v[54:57], v[14:17], v[0:3]
	s_waitcnt lgkmcnt(6)
	v_mfma_f32_16x16x32_f16 v[8:11], v[58:61], v[14:17], v[10:13]
	s_waitcnt lgkmcnt(5)
	v_mfma_f32_16x16x32_f16 v[30:33], v[62:65], v[14:17], v[30:33]
	s_waitcnt lgkmcnt(4)
	v_mfma_f32_16x16x32_f16 v[34:37], v[66:69], v[14:17], v[34:37]
	ds_read_b128 v[54:57], v28 offset:16384

.Lw3b143:
	ds_read_b128 v[58:61], v28 offset:17408
	ds_read_b128 v[62:65], v28 offset:18432
	ds_read_b128 v[66:69], v28 offset:19456
	s_waitcnt lgkmcnt(7)
	v_mfma_f32_16x16x32_f16 v[38:41], v[50:53], v[14:17], v[38:41]
	s_waitcnt lgkmcnt(6)
	v_mfma_f32_16x16x32_f16 v[42:45], v[104:107], v[14:17], v[42:45]
	s_waitcnt lgkmcnt(5)
	v_mfma_f32_16x16x32_f16 v[46:49], v[108:111], v[14:17], v[46:49]

.Lw3b144:
	s_waitcnt lgkmcnt(4)
	v_mfma_f32_16x16x32_f16 v[4:7], v[112:115], v[14:17], v[4:7]
	ds_read_b128 v[12:15], v28 offset:20480
	ds_read_b128 v[50:53], v28 offset:21504
	ds_read_b128 v[104:107], v28 offset:22528
	ds_read_b128 v[108:111], v28 offset:23552
	s_waitcnt lgkmcnt(7)
	v_mfma_f32_16x16x32_f16 v[0:3], v[54:57], v[18:21], v[0:3]
	s_waitcnt lgkmcnt(6)

.Lw3b145:
	v_mfma_f32_16x16x32_f16 v[8:11], v[58:61], v[18:21], v[8:11]
	s_waitcnt lgkmcnt(5)
	v_mfma_f32_16x16x32_f16 v[30:33], v[62:65], v[18:21], v[30:33]
	s_waitcnt lgkmcnt(4)
	v_mfma_f32_16x16x32_f16 v[34:37], v[66:69], v[18:21], v[34:37]
	ds_read_b128 v[54:57], v28 offset:24576
	ds_read_b128 v[58:61], v28 offset:25600
	ds_read_b128 v[62:65], v28 offset:26624
	ds_read_b128 v[66:69], v28 offset:27648

.Lw3b146:
	s_waitcnt lgkmcnt(7)
	v_mfma_f32_16x16x32_f16 v[12:15], v[12:15], v[18:21], v[38:41]
	s_waitcnt lgkmcnt(6)
	v_mfma_f32_16x16x32_f16 v[38:41], v[50:53], v[18:21], v[42:45]
	s_waitcnt lgkmcnt(5)
	v_mfma_f32_16x16x32_f16 v[42:45], v[104:107], v[18:21], v[46:49]
	s_waitcnt lgkmcnt(4)
	v_mfma_f32_16x16x32_f16 v[46:49], v[108:111], v[18:21], v[4:7]
	s_nop 2
	ds_read_b128 v[4:7], v28 offset:28672

.Lw3b147:
	ds_read_b128 v[50:53], v28 offset:29696
	ds_read_b128 v[104:107], v28 offset:30720
	ds_read_b128 v[108:111], v28 offset:31744
	s_waitcnt lgkmcnt(7)
	v_mfma_f32_16x16x32_f16 v[54:57], v[54:57], v[24:27], v[0:3]
	s_waitcnt lgkmcnt(6)
	v_mfma_f32_16x16x32_f16 v[58:61], v[58:61], v[24:27], v[8:11]
	s_waitcnt lgkmcnt(5)
	v_mfma_f32_16x16x32_f16 v[20:23], v[62:65], v[24:27], v[30:33]

.Lw3b148:
	s_waitcnt lgkmcnt(4)
	v_mfma_f32_16x16x32_f16 v[16:19], v[66:69], v[24:27], v[34:37]
	s_waitcnt lgkmcnt(0)
	v_mfma_f32_16x16x32_f16 v[0:3], v[108:111], v[24:27], v[46:49]
	v_mfma_f32_16x16x32_f16 v[12:15], v[4:7], v[24:27], v[12:15]
	v_mfma_f32_16x16x32_f16 v[8:11], v[50:53], v[24:27], v[38:41]
	v_mfma_f32_16x16x32_f16 v[4:7], v[104:107], v[24:27], v[42:45]
	v_mul_f32_e32 v24, v54, v54
	v_fmamk_f32 v24, v24, 0xbdd2d3e8, v99

.Lw3b149:
	v_mul_f32_e32 v24, v54, v24
	v_exp_f32_e32 v24, v24
	v_mul_f32_e32 v25, v55, v55
	v_mul_f32_e32 v26, v56, v56
	v_fmamk_f32 v25, v25, 0xbdd2d3e8, v99
	v_fmamk_f32 v26, v26, 0xbdd2d3e8, v99
	v_mul_f32_e32 v25, v55, v25
	v_add_f32_e32 v24, 1.0, v24
	v_mul_f32_e32 v26, v56, v26
	v_rcp_f32_e32 v24, v24
	v_exp_f32_e32 v25, v25
	v_exp_f32_e32 v26, v26

.Lw3b150:
	v_mul_f32_e32 v30, v57, v57
	v_mul_f32_e32 v31, v58, v58
	v_fmamk_f32 v30, v30, 0xbdd2d3e8, v99
	v_fmamk_f32 v31, v31, 0xbdd2d3e8, v99
	v_fma_mixlo_f16 v29, v54, v24, 0
	v_add_f32_e32 v24, 1.0, v25
	v_add_f32_e32 v25, 1.0, v26
	v_mul_f32_e32 v30, v57, v30
	v_mul_f32_e32 v31, v58, v31
	v_rcp_f32_e32 v24, v24
	v_rcp_f32_e32 v25, v25
	v_exp_f32_e32 v30, v30

.Lw3b151:
	v_exp_f32_e32 v31, v31
	v_mov_b32_e32 v26, v55
	v_mov_b32_e32 v27, v56
	v_pk_mul_f32 v[24:25], v[26:27], v[24:25]
	v_add_f32_e32 v26, 1.0, v30
	v_add_f32_e32 v27, 1.0, v31
	v_rcp_f32_e32 v26, v26
	v_rcp_f32_e32 v27, v27
	v_cvt_pk_f16_f32 v25, v24, v25
	v_pk_mov_b32 v[30:31], v[56:57], v[58:59] op_sel:[1,0]
	v_pack_b32_f16 v24, v29, v25

.Lw3b152:
	v_pk_mul_f32 v[26:27], v[30:31], v[26:27]
	v_mul_f32_e32 v29, v59, v59
	v_mul_f32_e32 v30, v60, v60
	v_fmamk_f32 v29, v29, 0xbdd2d3e8, v99
	v_fmamk_f32 v30, v30, 0xbdd2d3e8, v99
	v_mul_f32_e32 v29, v59, v29
	v_mul_f32_e32 v30, v60, v30
	v_exp_f32_e32 v29, v29
	v_exp_f32_e32 v30, v30
	v_cvt_pk_f16_f32 v32, v26, v27
	v_mov_b32_e32 v31, v60

.Lw3b153:
	v_add_f32_e32 v26, 1.0, v29
	v_add_f32_e32 v27, 1.0, v30
	v_rcp_f32_e32 v26, v26
	v_rcp_f32_e32 v27, v27
	v_mov_b32_e32 v30, v59
	v_alignbit_b32 v25, v32, v25, 16
	v_mul_f32_e32 v34, v20, v20
	v_pk_mul_f32 v[26:27], v[30:31], v[26:27]
	v_fmamk_f32 v34, v34, 0xbdd2d3e8, v99
	v_cvt_pk_f16_f32 v27, v26, v27
	v_mul_f32_e32 v26, v61, v61

.Lw3b154:
	v_fmamk_f32 v26, v26, 0xbdd2d3e8, v99
	v_mul_f32_e32 v26, v61, v26
	v_exp_f32_e32 v29, v26
	v_alignbit_b32 v26, v27, v32, 16
	ds_read_b128 v[30:33], v28 offset:32768
	v_mul_f32_e32 v34, v20, v34
	v_add_f32_e32 v29, 1.0, v29
	v_rcp_f32_e32 v29, v29
	v_lshrrev_b32_e32 v27, 16, v27
	v_exp_f32_e32 v38, v34
	ds_read_b128 v[34:37], v28 offset:33792

.Lw3b155:
	v_fma_mixhi_f16 v27, v61, v29, 0
	v_add_f32_e32 v29, 1.0, v38
	s_waitcnt lgkmcnt(1)
	v_mfma_f32_16x16x32_f16 v[24:27], v[30:33], v[24:27], 0
	v_mul_f32_e32 v30, v21, v21
	v_fmamk_f32 v30, v30, 0xbdd2d3e8, v99
	v_mul_f32_e32 v31, v22, v22
	v_mul_f32_e32 v30, v21, v30
	v_fmamk_f32 v31, v31, 0xbdd2d3e8, v99
	v_rcp_f32_e32 v29, v29
	v_exp_f32_e32 v30, v30

.Lw3b156:
	v_mul_f32_e32 v31, v22, v31
	v_exp_f32_e32 v31, v31
	v_fma_mixlo_f16 v29, v20, v29, 0
	v_add_f32_e32 v20, 1.0, v30
	v_rcp_f32_e32 v30, v20
	v_add_f32_e32 v20, 1.0, v31
	v_rcp_f32_e32 v31, v20
	v_mov_b32_e32 v20, v21
	v_mov_b32_e32 v21, v22
	v_mul_f32_e32 v22, v23, v23
	v_fmamk_f32 v22, v22, 0xbdd2d3e8, v99
	v_mul_f32_e32 v32, v16, v16
	v_mul_f32_e32 v22, v23, v22

.Lw3b157:
	v_fmamk_f32 v32, v32, 0xbdd2d3e8, v99
	v_exp_f32_e32 v22, v22
	v_mul_f32_e32 v32, v16, v32
	v_exp_f32_e32 v32, v32
	v_pk_mul_f32 v[20:21], v[20:21], v[30:31]
	v_add_f32_e32 v22, 1.0, v22
	v_rcp_f32_e32 v30, v22
	v_add_f32_e32 v22, 1.0, v32
	v_rcp_f32_e32 v31, v22
	v_pk_mov_b32 v[22:23], v[22:23], v[16:17] op_sel:[1,0]
	v_cvt_pk_f16_f32 v21, v20, v21

.Lw3b158:
	v_mul_f32_e32 v16, v17, v17
	v_pk_mul_f32 v[22:23], v[22:23], v[30:31]
	v_pack_b32_f16 v20, v29, v21
	v_cvt_pk_f16_f32 v29, v22, v23
	v_fmamk_f32 v16, v16, 0xbdd2d3e8, v99
	v_mul_f32_e32 v22, v18, v18
	v_mul_f32_e32 v16, v17, v16
	v_fmamk_f32 v22, v22, 0xbdd2d3e8, v99
	v_exp_f32_e32 v16, v16
	v_mul_f32_e32 v22, v18, v22

.Lw3b159:
	v_exp_f32_e32 v23, v22
	v_alignbit_b32 v21, v29, v21, 16
	v_add_f32_e32 v16, 1.0, v16
	v_rcp_f32_e32 v22, v16
	v_add_f32_e32 v16, 1.0, v23
	v_rcp_f32_e32 v23, v16
	v_mul_f32_e32 v16, v19, v19
	v_fmamk_f32 v16, v16, 0xbdd2d3e8, v99
	v_mul_f32_e32 v16, v19, v16
	v_exp_f32_e32 v30, v16
	v_mov_b32_e32 v16, v17
	v_mov_b32_e32 v17, v18
	v_pk_mul_f32 v[16:17], v[16:17], v[22:23]

.Lw3b160:
	v_add_f32_e32 v18, 1.0, v30
	v_rcp_f32_e32 v18, v18
	v_cvt_pk_f16_f32 v16, v16, v17
	v_lshrrev_b32_e32 v23, 16, v16
	v_alignbit_b32 v22, v16, v29, 16
	v_fma_mixhi_f16 v23, v19, v18, 0
	s_waitcnt lgkmcnt(0)
	s_nop 0
	v_mfma_f32_16x16x32_f16 v[16:19], v[34:37], v[20:23], v[24:27]
	v_mul_f32_e32 v20, v12, v12

.Lw3b161:
	v_fmamk_f32 v20, v20, 0xbdd2d3e8, v99
	v_mul_f32_e32 v20, v12, v20
	v_exp_f32_e32 v20, v20
	v_mul_f32_e32 v21, v13, v13
	v_fmamk_f32 v21, v21, 0xbdd2d3e8, v99
	v_mul_f32_e32 v22, v14, v14
	v_mul_f32_e32 v21, v13, v21
	v_add_f32_e32 v20, 1.0, v20
	v_fmamk_f32 v22, v22, 0xbdd2d3e8, v99
	v_rcp_f32_e32 v20, v20
	v_exp_f32_e32 v21, v21
	v_mul_f32_e32 v22, v14, v22

.Lw3b162:
	v_exp_f32_e32 v22, v22
	v_fma_mixlo_f16 v23, v12, v20, 0
	v_add_f32_e32 v12, 1.0, v21
	v_rcp_f32_e32 v20, v12
	v_add_f32_e32 v12, 1.0, v22
	v_rcp_f32_e32 v21, v12
	v_mov_b32_e32 v12, v13
	v_mov_b32_e32 v13, v14
	v_mul_f32_e32 v14, v15, v15
	v_fmamk_f32 v14, v14, 0xbdd2d3e8, v99
	v_mul_f32_e32 v22, v8, v8
	v_mul_f32_e32 v14, v15, v14
	v_fmamk_f32 v22, v22, 0xbdd2d3e8, v99

.Lw3b163:
	v_exp_f32_e32 v14, v14
	v_mul_f32_e32 v22, v8, v22
	v_exp_f32_e32 v22, v22
	v_pk_mul_f32 v[12:13], v[12:13], v[20:21]
	v_add_f32_e32 v14, 1.0, v14
	v_rcp_f32_e32 v20, v14
	v_add_f32_e32 v14, 1.0, v22
	v_rcp_f32_e32 v21, v14
	v_pk_mov_b32 v[14:15], v[14:15], v[8:9] op_sel:[1,0]
	v_mul_f32_e32 v8, v9, v9
	v_fmamk_f32 v8, v8, 0xbdd2d3e8, v99

.Lw3b164:
	v_pk_mul_f32 v[14:15], v[14:15], v[20:21]
	v_mul_f32_e32 v20, v10, v10
	v_mul_f32_e32 v8, v9, v8
	v_fmamk_f32 v20, v20, 0xbdd2d3e8, v99
	v_exp_f32_e32 v8, v8
	v_mul_f32_e32 v20, v10, v20
	v_exp_f32_e32 v20, v20
	v_cvt_pk_f16_f32 v21, v14, v15
	v_add_f32_e32 v8, 1.0, v8
	v_rcp_f32_e32 v14, v8
	v_add_f32_e32 v8, 1.0, v20
	v_rcp_f32_e32 v15, v8

.Lw3b165:
	v_mov_b32_e32 v8, v9
	v_mov_b32_e32 v9, v10
	v_cvt_pk_f16_f32 v13, v12, v13
	v_pk_mul_f32 v[8:9], v[8:9], v[14:15]
	v_pack_b32_f16 v12, v23, v13
	v_cvt_pk_f16_f32 v8, v8, v9
	v_mul_f32_e32 v9, v11, v11
	v_fmamk_f32 v9, v9, 0xbdd2d3e8, v99
	v_mul_f32_e32 v9, v11, v9
	v_exp_f32_e32 v9, v9

.Lw3b166:
	v_alignbit_b32 v13, v21, v13, 16
	v_alignbit_b32 v14, v8, v21, 16
	ds_read_b128 v[20:23], v28 offset:34816
	v_lshrrev_b32_e32 v15, 16, v8
	v_add_f32_e32 v8, 1.0, v9
	v_rcp_f32_e32 v8, v8
	v_mul_f32_e32 v9, v4, v4
	v_fmamk_f32 v9, v9, 0xbdd2d3e8, v99
	v_mul_f32_e32 v9, v4, v9
	v_exp_f32_e32 v24, v9
	v_fma_mixhi_f16 v15, v11, v8, 0

.Lw3b167:
	ds_read_b128 v[8:11], v28 offset:35840
	s_waitcnt lgkmcnt(1)
	v_mfma_f32_16x16x32_f16 v[12:15], v[20:23], v[12:15], v[16:19]
	s_nop 2
	v_mul_f32_e32 v17, v5, v5
	v_fmamk_f32 v17, v17, 0xbdd2d3e8, v99
	v_mul_f32_e32 v18, v6, v6
	v_add_f32_e32 v16, 1.0, v24
	v_mul_f32_e32 v17, v5, v17
	v_fmamk_f32 v18, v18, 0xbdd2d3e8, v99

.Lw3b168:
	v_rcp_f32_e32 v16, v16
	v_exp_f32_e32 v17, v17
	v_mul_f32_e32 v18, v6, v18
	v_exp_f32_e32 v18, v18
	v_fma_mixlo_f16 v19, v4, v16, 0
	v_add_f32_e32 v4, 1.0, v17
	v_rcp_f32_e32 v16, v4
	v_add_f32_e32 v4, 1.0, v18
	v_rcp_f32_e32 v17, v4
	v_mov_b32_e32 v4, v5
	v_mov_b32_e32 v5, v6
	v_mul_f32_e32 v6, v7, v7
	v_fmamk_f32 v6, v6, 0xbdd2d3e8, v99

.Lw3b169:
	v_mul_f32_e32 v18, v0, v0
	v_mul_f32_e32 v6, v7, v6
	v_fmamk_f32 v18, v18, 0xbdd2d3e8, v99
	v_exp_f32_e32 v6, v6
	v_mul_f32_e32 v18, v0, v18
	v_exp_f32_e32 v18, v18
	v_pk_mul_f32 v[4:5], v[4:5], v[16:17]
	v_add_f32_e32 v6, 1.0, v6
	v_rcp_f32_e32 v16, v6
	v_add_f32_e32 v6, 1.0, v18
	v_rcp_f32_e32 v17, v6
	v_pk_mov_b32 v[6:7], v[6:7], v[0:1] op_sel:[1,0]

.Lw3b170:
	v_mul_f32_e32 v0, v1, v1
	v_fmamk_f32 v0, v0, 0xbdd2d3e8, v99
	v_pk_mul_f32 v[6:7], v[6:7], v[16:17]
	v_mul_f32_e32 v0, v1, v0
	v_cvt_pk_f16_f32 v16, v6, v7
	v_mul_f32_e32 v6, v2, v2
	v_fmamk_f32 v6, v6, 0xbdd2d3e8, v99
	v_exp_f32_e32 v0, v0
	v_mul_f32_e32 v6, v2, v6
	v_exp_f32_e32 v7, v6
	v_cvt_pk_f16_f32 v5, v4, v5

.Lw3b171:
	v_add_f32_e32 v0, 1.0, v0
	v_rcp_f32_e32 v6, v0
	v_add_f32_e32 v0, 1.0, v7
	v_rcp_f32_e32 v7, v0
	v_mul_f32_e32 v0, v3, v3
	v_fmamk_f32 v0, v0, 0xbdd2d3e8, v99
	v_mul_f32_e32 v0, v3, v0
	v_exp_f32_e32 v17, v0
	v_mov_b32_e32 v0, v1
	v_mov_b32_e32 v1, v2
	v_pk_mul_f32 v[0:1], v[0:1], v[6:7]
	v_add_f32_e32 v2, 1.0, v17

.Lw3b172:
	v_rcp_f32_e32 v2, v2
	v_cvt_pk_f16_f32 v0, v0, v1
	v_lshrrev_b32_e32 v7, 16, v0
	v_pack_b32_f16 v4, v19, v5
	v_alignbit_b32 v5, v16, v5, 16
	v_alignbit_b32 v6, v0, v16, 16
	v_fma_mixhi_f16 v7, v3, v2, 0
	s_waitcnt lgkmcnt(0)
	s_nop 0
	v_mfma_f32_16x16x32_f16 v[0:3], v[8:11], v[4:7], v[12:15]

.Lw3b173:
	s_and_saveexec_b64 s[14:15], s[4:5]
	s_xor_b64 s[14:15], exec, s[14:15]
	s_cbranch_execz .LBB3_9
	s_load_dwordx2 s[20:21], s[16:17], 0x0
	s_nop 3
	v_or_b32_e32 v2, s10, v80
	v_ashrrev_i32_e32 v3, 31, v2
	v_lshl_add_u64 v[2:3], v[2:3], 3, s[6:7]
	s_waitcnt lgkmcnt(0)
	v_pk_add_f32 v[0:1], v[0:1], s[20:21]
	global_store_dwordx2 v[2:3], v[0:1], off

.Lw3b174:
	s_branch .LBB3_9
.LBB3_96:
	s_endpgm

amdhsa.kernels:
  - .agpr_count:     0
    .args:
      - .actual_access:  read_only
        .address_space:  global
        .offset:         0
        .size:           8
        .value_kind:     global_buffer
      - .actual_access:  read_only
        .address_space:  global
        .offset:         8
        .size:           8
        .value_kind:     global_buffer
      - .actual_access:  write_only
        .address_space:  global
        .offset:         16
        .size:           8
        .value_kind:     global_buffer
      - .actual_access:  write_only
        .address_space:  global
        .offset:         24
        .size:           8
        .value_kind:     global_buffer
      - .actual_access:  write_only
        .address_space:  global
        .offset:         32
        .size:           8
        .value_kind:     global_buffer
      - .actual_access:  read_only
        .address_space:  global
        .offset:         40
        .size:           8
        .value_kind:     global_buffer
      - .actual_access:  read_only
        .address_space:  global
        .offset:         48
        .size:           8
        .value_kind:     global_buffer
      - .actual_access:  read_only
        .address_space:  global
        .offset:         56
        .size:           8
        .value_kind:     global_buffer
      - .actual_access:  write_only
        .address_space:  global
        .offset:         64
        .size:           8
        .value_kind:     global_buffer
      - .actual_access:  write_only
        .address_space:  global
        .offset:         72
        .size:           8
        .value_kind:     global_buffer
      - .actual_access:  read_only
        .address_space:  global
        .offset:         80
        .size:           8
        .value_kind:     global_buffer
      - .address_space:  global
        .offset:         88
        .size:           8
        .value_kind:     global_buffer
      - .actual_access:  write_only
        .address_space:  global
        .offset:         96
        .size:           8
        .value_kind:     global_buffer
    .group_segment_fixed_size: 34400
    .kernarg_segment_align: 8
    .kernarg_segment_size: 104
    .language:       OpenCL C
    .language_version:
      - 2
      - 0
    .max_flat_workgroup_size: 1024
    .name:           _Z7k_frontPKiS0_PiS1_PjPKfS4_S4_P15HIP_vector_typeIjLj4EES7_PKS5_IfLj4EES7_S7_
    .private_segment_fixed_size: 0
    .sgpr_count:     44
    .sgpr_spill_count: 0
    .symbol:         _Z7k_frontPKiS0_PiS1_PjPKfS4_S4_P15HIP_vector_typeIjLj4EES7_PKS5_IfLj4EES7_S7_.kd
    .uniform_work_group_size: 1
    .uses_dynamic_stack: false
    .vgpr_count:     41
    .vgpr_spill_count: 0
    .wavefront_size: 64
  - .agpr_count:     0
    .args:
      - .actual_access:  read_only
        .address_space:  global
        .offset:         0
        .size:           8
        .value_kind:     global_buffer
      - .actual_access:  read_only
        .address_space:  global
        .offset:         8
        .size:           8
        .value_kind:     global_buffer
      - .actual_access:  read_only
        .address_space:  global
        .offset:         16
        .size:           8
        .value_kind:     global_buffer
      - .actual_access:  write_only
        .address_space:  global
        .offset:         24
        .size:           8
        .value_kind:     global_buffer
      - .address_space:  global
        .offset:         32
        .size:           8
        .value_kind:     global_buffer
      - .actual_access:  read_only
        .address_space:  global
        .offset:         40
        .size:           8
        .value_kind:     global_buffer
      - .address_space:  global
        .offset:         48
        .size:           8
        .value_kind:     global_buffer
    .group_segment_fixed_size: 72624
    .kernarg_segment_align: 8
    .kernarg_segment_size: 56
    .language:       OpenCL C
    .language_version:
      - 2
      - 0
    .max_flat_workgroup_size: 1024
    .name:           _Z8k_bucketPKiS0_PKjPiS3_PK15HIP_vector_typeIfLj4EEPS4_IjLj4EE
    .private_segment_fixed_size: 0
    .sgpr_count:     74
    .sgpr_spill_count: 0
    .symbol:         _Z8k_bucketPKiS0_PKjPiS3_PK15HIP_vector_typeIfLj4EEPS4_IjLj4EE.kd
    .uniform_work_group_size: 1
    .uses_dynamic_stack: false
    .vgpr_count:     40
    .vgpr_spill_count: 0
    .wavefront_size: 64
  - .agpr_count:     0
    .args:
      - .actual_access:  read_only
        .address_space:  global
        .offset:         0
        .size:           8
        .value_kind:     global_buffer
      - .actual_access:  read_only
        .address_space:  global
        .offset:         8
        .size:           8
        .value_kind:     global_buffer
      - .actual_access:  read_only
        .address_space:  global
        .offset:         16
        .size:           8
        .value_kind:     global_buffer
      - .actual_access:  read_only
        .address_space:  global
        .offset:         24
        .size:           8
        .value_kind:     global_buffer
      - .actual_access:  read_only
        .address_space:  global
        .offset:         32
        .size:           8
        .value_kind:     global_buffer
      - .actual_access:  read_only
        .address_space:  global
        .offset:         40
        .size:           8
        .value_kind:     global_buffer
      - .actual_access:  read_only
        .address_space:  global
        .offset:         48
        .size:           8
        .value_kind:     global_buffer
      - .actual_access:  read_only
        .address_space:  global
        .offset:         56
        .size:           8
        .value_kind:     global_buffer
      - .actual_access:  read_only
        .address_space:  global
        .offset:         64
        .size:           8
        .value_kind:     global_buffer
      - .actual_access:  read_only
        .address_space:  global
        .offset:         72
        .size:           8
        .value_kind:     global_buffer
      - .actual_access:  read_only
        .address_space:  global
        .offset:         80
        .size:           8
        .value_kind:     global_buffer
      - .actual_access:  write_only
        .address_space:  global
        .offset:         88
        .size:           8
        .value_kind:     global_buffer
      - .actual_access:  read_only
        .address_space:  global
        .offset:         96
        .size:           8
        .value_kind:     global_buffer
      - .offset:         104
        .size:           4
        .value_kind:     hidden_block_count_x
      - .offset:         108
        .size:           4
        .value_kind:     hidden_block_count_y
      - .offset:         112
        .size:           4
        .value_kind:     hidden_block_count_z
      - .offset:         116
        .size:           2
        .value_kind:     hidden_group_size_x
      - .offset:         118
        .size:           2
        .value_kind:     hidden_group_size_y
      - .offset:         120
        .size:           2
        .value_kind:     hidden_group_size_z
      - .offset:         122
        .size:           2
        .value_kind:     hidden_remainder_x
      - .offset:         124
        .size:           2
        .value_kind:     hidden_remainder_y
      - .offset:         126
        .size:           2
        .value_kind:     hidden_remainder_z
      - .offset:         144
        .size:           8
        .value_kind:     hidden_global_offset_x
      - .offset:         152
        .size:           8
        .value_kind:     hidden_global_offset_y
      - .offset:         160
        .size:           8
        .value_kind:     hidden_global_offset_z
      - .offset:         168
        .size:           2
        .value_kind:     hidden_grid_dims
    .group_segment_fixed_size: 125188
    .kernarg_segment_align: 8
    .kernarg_segment_size: 360
    .language:       OpenCL C
    .language_version:
      - 2
      - 0
    .max_flat_workgroup_size: 832
    .name:           _Z10k_layer_a2ILi0ELi13EEvPKDF16_PKiS3_PK15HIP_vector_typeIjLj4EES7_PKfS9_S9_S9_S9_S9_PDF16_Pf
    .private_segment_fixed_size: 0
    .sgpr_count:     58
    .sgpr_spill_count: 0
    .symbol:         _Z10k_layer_a2ILi0ELi13EEvPKDF16_PKiS3_PK15HIP_vector_typeIjLj4EES7_PKfS9_S9_S9_S9_S9_PDF16_Pf.kd
    .uniform_work_group_size: 1
    .uses_dynamic_stack: false
    .vgpr_count:     128
    .vgpr_spill_count: 0
    .wavefront_size: 64
  - .agpr_count:     0
    .args:
      - .actual_access:  read_only
        .address_space:  global
        .offset:         0
        .size:           8
        .value_kind:     global_buffer
      - .actual_access:  read_only
        .address_space:  global
        .offset:         8
        .size:           8
        .value_kind:     global_buffer
      - .actual_access:  read_only
        .address_space:  global
        .offset:         16
        .size:           8
        .value_kind:     global_buffer
      - .actual_access:  read_only
        .address_space:  global
        .offset:         24
        .size:           8
        .value_kind:     global_buffer
      - .actual_access:  read_only
        .address_space:  global
        .offset:         32
        .size:           8
        .value_kind:     global_buffer
      - .actual_access:  read_only
        .address_space:  global
        .offset:         40
        .size:           8
        .value_kind:     global_buffer
      - .actual_access:  read_only
        .address_space:  global
        .offset:         48
        .size:           8
        .value_kind:     global_buffer
      - .actual_access:  read_only
        .address_space:  global
        .offset:         56
        .size:           8
        .value_kind:     global_buffer
      - .actual_access:  read_only
        .address_space:  global
        .offset:         64
        .size:           8
        .value_kind:     global_buffer
      - .actual_access:  read_only
        .address_space:  global
        .offset:         72
        .size:           8
        .value_kind:     global_buffer
      - .actual_access:  read_only
        .address_space:  global
        .offset:         80
        .size:           8
        .value_kind:     global_buffer
      - .actual_access:  read_only
        .address_space:  global
        .offset:         88
        .size:           8
        .value_kind:     global_buffer
      - .actual_access:  write_only
        .address_space:  global
        .offset:         96
        .size:           8
        .value_kind:     global_buffer
      - .offset:         104
        .size:           4
        .value_kind:     hidden_block_count_x
      - .offset:         108
        .size:           4
        .value_kind:     hidden_block_count_y
      - .offset:         112
        .size:           4
        .value_kind:     hidden_block_count_z
      - .offset:         116
        .size:           2
        .value_kind:     hidden_group_size_x
      - .offset:         118
        .size:           2
        .value_kind:     hidden_group_size_y
      - .offset:         120
        .size:           2
        .value_kind:     hidden_group_size_z
      - .offset:         122
        .size:           2
        .value_kind:     hidden_remainder_x
      - .offset:         124
        .size:           2
        .value_kind:     hidden_remainder_y
      - .offset:         126
        .size:           2
        .value_kind:     hidden_remainder_z
      - .offset:         144
        .size:           8
        .value_kind:     hidden_global_offset_x
      - .offset:         152
        .size:           8
        .value_kind:     hidden_global_offset_y
      - .offset:         160
        .size:           8
        .value_kind:     hidden_global_offset_z
      - .offset:         168
        .size:           2
        .value_kind:     hidden_grid_dims
    .group_segment_fixed_size: 162052
    .kernarg_segment_align: 8
    .kernarg_segment_size: 360
    .language:       OpenCL C
    .language_version:
      - 2
      - 0
    .max_flat_workgroup_size: 832
    .name:           _Z10k_layer_a2ILi1ELi13EEvPKDF16_PKiS3_PK15HIP_vector_typeIjLj4EES7_PKfS9_S9_S9_S9_S9_PDF16_Pf
    .private_segment_fixed_size: 0
    .sgpr_count:     58
    .sgpr_spill_count: 0
    .symbol:         _Z10k_layer_a2ILi1ELi13EEvPKDF16_PKiS3_PK15HIP_vector_typeIjLj4EES7_PKfS9_S9_S9_S9_S9_PDF16_Pf.kd
    .uniform_work_group_size: 1
    .uses_dynamic_stack: false
    .vgpr_count:     125
    .vgpr_spill_count: 0
    .wavefront_size: 64
